# MFMA order variant S3: srcA operand quad held across the four accumulators of a column, on top of the guarded P6-hosted conversion
# baseline (speedup 1.0000x reference)
; #define PG8_STAGE(bufoff, gbase, voff) do { const char* _gb = (const char*)(gbase); asm volatile("" : "+s"(_gb)); _Pragma("unroll") for (int _i = 0; _i < 2; ++_i) \
;         __builtin_amdgcn_global_load_lds((const unsigned*)(_gb + (voff)[_i]), (PG8_LAS unsigned*)(lds + (bufoff) + ldsw + _i * 8192), 16, 0, 0); } while (0)
; #define PG8_LDA(dst, b, h) do { _Pragma("unroll") for (int m = 0; m < 4; ++m) _Pragma("unroll") for (int k = 0; k < 2; ++k) dst[m][k] = *(const PG8_LAS bf16x8*)(lds + PG8_SA(b, h) + aoff + m * 2048 + k * 1024); } while (0)
; #define PG8_MMA(ai, bj, At, Bt) do { __builtin_amdgcn_s_setprio(1); _Pragma("unroll") for (int m = 0; m < 4; ++m) _Pragma("unroll") for (int n = 0; n < 2; ++n) _Pragma("unroll") for (int k = 0; k < 2; ++k) \
;         acc[ai][bj][m][n] = __builtin_amdgcn_mfma_f32_16x16x32_bf16(Bt[n][k], At[m][k], acc[ai][bj][m][n], 0, 0, 0); __builtin_amdgcn_s_setprio(0); } while (0)
; #define PG8_WAIT_L(n) asm volatile("s_waitcnt lgkmcnt(" #n ")" ::: "memory")
; #define PG8_BAR __builtin_amdgcn_s_barrier()
; #define PG8_SCHED __builtin_amdgcn_sched_barrier(0)
; template <class Epi, class Sched, bool ALIGN_EPI = false, bool SP2 = false, bool HALFM = false>
; __device__ __forceinline__ void gemm_phase(PG8_LAS unsigned char* lds, const Gemm g, const Sched& S, const Epi& E) {
;     ...
;             PG8_WAIT_V8R; PG8_WAIT_L(0); PG8_BAR; PG8_MMA(0, 0, At, B0); PG8_MMA(0, 1, At, B1); PG8_BAR; PG8_SCHED;
;             if constexpr (!HALFM) { PG8_LDA(At, 0, 1); } PG8_STAGE(PG8_SB(0, 0), b2, voffB); PG8_STAGE(PG8_SB(0, 1), b2 + hstep, voffB); PG8_STAGE(PG8_SA(0, 0), a2, voffA);
.Lry0:
	s_waitcnt lgkmcnt(0)
	s_barrier
	s_setprio 1
	s_waitcnt lgkmcnt(0)
	v_mfma_f32_16x16x32_bf16 v[126:129], v[130:133], v[162:165], v[126:129]
	v_mfma_f32_16x16x32_bf16 v[126:129], v[134:137], v[166:169], v[126:129]
	v_mfma_f32_16x16x32_bf16 v[110:113], v[134:137], v[174:177], v[110:113]
	v_mfma_f32_16x16x32_bf16 v[110:113], v[130:133], v[170:173], v[110:113]
	v_mfma_f32_16x16x32_bf16 v[94:97], v[130:133], v[194:197], v[94:97]
	v_mfma_f32_16x16x32_bf16 v[94:97], v[134:137], v[198:201], v[94:97]
	v_mfma_f32_16x16x32_bf16 v[78:81], v[134:137], v[206:209], v[78:81]
	v_mfma_f32_16x16x32_bf16 v[78:81], v[130:133], v[202:205], v[78:81]
	v_mfma_f32_16x16x32_bf16 v[74:77], v[138:141], v[202:205], v[74:77]
	v_mfma_f32_16x16x32_bf16 v[74:77], v[142:145], v[206:209], v[74:77]
	v_mfma_f32_16x16x32_bf16 v[90:93], v[142:145], v[198:201], v[90:93]
	v_mfma_f32_16x16x32_bf16 v[90:93], v[138:141], v[194:197], v[90:93]
	v_mfma_f32_16x16x32_bf16 v[106:109], v[138:141], v[170:173], v[106:109]
	v_mfma_f32_16x16x32_bf16 v[106:109], v[142:145], v[174:177], v[106:109]
	v_mfma_f32_16x16x32_bf16 v[122:125], v[142:145], v[166:169], v[122:125]
	v_mfma_f32_16x16x32_bf16 v[122:125], v[138:141], v[162:165], v[122:125]
	s_setprio 0
	s_setprio 1
	v_mfma_f32_16x16x32_bf16 v[114:117], v[154:157], v[162:165], v[114:117]
	v_mfma_f32_16x16x32_bf16 v[114:117], v[158:161], v[166:169], v[114:117]
	v_mfma_f32_16x16x32_bf16 v[98:101], v[158:161], v[174:177], v[98:101]
	v_mfma_f32_16x16x32_bf16 v[98:101], v[154:157], v[170:173], v[98:101]
	v_mfma_f32_16x16x32_bf16 v[82:85], v[154:157], v[194:197], v[82:85]
	v_mfma_f32_16x16x32_bf16 v[82:85], v[158:161], v[198:201], v[82:85]
	v_mfma_f32_16x16x32_bf16 v[66:69], v[158:161], v[206:209], v[66:69]
	v_mfma_f32_16x16x32_bf16 v[66:69], v[154:157], v[202:205], v[66:69]
	v_mfma_f32_16x16x32_bf16 v[70:73], v[146:149], v[202:205], v[70:73]
	v_mfma_f32_16x16x32_bf16 v[70:73], v[150:153], v[206:209], v[70:73]
	v_mfma_f32_16x16x32_bf16 v[86:89], v[150:153], v[198:201], v[86:89]
	v_mfma_f32_16x16x32_bf16 v[86:89], v[146:149], v[194:197], v[86:89]
	v_mfma_f32_16x16x32_bf16 v[102:105], v[146:149], v[170:173], v[102:105]
	v_mfma_f32_16x16x32_bf16 v[102:105], v[150:153], v[174:177], v[102:105]
	v_mfma_f32_16x16x32_bf16 v[118:121], v[150:153], v[166:169], v[118:121]
	v_mfma_f32_16x16x32_bf16 v[118:121], v[146:149], v[162:165], v[118:121]
	s_setprio 0
	s_barrier
	s_add_i32 s89, s46, s41
	s_mov_b64 s[86:87], s[38:39]
	s_mov_b32 m0, s89
	ds_read_b128 v[162:165], v218 offset:16384
	ds_read_b128 v[166:169], v218 offset:17408
	ds_read_b128 v[170:173], v218 offset:18432
	ds_read_b128 v[174:177], v218 offset:19456
	ds_read_b128 v[194:197], v218 offset:20480
	ds_read_b128 v[198:201], v218 offset:21504
	ds_read_b128 v[202:205], v218 offset:22528
	ds_read_b128 v[206:209], v218 offset:23552
	s_nop 0
	global_load_lds_dwordx4 v221, s[86:87]
	s_add_i32 m0, s89, 0x2000
	s_nop 0
	global_load_lds_dwordx4 v181, s[86:87]
	s_add_u32 s86, s38, 0x4000
	s_addc_u32 s87, s39, 0
	s_add_i32 s89, s47, s41
	s_mov_b32 m0, s89
	s_nop 0
	global_load_lds_dwordx4 v221, s[86:87]
	s_add_i32 m0, s89, 0x2000
	s_nop 0
	global_load_lds_dwordx4 v181, s[86:87]
	s_mov_b64 s[86:87], s[0:1]
	s_mov_b32 m0, s37
	s_nop 0
	global_load_lds_dwordx4 v221, s[86:87]
	s_mov_b32 m0, s52
	s_nop 0
	global_load_lds_dwordx4 v181, s[86:87]
	s_cmp_eq_u32 s88, 0
	s_cbranch_scc1 .Lrx1
	s_waitcnt vmcnt(32)
	s_branch .Lry1

; #define PG8_STAGE(bufoff, gbase, voff) do { const char* _gb = (const char*)(gbase); asm volatile("" : "+s"(_gb)); _Pragma("unroll") for (int _i = 0; _i < 2; ++_i) \
;         __builtin_amdgcn_global_load_lds((const unsigned*)(_gb + (voff)[_i]), (PG8_LAS unsigned*)(lds + (bufoff) + ldsw + _i * 8192), 16, 0, 0); } while (0)
; #define PG8_LDA(dst, b, h) do { _Pragma("unroll") for (int m = 0; m < 4; ++m) _Pragma("unroll") for (int k = 0; k < 2; ++k) dst[m][k] = *(const PG8_LAS bf16x8*)(lds + PG8_SA(b, h) + aoff + m * 2048 + k * 1024); } while (0)
; #define PG8_LDB(dst, b, h) do { _Pragma("unroll") for (int n = 0; n < 2; ++n) _Pragma("unroll") for (int k = 0; k < 2; ++k) dst[n][k] = *(const PG8_LAS bf16x8*)(lds + PG8_SB(b, h) + boff + n * 2048 + k * 1024); } while (0)
; #define PG8_MMA(ai, bj, At, Bt) do { __builtin_amdgcn_s_setprio(1); _Pragma("unroll") for (int m = 0; m < 4; ++m) _Pragma("unroll") for (int n = 0; n < 2; ++n) _Pragma("unroll") for (int k = 0; k < 2; ++k) \
;         acc[ai][bj][m][n] = __builtin_amdgcn_mfma_f32_16x16x32_bf16(Bt[n][k], At[m][k], acc[ai][bj][m][n], 0, 0, 0); __builtin_amdgcn_s_setprio(0); } while (0)
; #define PG8_WAIT_L(n) asm volatile("s_waitcnt lgkmcnt(" #n ")" ::: "memory")
; #define PG8_BAR __builtin_amdgcn_s_barrier()
; #define PG8_SCHED __builtin_amdgcn_sched_barrier(0)
; template <class Epi, class Sched, bool ALIGN_EPI = false, bool SP2 = false, bool HALFM = false>
; __device__ __forceinline__ void gemm_phase(PG8_LAS unsigned char* lds, const Gemm g, const Sched& S, const Epi& E) {
;     ...
;             PG8_WAIT_V8R; PG8_WAIT_L(0); PG8_BAR; if constexpr (!HALFM) { PG8_MMA(1, 0, At, B0); PG8_MMA(1, 1, At, B1); } PG8_BAR; PG8_SCHED;
;             PG8_LDB(B0, 1, 0); PG8_LDB(B1, 1, 1); PG8_SCHED; PG8_LDA(At, 1, 0); PG8_STAGE(PG8_SA(0, 1), a2 + hstepA, voffA);
.Lry1:
	s_waitcnt lgkmcnt(0)
	s_barrier
	s_setprio 1
	s_waitcnt lgkmcnt(0)
	v_mfma_f32_16x16x32_bf16 v[62:65], v[130:133], v[162:165], v[62:65]
	v_mfma_f32_16x16x32_bf16 v[62:65], v[134:137], v[166:169], v[62:65]
	v_mfma_f32_16x16x32_bf16 v[46:49], v[134:137], v[174:177], v[46:49]
	v_mfma_f32_16x16x32_bf16 v[46:49], v[130:133], v[170:173], v[46:49]
	v_mfma_f32_16x16x32_bf16 v[30:33], v[130:133], v[194:197], v[30:33]
	v_mfma_f32_16x16x32_bf16 v[30:33], v[134:137], v[198:201], v[30:33]
	v_mfma_f32_16x16x32_bf16 v[14:17], v[134:137], v[206:209], v[14:17]
	v_mfma_f32_16x16x32_bf16 v[14:17], v[130:133], v[202:205], v[14:17]
	v_mfma_f32_16x16x32_bf16 v[10:13], v[138:141], v[202:205], v[10:13]
	v_mfma_f32_16x16x32_bf16 v[10:13], v[142:145], v[206:209], v[10:13]
	v_mfma_f32_16x16x32_bf16 v[26:29], v[142:145], v[198:201], v[26:29]
	v_mfma_f32_16x16x32_bf16 v[26:29], v[138:141], v[194:197], v[26:29]
	v_mfma_f32_16x16x32_bf16 v[42:45], v[138:141], v[170:173], v[42:45]
	v_mfma_f32_16x16x32_bf16 v[42:45], v[142:145], v[174:177], v[42:45]
	v_mfma_f32_16x16x32_bf16 v[58:61], v[142:145], v[166:169], v[58:61]
	v_mfma_f32_16x16x32_bf16 v[58:61], v[138:141], v[162:165], v[58:61]
	s_setprio 0
	s_setprio 1
	v_mfma_f32_16x16x32_bf16 v[50:53], v[154:157], v[162:165], v[50:53]
	v_mfma_f32_16x16x32_bf16 v[50:53], v[158:161], v[166:169], v[50:53]
	v_mfma_f32_16x16x32_bf16 v[34:37], v[158:161], v[174:177], v[34:37]
	v_mfma_f32_16x16x32_bf16 v[34:37], v[154:157], v[170:173], v[34:37]
	v_mfma_f32_16x16x32_bf16 v[18:21], v[154:157], v[194:197], v[18:21]
	v_mfma_f32_16x16x32_bf16 v[18:21], v[158:161], v[198:201], v[18:21]
	v_mfma_f32_16x16x32_bf16 v[2:5], v[158:161], v[206:209], v[2:5]
	v_mfma_f32_16x16x32_bf16 v[2:5], v[154:157], v[202:205], v[2:5]
	v_mfma_f32_16x16x32_bf16 v[6:9], v[146:149], v[202:205], v[6:9]
	v_mfma_f32_16x16x32_bf16 v[6:9], v[150:153], v[206:209], v[6:9]
	v_mfma_f32_16x16x32_bf16 v[22:25], v[150:153], v[198:201], v[22:25]
	v_mfma_f32_16x16x32_bf16 v[22:25], v[146:149], v[194:197], v[22:25]
	v_mfma_f32_16x16x32_bf16 v[38:41], v[146:149], v[170:173], v[38:41]
	v_mfma_f32_16x16x32_bf16 v[38:41], v[150:153], v[174:177], v[38:41]
	v_mfma_f32_16x16x32_bf16 v[54:57], v[150:153], v[166:169], v[54:57]
	v_mfma_f32_16x16x32_bf16 v[54:57], v[146:149], v[162:165], v[54:57]
	s_setprio 0
	s_barrier
	s_add_i32 s89, 0, 0x18000
	s_add_i32 s90, 0, 0x1c000
	v_add_u32_e32 v142, s89, v214
	v_add_u32_e32 v158, s90, v214
	ds_read_b128 v[130:133], v142
	ds_read_b128 v[134:137], v142 offset:1024
	ds_read_b128 v[138:141], v142 offset:2048
	ds_read_b128 v[142:145], v142 offset:3072
	ds_read_b128 v[146:149], v158
	ds_read_b128 v[150:153], v158 offset:1024
	ds_read_b128 v[154:157], v158 offset:2048
	ds_read_b128 v[158:161], v158 offset:3072
	s_add_u32 s86, s0, 0x4000
	s_addc_u32 s87, s1, 0
	s_mov_b32 m0, s53
	ds_read_b128 v[162:165], v218 offset:32768
	ds_read_b128 v[166:169], v218 offset:33792
	ds_read_b128 v[170:173], v218 offset:34816
	ds_read_b128 v[174:177], v218 offset:35840
	ds_read_b128 v[194:197], v218 offset:36864
	ds_read_b128 v[198:201], v218 offset:37888
	ds_read_b128 v[202:205], v218 offset:38912
	ds_read_b128 v[206:209], v218 offset:39936
	s_nop 0
	global_load_lds_dwordx4 v221, s[86:87]
	s_mov_b32 m0, s54
	s_nop 0
	global_load_lds_dwordx4 v181, s[86:87]
	s_cmp_eq_u32 s88, 0
	s_cbranch_scc1 .Lrx2
	s_waitcnt vmcnt(32)
	s_branch .Lry2

; #define PG8_STAGE(bufoff, gbase, voff) do { const char* _gb = (const char*)(gbase); asm volatile("" : "+s"(_gb)); _Pragma("unroll") for (int _i = 0; _i < 2; ++_i) \
;         __builtin_amdgcn_global_load_lds((const unsigned*)(_gb + (voff)[_i]), (PG8_LAS unsigned*)(lds + (bufoff) + ldsw + _i * 8192), 16, 0, 0); } while (0)
; #define PG8_LDA(dst, b, h) do { _Pragma("unroll") for (int m = 0; m < 4; ++m) _Pragma("unroll") for (int k = 0; k < 2; ++k) dst[m][k] = *(const PG8_LAS bf16x8*)(lds + PG8_SA(b, h) + aoff + m * 2048 + k * 1024); } while (0)
; #define PG8_MMA(ai, bj, At, Bt) do { __builtin_amdgcn_s_setprio(1); _Pragma("unroll") for (int m = 0; m < 4; ++m) _Pragma("unroll") for (int n = 0; n < 2; ++n) _Pragma("unroll") for (int k = 0; k < 2; ++k) \
;         acc[ai][bj][m][n] = __builtin_amdgcn_mfma_f32_16x16x32_bf16(Bt[n][k], At[m][k], acc[ai][bj][m][n], 0, 0, 0); __builtin_amdgcn_s_setprio(0); } while (0)
; #define PG8_WAIT_V(n) asm volatile("s_waitcnt vmcnt(" #n ")" ::: "memory")
; #define PG8_WAIT_L(n) asm volatile("s_waitcnt lgkmcnt(" #n ")" ::: "memory")
; #define PG8_BAR __builtin_amdgcn_s_barrier()
; #define PG8_SCHED __builtin_amdgcn_sched_barrier(0)
; template <class Epi, class Sched, bool ALIGN_EPI = false, bool SP2 = false, bool HALFM = false>
; __device__ __forceinline__ void gemm_phase(PG8_LAS unsigned char* lds, const Gemm g, const Sched& S, const Epi& E) {
;     ...
;             PG8_WAIT_V8R; PG8_WAIT_L(0); PG8_BAR; PG8_MMA(0, 0, At, B0); PG8_MMA(0, 1, At, B1); PG8_BAR; PG8_SCHED;
;             if constexpr (!HALFM) { PG8_LDA(At, 1, 1); } PG8_STAGE(PG8_SB(1, 0), b3, voffB); PG8_STAGE(PG8_SB(1, 1), b3 + hstep, voffB); PG8_STAGE(PG8_SA(1, 0), a3, voffA);
;             PG8_WAIT_V(8); PG8_WAIT_L(0); PG8_BAR; if constexpr (!HALFM) { PG8_MMA(1, 0, At, B0); PG8_MMA(1, 1, At, B1); } PG8_BAR; PG8_SCHED;
;             PG8_STAGE(PG8_SA(1, 1), a3 + hstepA, voffA);
.Lry2:
	s_waitcnt lgkmcnt(0)
	s_barrier
	s_setprio 1
	s_waitcnt lgkmcnt(0)
	v_mfma_f32_16x16x32_bf16 v[126:129], v[130:133], v[162:165], v[126:129]
	v_mfma_f32_16x16x32_bf16 v[126:129], v[134:137], v[166:169], v[126:129]
	v_mfma_f32_16x16x32_bf16 v[110:113], v[134:137], v[174:177], v[110:113]
	v_mfma_f32_16x16x32_bf16 v[110:113], v[130:133], v[170:173], v[110:113]
	v_mfma_f32_16x16x32_bf16 v[94:97], v[130:133], v[194:197], v[94:97]
	v_mfma_f32_16x16x32_bf16 v[94:97], v[134:137], v[198:201], v[94:97]
	v_mfma_f32_16x16x32_bf16 v[78:81], v[134:137], v[206:209], v[78:81]
	v_mfma_f32_16x16x32_bf16 v[78:81], v[130:133], v[202:205], v[78:81]
	v_mfma_f32_16x16x32_bf16 v[74:77], v[138:141], v[202:205], v[74:77]
	v_mfma_f32_16x16x32_bf16 v[74:77], v[142:145], v[206:209], v[74:77]
	v_mfma_f32_16x16x32_bf16 v[90:93], v[142:145], v[198:201], v[90:93]
	v_mfma_f32_16x16x32_bf16 v[90:93], v[138:141], v[194:197], v[90:93]
	v_mfma_f32_16x16x32_bf16 v[106:109], v[138:141], v[170:173], v[106:109]
	v_mfma_f32_16x16x32_bf16 v[106:109], v[142:145], v[174:177], v[106:109]
	v_mfma_f32_16x16x32_bf16 v[122:125], v[142:145], v[166:169], v[122:125]
	v_mfma_f32_16x16x32_bf16 v[122:125], v[138:141], v[162:165], v[122:125]
	s_setprio 0
	s_setprio 1
	v_mfma_f32_16x16x32_bf16 v[114:117], v[154:157], v[162:165], v[114:117]
	v_mfma_f32_16x16x32_bf16 v[114:117], v[158:161], v[166:169], v[114:117]
	v_mfma_f32_16x16x32_bf16 v[98:101], v[158:161], v[174:177], v[98:101]
	v_mfma_f32_16x16x32_bf16 v[98:101], v[154:157], v[170:173], v[98:101]
	v_mfma_f32_16x16x32_bf16 v[82:85], v[154:157], v[194:197], v[82:85]
	v_mfma_f32_16x16x32_bf16 v[82:85], v[158:161], v[198:201], v[82:85]
	v_mfma_f32_16x16x32_bf16 v[66:69], v[158:161], v[206:209], v[66:69]
	v_mfma_f32_16x16x32_bf16 v[66:69], v[154:157], v[202:205], v[66:69]
	v_mfma_f32_16x16x32_bf16 v[70:73], v[146:149], v[202:205], v[70:73]
	v_mfma_f32_16x16x32_bf16 v[70:73], v[150:153], v[206:209], v[70:73]
	v_mfma_f32_16x16x32_bf16 v[86:89], v[150:153], v[198:201], v[86:89]
	v_mfma_f32_16x16x32_bf16 v[86:89], v[146:149], v[194:197], v[86:89]
	v_mfma_f32_16x16x32_bf16 v[102:105], v[146:149], v[170:173], v[102:105]
	v_mfma_f32_16x16x32_bf16 v[102:105], v[150:153], v[174:177], v[102:105]
	v_mfma_f32_16x16x32_bf16 v[118:121], v[150:153], v[166:169], v[118:121]
	v_mfma_f32_16x16x32_bf16 v[118:121], v[146:149], v[162:165], v[118:121]
	s_setprio 0
	s_barrier
	s_add_u32 s86, s38, 0x8000
	s_addc_u32 s87, s39, 0
	s_add_i32 s88, s89, s41
	s_mov_b32 m0, s88
	ds_read_b128 v[162:165], v218 offset:49152
	ds_read_b128 v[166:169], v218 offset:50176
	ds_read_b128 v[170:173], v218 offset:51200
	ds_read_b128 v[174:177], v218 offset:52224
	ds_read_b128 v[194:197], v218 offset:53248
	ds_read_b128 v[198:201], v218 offset:54272
	ds_read_b128 v[202:205], v218 offset:55296
	ds_read_b128 v[206:209], v218 offset:56320
	s_nop 0
	global_load_lds_dwordx4 v221, s[86:87]
	s_add_i32 m0, s88, 0x2000
	s_add_u32 s38, s38, 0xc000
	global_load_lds_dwordx4 v181, s[86:87]
	s_addc_u32 s39, s39, 0
	s_add_i32 s86, s90, s41
	s_mov_b32 m0, s86
	s_nop 0
	global_load_lds_dwordx4 v221, s[38:39]
	s_add_i32 m0, s86, 0x2000
	s_nop 0
	global_load_lds_dwordx4 v181, s[38:39]
	s_mov_b32 m0, s56
	s_nop 0
	global_load_lds_dwordx4 v221, s[10:11]
	s_mov_b32 m0, s57
	s_nop 0
	global_load_lds_dwordx4 v181, s[10:11]
	s_waitcnt vmcnt(8)
	s_waitcnt lgkmcnt(0)
	s_barrier
	s_setprio 1
	s_waitcnt lgkmcnt(0)
	v_mfma_f32_16x16x32_bf16 v[62:65], v[130:133], v[162:165], v[62:65]
	v_mfma_f32_16x16x32_bf16 v[62:65], v[134:137], v[166:169], v[62:65]
	v_mfma_f32_16x16x32_bf16 v[46:49], v[134:137], v[174:177], v[46:49]
	v_mfma_f32_16x16x32_bf16 v[46:49], v[130:133], v[170:173], v[46:49]
	v_mfma_f32_16x16x32_bf16 v[30:33], v[130:133], v[194:197], v[30:33]
	v_mfma_f32_16x16x32_bf16 v[30:33], v[134:137], v[198:201], v[30:33]
	v_mfma_f32_16x16x32_bf16 v[14:17], v[134:137], v[206:209], v[14:17]
	v_mfma_f32_16x16x32_bf16 v[14:17], v[130:133], v[202:205], v[14:17]
	v_mfma_f32_16x16x32_bf16 v[10:13], v[138:141], v[202:205], v[10:13]
	v_mfma_f32_16x16x32_bf16 v[10:13], v[142:145], v[206:209], v[10:13]
	v_mfma_f32_16x16x32_bf16 v[26:29], v[142:145], v[198:201], v[26:29]
	v_mfma_f32_16x16x32_bf16 v[26:29], v[138:141], v[194:197], v[26:29]
	v_mfma_f32_16x16x32_bf16 v[42:45], v[138:141], v[170:173], v[42:45]
	v_mfma_f32_16x16x32_bf16 v[42:45], v[142:145], v[174:177], v[42:45]
	v_mfma_f32_16x16x32_bf16 v[58:61], v[142:145], v[166:169], v[58:61]
	v_mfma_f32_16x16x32_bf16 v[58:61], v[138:141], v[162:165], v[58:61]
	s_setprio 0
	s_setprio 1
	v_mfma_f32_16x16x32_bf16 v[50:53], v[154:157], v[162:165], v[50:53]
	v_mfma_f32_16x16x32_bf16 v[50:53], v[158:161], v[166:169], v[50:53]
	v_mfma_f32_16x16x32_bf16 v[34:37], v[158:161], v[174:177], v[34:37]
	v_mfma_f32_16x16x32_bf16 v[34:37], v[154:157], v[170:173], v[34:37]
	v_mfma_f32_16x16x32_bf16 v[18:21], v[154:157], v[194:197], v[18:21]
	v_mfma_f32_16x16x32_bf16 v[18:21], v[158:161], v[198:201], v[18:21]
	v_mfma_f32_16x16x32_bf16 v[2:5], v[158:161], v[206:209], v[2:5]
	v_mfma_f32_16x16x32_bf16 v[2:5], v[154:157], v[202:205], v[2:5]
	v_mfma_f32_16x16x32_bf16 v[6:9], v[146:149], v[202:205], v[6:9]
	v_mfma_f32_16x16x32_bf16 v[6:9], v[150:153], v[206:209], v[6:9]
	v_mfma_f32_16x16x32_bf16 v[22:25], v[150:153], v[198:201], v[22:25]
	v_mfma_f32_16x16x32_bf16 v[22:25], v[146:149], v[194:197], v[22:25]
	v_mfma_f32_16x16x32_bf16 v[38:41], v[146:149], v[170:173], v[38:41]
	v_mfma_f32_16x16x32_bf16 v[38:41], v[150:153], v[174:177], v[38:41]
	v_mfma_f32_16x16x32_bf16 v[54:57], v[150:153], v[166:169], v[54:57]
	v_mfma_f32_16x16x32_bf16 v[54:57], v[146:149], v[162:165], v[54:57]
	s_setprio 0
	s_barrier
	s_add_u32 s0, s0, 0xc000
	s_mov_b32 m0, s58
	s_addc_u32 s1, s1, 0
	s_add_i32 s81, s81, 2
	global_load_lds_dwordx4 v221, s[0:1]
	s_mov_b32 m0, s59
	s_add_u32 s33, s33, 0x10000
	global_load_lds_dwordx4 v181, s[0:1]
	s_addc_u32 s65, s65, 0
	s_add_u32 s66, s66, 0x10000
	s_addc_u32 s67, s67, 0
	s_cmp_gt_u32 s81, 61
	s_cbranch_scc0 .LBB0_248
	s_and_b64 vcc, exec, s[20:21]
	s_cbranch_vccz .LBB0_253
	s_barrier
	s_mov_b64 s[0:1], -1
	s_cmp_gt_u32 s36, 7
	v_lshl_add_u32 v194, s8, 8, v183
	s_cbranch_scc1 .LBB0_254

; __global__ void __launch_bounds__(NWAVES * 64, 2) mk_fwd(Args args) {
;     ...
;         const int NCONV = (CONV_OVERLAP && G >= 128) ? 51 : 0;
;         if (bx < NCONV) convert_weights<false, true>(P, lds, bx * NWAVES + wave, NCONV * NWAVES, wave, lane, 0, (CONV_OVERLAP && G >= 192) ? LATE_SPLIT : 0x7fffffff);
;         else {
;             sb_phase(lds, PROJ, (bf16*)(ws + WS_MIX), (const float*)(ws + WS_RSB), P.sbo_norm, bx - NCONV, G - NCONV, tid);
;             ret_out_phase(lds, PROJ, (bf16*)(ws + WS_MIX), (const bf16*)(ws + WS_ST), P.ret_norm, bx - NCONV, G - NCONV, tid);
;         }
;         if (NCONV == 0) convert_weights<false>(P, lds, gw, NGW, wave, lane);
.LBB0_519:
	s_mov_b32 s98, 0
	s_mov_b32 s99, 0
	s_mov_b32 s100, s80
	s_mov_b32 s101, s56
	s_mov_b32 s0, 0x9900
	s_cmp_eq_u32 s80, 0x100
	s_cselect_b32 s1, 1, 0
	s_cmp_gt_i32 s75, 6
	s_cselect_b32 s1, s1, 0
	s_cmp_lg_u32 s1, 0
	s_cselect_b32 s0, 0x6e00, s0
	v_writelane_b32 v255, s0, 2
	s_mov_b32 s0, 0
	v_writelane_b32 v255, s0, 3

; #define PG8_STAGE(bufoff, gbase, voff) do { const char* _gb = (const char*)(gbase); asm volatile("" : "+s"(_gb)); _Pragma("unroll") for (int _i = 0; _i < 2; ++_i) \
;         __builtin_amdgcn_global_load_lds((const unsigned*)(_gb + (voff)[_i]), (PG8_LAS unsigned*)(lds + (bufoff) + ldsw + _i * 8192), 16, 0, 0); } while (0)
; #define PG8_LDA(dst, b, h) do { _Pragma("unroll") for (int m = 0; m < 4; ++m) _Pragma("unroll") for (int k = 0; k < 2; ++k) dst[m][k] = *(const PG8_LAS bf16x8*)(lds + PG8_SA(b, h) + aoff + m * 2048 + k * 1024); } while (0)
; #define PG8_MMA(ai, bj, At, Bt) do { __builtin_amdgcn_s_setprio(1); _Pragma("unroll") for (int m = 0; m < 4; ++m) _Pragma("unroll") for (int n = 0; n < 2; ++n) _Pragma("unroll") for (int k = 0; k < 2; ++k) \
;         acc[ai][bj][m][n] = __builtin_amdgcn_mfma_f32_16x16x32_bf16(Bt[n][k], At[m][k], acc[ai][bj][m][n], 0, 0, 0); __builtin_amdgcn_s_setprio(0); } while (0)
; #define PG8_WAIT_L(n) asm volatile("s_waitcnt lgkmcnt(" #n ")" ::: "memory")
; #define PG8_BAR __builtin_amdgcn_s_barrier()
; #define PG8_SCHED __builtin_amdgcn_sched_barrier(0)
; template <class Epi, class Sched, bool ALIGN_EPI = false, bool SP2 = false, bool HALFM = false>
; __device__ __forceinline__ void gemm_phase(PG8_LAS unsigned char* lds, const Gemm g, const Sched& S, const Epi& E) {
;     ...
;             PG8_WAIT_V8R; PG8_WAIT_L(0); PG8_BAR; PG8_MMA(0, 0, At, B0); PG8_MMA(0, 1, At, B1); PG8_BAR; PG8_SCHED;
;             if constexpr (!HALFM) { PG8_LDA(At, 0, 1); } PG8_STAGE(PG8_SB(0, 0), b2, voffB); PG8_STAGE(PG8_SB(0, 1), b2 + hstep, voffB); PG8_STAGE(PG8_SA(0, 0), a2, voffA);
.Lry3:
	s_waitcnt lgkmcnt(0)
	s_barrier
	s_setprio 1
	s_waitcnt lgkmcnt(0)
	v_mfma_f32_16x16x32_bf16 v[126:129], v[130:133], v[162:165], v[126:129]
	v_mfma_f32_16x16x32_bf16 v[126:129], v[134:137], v[166:169], v[126:129]
	v_mfma_f32_16x16x32_bf16 v[110:113], v[134:137], v[178:181], v[110:113]
	v_mfma_f32_16x16x32_bf16 v[110:113], v[130:133], v[174:177], v[110:113]
	v_mfma_f32_16x16x32_bf16 v[94:97], v[130:133], v[182:185], v[94:97]
	v_mfma_f32_16x16x32_bf16 v[94:97], v[134:137], v[186:189], v[94:97]
	v_mfma_f32_16x16x32_bf16 v[78:81], v[134:137], v[194:197], v[78:81]
	v_mfma_f32_16x16x32_bf16 v[78:81], v[130:133], v[190:193], v[78:81]
	v_mfma_f32_16x16x32_bf16 v[74:77], v[138:141], v[190:193], v[74:77]
	v_mfma_f32_16x16x32_bf16 v[74:77], v[142:145], v[194:197], v[74:77]
	v_mfma_f32_16x16x32_bf16 v[90:93], v[142:145], v[186:189], v[90:93]
	v_mfma_f32_16x16x32_bf16 v[90:93], v[138:141], v[182:185], v[90:93]
	v_mfma_f32_16x16x32_bf16 v[106:109], v[138:141], v[174:177], v[106:109]
	v_mfma_f32_16x16x32_bf16 v[106:109], v[142:145], v[178:181], v[106:109]
	v_mfma_f32_16x16x32_bf16 v[122:125], v[142:145], v[166:169], v[122:125]
	v_mfma_f32_16x16x32_bf16 v[122:125], v[138:141], v[162:165], v[122:125]
	s_setprio 0
	s_setprio 1
	v_mfma_f32_16x16x32_bf16 v[114:117], v[154:157], v[162:165], v[114:117]
	v_mfma_f32_16x16x32_bf16 v[114:117], v[158:161], v[166:169], v[114:117]
	v_mfma_f32_16x16x32_bf16 v[98:101], v[158:161], v[178:181], v[98:101]
	v_mfma_f32_16x16x32_bf16 v[98:101], v[154:157], v[174:177], v[98:101]
	v_mfma_f32_16x16x32_bf16 v[82:85], v[154:157], v[182:185], v[82:85]
	v_mfma_f32_16x16x32_bf16 v[82:85], v[158:161], v[186:189], v[82:85]
	v_mfma_f32_16x16x32_bf16 v[66:69], v[158:161], v[194:197], v[66:69]
	v_mfma_f32_16x16x32_bf16 v[66:69], v[154:157], v[190:193], v[66:69]
	v_mfma_f32_16x16x32_bf16 v[70:73], v[146:149], v[190:193], v[70:73]
	v_mfma_f32_16x16x32_bf16 v[70:73], v[150:153], v[194:197], v[70:73]
	v_mfma_f32_16x16x32_bf16 v[86:89], v[150:153], v[186:189], v[86:89]
	v_mfma_f32_16x16x32_bf16 v[86:89], v[146:149], v[182:185], v[86:89]
	v_mfma_f32_16x16x32_bf16 v[102:105], v[146:149], v[174:177], v[102:105]
	v_mfma_f32_16x16x32_bf16 v[102:105], v[150:153], v[178:181], v[102:105]
	v_mfma_f32_16x16x32_bf16 v[118:121], v[150:153], v[166:169], v[118:121]
	v_mfma_f32_16x16x32_bf16 v[118:121], v[146:149], v[162:165], v[118:121]
	s_setprio 0
	s_barrier
	s_add_i32 s65, s54, s3
	s_mov_b64 s[62:63], s[34:35]
	s_mov_b32 m0, s65
	ds_read_b128 v[162:165], v210 offset:16384
	ds_read_b128 v[166:169], v210 offset:17408
	ds_read_b128 v[174:177], v210 offset:18432
	ds_read_b128 v[178:181], v210 offset:19456
	ds_read_b128 v[182:185], v210 offset:20480
	ds_read_b128 v[186:189], v210 offset:21504
	ds_read_b128 v[190:193], v210 offset:22528
	ds_read_b128 v[194:197], v210 offset:23552
	s_nop 0
	global_load_lds_dwordx4 v170, s[62:63]
	s_add_i32 m0, s65, 0x2000
	s_nop 0
	global_load_lds_dwordx4 v171, s[62:63]
	s_add_u32 s62, s34, 0x4000
	s_addc_u32 s63, s35, 0
	s_add_i32 s65, s55, s3
	s_mov_b32 m0, s65
	s_nop 0
	global_load_lds_dwordx4 v170, s[62:63]
	s_add_i32 m0, s65, 0x2000
	s_nop 0
	global_load_lds_dwordx4 v171, s[62:63]
	s_mov_b64 s[62:63], s[28:29]
	s_mov_b32 m0, s25
	s_nop 0
	global_load_lds_dwordx4 v170, s[62:63]
	s_mov_b32 m0, s27
	s_nop 0
	global_load_lds_dwordx4 v171, s[62:63]
	s_cmp_eq_u32 s64, 0
	s_cbranch_scc1 .Lrx4
	s_waitcnt vmcnt(40)
	s_branch .Lry4

; #define PG8_STAGE(bufoff, gbase, voff) do { const char* _gb = (const char*)(gbase); asm volatile("" : "+s"(_gb)); _Pragma("unroll") for (int _i = 0; _i < 2; ++_i) \
;         __builtin_amdgcn_global_load_lds((const unsigned*)(_gb + (voff)[_i]), (PG8_LAS unsigned*)(lds + (bufoff) + ldsw + _i * 8192), 16, 0, 0); } while (0)
; #define PG8_LDA(dst, b, h) do { _Pragma("unroll") for (int m = 0; m < 4; ++m) _Pragma("unroll") for (int k = 0; k < 2; ++k) dst[m][k] = *(const PG8_LAS bf16x8*)(lds + PG8_SA(b, h) + aoff + m * 2048 + k * 1024); } while (0)
; #define PG8_LDB(dst, b, h) do { _Pragma("unroll") for (int n = 0; n < 2; ++n) _Pragma("unroll") for (int k = 0; k < 2; ++k) dst[n][k] = *(const PG8_LAS bf16x8*)(lds + PG8_SB(b, h) + boff + n * 2048 + k * 1024); } while (0)
; #define PG8_MMA(ai, bj, At, Bt) do { __builtin_amdgcn_s_setprio(1); _Pragma("unroll") for (int m = 0; m < 4; ++m) _Pragma("unroll") for (int n = 0; n < 2; ++n) _Pragma("unroll") for (int k = 0; k < 2; ++k) \
;         acc[ai][bj][m][n] = __builtin_amdgcn_mfma_f32_16x16x32_bf16(Bt[n][k], At[m][k], acc[ai][bj][m][n], 0, 0, 0); __builtin_amdgcn_s_setprio(0); } while (0)
; #define PG8_WAIT_L(n) asm volatile("s_waitcnt lgkmcnt(" #n ")" ::: "memory")
; #define PG8_BAR __builtin_amdgcn_s_barrier()
; #define PG8_SCHED __builtin_amdgcn_sched_barrier(0)
; template <class Epi, class Sched, bool ALIGN_EPI = false, bool SP2 = false, bool HALFM = false>
; __device__ __forceinline__ void gemm_phase(PG8_LAS unsigned char* lds, const Gemm g, const Sched& S, const Epi& E) {
;     ...
;             PG8_WAIT_V8R; PG8_WAIT_L(0); PG8_BAR; if constexpr (!HALFM) { PG8_MMA(1, 0, At, B0); PG8_MMA(1, 1, At, B1); } PG8_BAR; PG8_SCHED;
;             PG8_LDB(B0, 1, 0); PG8_LDB(B1, 1, 1); PG8_SCHED; PG8_LDA(At, 1, 0); PG8_STAGE(PG8_SA(0, 1), a2 + hstepA, voffA);
.Lry4:
	s_waitcnt lgkmcnt(0)
	s_barrier
	s_setprio 1
	s_waitcnt lgkmcnt(0)
	v_mfma_f32_16x16x32_bf16 v[62:65], v[130:133], v[162:165], v[62:65]
	v_mfma_f32_16x16x32_bf16 v[62:65], v[134:137], v[166:169], v[62:65]
	v_mfma_f32_16x16x32_bf16 v[46:49], v[134:137], v[178:181], v[46:49]
	v_mfma_f32_16x16x32_bf16 v[46:49], v[130:133], v[174:177], v[46:49]
	v_mfma_f32_16x16x32_bf16 v[30:33], v[130:133], v[182:185], v[30:33]
	v_mfma_f32_16x16x32_bf16 v[30:33], v[134:137], v[186:189], v[30:33]
	v_mfma_f32_16x16x32_bf16 v[14:17], v[134:137], v[194:197], v[14:17]
	v_mfma_f32_16x16x32_bf16 v[14:17], v[130:133], v[190:193], v[14:17]
	v_mfma_f32_16x16x32_bf16 v[10:13], v[138:141], v[190:193], v[10:13]
	v_mfma_f32_16x16x32_bf16 v[10:13], v[142:145], v[194:197], v[10:13]
	v_mfma_f32_16x16x32_bf16 v[26:29], v[142:145], v[186:189], v[26:29]
	v_mfma_f32_16x16x32_bf16 v[26:29], v[138:141], v[182:185], v[26:29]
	v_mfma_f32_16x16x32_bf16 v[42:45], v[138:141], v[174:177], v[42:45]
	v_mfma_f32_16x16x32_bf16 v[42:45], v[142:145], v[178:181], v[42:45]
	v_mfma_f32_16x16x32_bf16 v[58:61], v[142:145], v[166:169], v[58:61]
	v_mfma_f32_16x16x32_bf16 v[58:61], v[138:141], v[162:165], v[58:61]
	s_setprio 0
	s_setprio 1
	v_mfma_f32_16x16x32_bf16 v[50:53], v[154:157], v[162:165], v[50:53]
	v_mfma_f32_16x16x32_bf16 v[50:53], v[158:161], v[166:169], v[50:53]
	v_mfma_f32_16x16x32_bf16 v[34:37], v[158:161], v[178:181], v[34:37]
	v_mfma_f32_16x16x32_bf16 v[34:37], v[154:157], v[174:177], v[34:37]
	v_mfma_f32_16x16x32_bf16 v[18:21], v[154:157], v[182:185], v[18:21]
	v_mfma_f32_16x16x32_bf16 v[18:21], v[158:161], v[186:189], v[18:21]
	v_mfma_f32_16x16x32_bf16 v[2:5], v[158:161], v[194:197], v[2:5]
	v_mfma_f32_16x16x32_bf16 v[2:5], v[154:157], v[190:193], v[2:5]
	v_mfma_f32_16x16x32_bf16 v[6:9], v[146:149], v[190:193], v[6:9]
	v_mfma_f32_16x16x32_bf16 v[6:9], v[150:153], v[194:197], v[6:9]
	v_mfma_f32_16x16x32_bf16 v[22:25], v[150:153], v[186:189], v[22:25]
	v_mfma_f32_16x16x32_bf16 v[22:25], v[146:149], v[182:185], v[22:25]
	v_mfma_f32_16x16x32_bf16 v[38:41], v[146:149], v[174:177], v[38:41]
	v_mfma_f32_16x16x32_bf16 v[38:41], v[150:153], v[178:181], v[38:41]
	v_mfma_f32_16x16x32_bf16 v[54:57], v[150:153], v[166:169], v[54:57]
	v_mfma_f32_16x16x32_bf16 v[54:57], v[146:149], v[162:165], v[54:57]
	s_setprio 0
	s_barrier
	s_add_i32 s65, 0, 0x18000
	s_add_i32 s70, 0, 0x1c000
	v_add_u32_e32 v142, s65, v205
	v_add_u32_e32 v158, s70, v205
	ds_read_b128 v[130:133], v142
	ds_read_b128 v[134:137], v142 offset:1024
	ds_read_b128 v[138:141], v142 offset:2048
	ds_read_b128 v[142:145], v142 offset:3072
	ds_read_b128 v[146:149], v158
	ds_read_b128 v[150:153], v158 offset:1024
	ds_read_b128 v[154:157], v158 offset:2048
	ds_read_b128 v[158:161], v158 offset:3072
	s_add_u32 s62, s28, 0x4000
	s_addc_u32 s63, s29, 0
	s_mov_b32 m0, s39
	ds_read_b128 v[162:165], v210 offset:32768
	ds_read_b128 v[166:169], v210 offset:33792
	ds_read_b128 v[174:177], v210 offset:34816
	ds_read_b128 v[178:181], v210 offset:35840
	ds_read_b128 v[182:185], v210 offset:36864
	ds_read_b128 v[186:189], v210 offset:37888
	ds_read_b128 v[190:193], v210 offset:38912
	ds_read_b128 v[194:197], v210 offset:39936
	s_nop 0
	global_load_lds_dwordx4 v170, s[62:63]
	s_mov_b32 m0, s40
	s_nop 0
	global_load_lds_dwordx4 v171, s[62:63]
	s_cmp_eq_u32 s64, 0
	s_cbranch_scc1 .Lrx5
	s_waitcnt vmcnt(40)
	s_branch .Lry5

; #define PG8_STAGE(bufoff, gbase, voff) do { const char* _gb = (const char*)(gbase); asm volatile("" : "+s"(_gb)); _Pragma("unroll") for (int _i = 0; _i < 2; ++_i) \
;         __builtin_amdgcn_global_load_lds((const unsigned*)(_gb + (voff)[_i]), (PG8_LAS unsigned*)(lds + (bufoff) + ldsw + _i * 8192), 16, 0, 0); } while (0)
; #define PG8_LDA(dst, b, h) do { _Pragma("unroll") for (int m = 0; m < 4; ++m) _Pragma("unroll") for (int k = 0; k < 2; ++k) dst[m][k] = *(const PG8_LAS bf16x8*)(lds + PG8_SA(b, h) + aoff + m * 2048 + k * 1024); } while (0)
; #define PG8_MMA(ai, bj, At, Bt) do { __builtin_amdgcn_s_setprio(1); _Pragma("unroll") for (int m = 0; m < 4; ++m) _Pragma("unroll") for (int n = 0; n < 2; ++n) _Pragma("unroll") for (int k = 0; k < 2; ++k) \
;         acc[ai][bj][m][n] = __builtin_amdgcn_mfma_f32_16x16x32_bf16(Bt[n][k], At[m][k], acc[ai][bj][m][n], 0, 0, 0); __builtin_amdgcn_s_setprio(0); } while (0)
; #define PG8_WAIT_V(n) asm volatile("s_waitcnt vmcnt(" #n ")" ::: "memory")
; #define PG8_WAIT_L(n) asm volatile("s_waitcnt lgkmcnt(" #n ")" ::: "memory")
; #define PG8_BAR __builtin_amdgcn_s_barrier()
; #define PG8_SCHED __builtin_amdgcn_sched_barrier(0)
; template <class Epi, class Sched, bool ALIGN_EPI = false, bool SP2 = false, bool HALFM = false>
; __device__ __forceinline__ void gemm_phase(PG8_LAS unsigned char* lds, const Gemm g, const Sched& S, const Epi& E) {
;     ...
;             PG8_WAIT_V8R; PG8_WAIT_L(0); PG8_BAR; PG8_MMA(0, 0, At, B0); PG8_MMA(0, 1, At, B1); PG8_BAR; PG8_SCHED;
;             if constexpr (!HALFM) { PG8_LDA(At, 1, 1); } PG8_STAGE(PG8_SB(1, 0), b3, voffB); PG8_STAGE(PG8_SB(1, 1), b3 + hstep, voffB); PG8_STAGE(PG8_SA(1, 0), a3, voffA);
;             PG8_WAIT_V(8); PG8_WAIT_L(0); PG8_BAR; if constexpr (!HALFM) { PG8_MMA(1, 0, At, B0); PG8_MMA(1, 1, At, B1); } PG8_BAR; PG8_SCHED;
;             PG8_STAGE(PG8_SA(1, 1), a3 + hstepA, voffA);
.Lry5:
	s_waitcnt lgkmcnt(0)
	s_barrier
	s_setprio 1
	s_waitcnt lgkmcnt(0)
	v_mfma_f32_16x16x32_bf16 v[126:129], v[130:133], v[162:165], v[126:129]
	v_mfma_f32_16x16x32_bf16 v[126:129], v[134:137], v[166:169], v[126:129]
	v_mfma_f32_16x16x32_bf16 v[110:113], v[134:137], v[178:181], v[110:113]
	v_mfma_f32_16x16x32_bf16 v[110:113], v[130:133], v[174:177], v[110:113]
	v_mfma_f32_16x16x32_bf16 v[94:97], v[130:133], v[182:185], v[94:97]
	v_mfma_f32_16x16x32_bf16 v[94:97], v[134:137], v[186:189], v[94:97]
	v_mfma_f32_16x16x32_bf16 v[78:81], v[134:137], v[194:197], v[78:81]
	v_mfma_f32_16x16x32_bf16 v[78:81], v[130:133], v[190:193], v[78:81]
	v_mfma_f32_16x16x32_bf16 v[74:77], v[138:141], v[190:193], v[74:77]
	v_mfma_f32_16x16x32_bf16 v[74:77], v[142:145], v[194:197], v[74:77]
	v_mfma_f32_16x16x32_bf16 v[90:93], v[142:145], v[186:189], v[90:93]
	v_mfma_f32_16x16x32_bf16 v[90:93], v[138:141], v[182:185], v[90:93]
	v_mfma_f32_16x16x32_bf16 v[106:109], v[138:141], v[174:177], v[106:109]
	v_mfma_f32_16x16x32_bf16 v[106:109], v[142:145], v[178:181], v[106:109]
	v_mfma_f32_16x16x32_bf16 v[122:125], v[142:145], v[166:169], v[122:125]
	v_mfma_f32_16x16x32_bf16 v[122:125], v[138:141], v[162:165], v[122:125]
	s_setprio 0
	s_setprio 1
	v_mfma_f32_16x16x32_bf16 v[114:117], v[154:157], v[162:165], v[114:117]
	v_mfma_f32_16x16x32_bf16 v[114:117], v[158:161], v[166:169], v[114:117]
	v_mfma_f32_16x16x32_bf16 v[98:101], v[158:161], v[178:181], v[98:101]
	v_mfma_f32_16x16x32_bf16 v[98:101], v[154:157], v[174:177], v[98:101]
	v_mfma_f32_16x16x32_bf16 v[82:85], v[154:157], v[182:185], v[82:85]
	v_mfma_f32_16x16x32_bf16 v[82:85], v[158:161], v[186:189], v[82:85]
	v_mfma_f32_16x16x32_bf16 v[66:69], v[158:161], v[194:197], v[66:69]
	v_mfma_f32_16x16x32_bf16 v[66:69], v[154:157], v[190:193], v[66:69]
	v_mfma_f32_16x16x32_bf16 v[70:73], v[146:149], v[190:193], v[70:73]
	v_mfma_f32_16x16x32_bf16 v[70:73], v[150:153], v[194:197], v[70:73]
	v_mfma_f32_16x16x32_bf16 v[86:89], v[150:153], v[186:189], v[86:89]
	v_mfma_f32_16x16x32_bf16 v[86:89], v[146:149], v[182:185], v[86:89]
	v_mfma_f32_16x16x32_bf16 v[102:105], v[146:149], v[174:177], v[102:105]
	v_mfma_f32_16x16x32_bf16 v[102:105], v[150:153], v[178:181], v[102:105]
	v_mfma_f32_16x16x32_bf16 v[118:121], v[150:153], v[166:169], v[118:121]
	v_mfma_f32_16x16x32_bf16 v[118:121], v[146:149], v[162:165], v[118:121]
	s_setprio 0
	s_barrier
	s_add_u32 s62, s34, 0x8000
	s_addc_u32 s63, s35, 0
	s_add_i32 s64, s65, s3
	s_mov_b32 m0, s64
	ds_read_b128 v[162:165], v210 offset:49152
	ds_read_b128 v[166:169], v210 offset:50176
	ds_read_b128 v[174:177], v210 offset:51200
	ds_read_b128 v[178:181], v210 offset:52224
	ds_read_b128 v[182:185], v210 offset:53248
	ds_read_b128 v[186:189], v210 offset:54272
	ds_read_b128 v[190:193], v210 offset:55296
	ds_read_b128 v[194:197], v210 offset:56320
	s_nop 0
	global_load_lds_dwordx4 v170, s[62:63]
	s_add_i32 m0, s64, 0x2000
	s_add_u32 s34, s34, 0xc000
	global_load_lds_dwordx4 v171, s[62:63]
	s_addc_u32 s35, s35, 0
	s_add_i32 s62, s70, s3
	s_mov_b32 m0, s62
	s_nop 0
	global_load_lds_dwordx4 v170, s[34:35]
	s_add_i32 m0, s62, 0x2000
	s_nop 0
	global_load_lds_dwordx4 v171, s[34:35]
	s_mov_b32 m0, s45
	s_nop 0
	global_load_lds_dwordx4 v170, s[30:31]
	s_mov_b32 m0, s46
	s_nop 0
	global_load_lds_dwordx4 v171, s[30:31]
	s_waitcnt vmcnt(8)
	s_waitcnt lgkmcnt(0)
	s_barrier
	s_setprio 1
	s_waitcnt lgkmcnt(0)
	v_mfma_f32_16x16x32_bf16 v[62:65], v[130:133], v[162:165], v[62:65]
	v_mfma_f32_16x16x32_bf16 v[62:65], v[134:137], v[166:169], v[62:65]
	v_mfma_f32_16x16x32_bf16 v[46:49], v[134:137], v[178:181], v[46:49]
	v_mfma_f32_16x16x32_bf16 v[46:49], v[130:133], v[174:177], v[46:49]
	v_mfma_f32_16x16x32_bf16 v[30:33], v[130:133], v[182:185], v[30:33]
	v_mfma_f32_16x16x32_bf16 v[30:33], v[134:137], v[186:189], v[30:33]
	v_mfma_f32_16x16x32_bf16 v[14:17], v[134:137], v[194:197], v[14:17]
	v_mfma_f32_16x16x32_bf16 v[14:17], v[130:133], v[190:193], v[14:17]
	v_mfma_f32_16x16x32_bf16 v[10:13], v[138:141], v[190:193], v[10:13]
	v_mfma_f32_16x16x32_bf16 v[10:13], v[142:145], v[194:197], v[10:13]
	v_mfma_f32_16x16x32_bf16 v[26:29], v[142:145], v[186:189], v[26:29]
	v_mfma_f32_16x16x32_bf16 v[26:29], v[138:141], v[182:185], v[26:29]
	v_mfma_f32_16x16x32_bf16 v[42:45], v[138:141], v[174:177], v[42:45]
	v_mfma_f32_16x16x32_bf16 v[42:45], v[142:145], v[178:181], v[42:45]
	v_mfma_f32_16x16x32_bf16 v[58:61], v[142:145], v[166:169], v[58:61]
	v_mfma_f32_16x16x32_bf16 v[58:61], v[138:141], v[162:165], v[58:61]
	s_setprio 0
	s_setprio 1
	v_mfma_f32_16x16x32_bf16 v[50:53], v[154:157], v[162:165], v[50:53]
	v_mfma_f32_16x16x32_bf16 v[50:53], v[158:161], v[166:169], v[50:53]
	v_mfma_f32_16x16x32_bf16 v[34:37], v[158:161], v[178:181], v[34:37]
	v_mfma_f32_16x16x32_bf16 v[34:37], v[154:157], v[174:177], v[34:37]
	v_mfma_f32_16x16x32_bf16 v[18:21], v[154:157], v[182:185], v[18:21]
	v_mfma_f32_16x16x32_bf16 v[18:21], v[158:161], v[186:189], v[18:21]
	v_mfma_f32_16x16x32_bf16 v[2:5], v[158:161], v[194:197], v[2:5]
	v_mfma_f32_16x16x32_bf16 v[2:5], v[154:157], v[190:193], v[2:5]
	v_mfma_f32_16x16x32_bf16 v[6:9], v[146:149], v[190:193], v[6:9]
	v_mfma_f32_16x16x32_bf16 v[6:9], v[150:153], v[194:197], v[6:9]
	v_mfma_f32_16x16x32_bf16 v[22:25], v[150:153], v[186:189], v[22:25]
	v_mfma_f32_16x16x32_bf16 v[22:25], v[146:149], v[182:185], v[22:25]
	v_mfma_f32_16x16x32_bf16 v[38:41], v[146:149], v[174:177], v[38:41]
	v_mfma_f32_16x16x32_bf16 v[38:41], v[150:153], v[178:181], v[38:41]
	v_mfma_f32_16x16x32_bf16 v[54:57], v[150:153], v[166:169], v[54:57]
	v_mfma_f32_16x16x32_bf16 v[54:57], v[146:149], v[162:165], v[54:57]
	s_setprio 0
	s_barrier
	s_add_u32 s28, s28, 0xc000
	s_mov_b32 m0, s47
	s_addc_u32 s29, s29, 0
	s_add_i32 s69, s69, 2
	global_load_lds_dwordx4 v170, s[28:29]
	s_mov_b32 m0, s48
	s_add_u32 s61, s61, 0x10000
	global_load_lds_dwordx4 v171, s[28:29]
	s_addc_u32 s66, s66, 0
	s_add_u32 s67, s67, 0x10000
	s_addc_u32 s68, s68, 0
	s_cmp_gt_u32 s69, 61
	s_cbranch_scc0 .LBB0_805
	s_and_b64 vcc, exec, s[12:13]
	s_cbranch_vccz .LBB0_808
	s_barrier

; #define PG8_STAGE(bufoff, gbase, voff) do { const char* _gb = (const char*)(gbase); asm volatile("" : "+s"(_gb)); _Pragma("unroll") for (int _i = 0; _i < 2; ++_i) \
;         __builtin_amdgcn_global_load_lds((const unsigned*)(_gb + (voff)[_i]), (PG8_LAS unsigned*)(lds + (bufoff) + ldsw + _i * 8192), 16, 0, 0); } while (0)
; #define PG8_LDA(dst, b, h) do { _Pragma("unroll") for (int m = 0; m < 4; ++m) _Pragma("unroll") for (int k = 0; k < 2; ++k) dst[m][k] = *(const PG8_LAS bf16x8*)(lds + PG8_SA(b, h) + aoff + m * 2048 + k * 1024); } while (0)
; #define PG8_LDB(dst, b, h) do { _Pragma("unroll") for (int n = 0; n < 2; ++n) _Pragma("unroll") for (int k = 0; k < 2; ++k) dst[n][k] = *(const PG8_LAS bf16x8*)(lds + PG8_SB(b, h) + boff + n * 2048 + k * 1024); } while (0)
; #define PG8_MMA(ai, bj, At, Bt) do { __builtin_amdgcn_s_setprio(1); _Pragma("unroll") for (int m = 0; m < 4; ++m) _Pragma("unroll") for (int n = 0; n < 2; ++n) _Pragma("unroll") for (int k = 0; k < 2; ++k) \
;         acc[ai][bj][m][n] = __builtin_amdgcn_mfma_f32_16x16x32_bf16(Bt[n][k], At[m][k], acc[ai][bj][m][n], 0, 0, 0); __builtin_amdgcn_s_setprio(0); } while (0)
; #define PG8_WAIT_L(n) asm volatile("s_waitcnt lgkmcnt(" #n ")" ::: "memory")
; #define PG8_BAR __builtin_amdgcn_s_barrier()
; #define PG8_SCHED __builtin_amdgcn_sched_barrier(0)
; template <class Epi, class Sched, bool ALIGN_EPI = false, bool SP2 = false, bool HALFM = false>
; __device__ __forceinline__ void gemm_phase(PG8_LAS unsigned char* lds, const Gemm g, const Sched& S, const Epi& E) {
;     ...
;             PG8_LDB(B0, 0, 0); PG8_LDB(B1, 0, 1); PG8_SCHED; PG8_LDA(At, 0, 0);
;             PG8_WAIT_V8R; PG8_WAIT_L(0); PG8_BAR; PG8_MMA(0, 0, At, B0); PG8_MMA(0, 1, At, B1); PG8_BAR; PG8_SCHED;
;             if constexpr (!HALFM) { PG8_LDA(At, 0, 1); } PG8_STAGE(PG8_SB(0, 0), b2, voffB); PG8_STAGE(PG8_SB(0, 1), b2 + hstep, voffB); PG8_STAGE(PG8_SA(0, 0), a2, voffA);
;             PG8_WAIT_V8R; PG8_WAIT_L(0); PG8_BAR; if constexpr (!HALFM) { PG8_MMA(1, 0, At, B0); PG8_MMA(1, 1, At, B1); } PG8_BAR; PG8_SCHED;
.LBB0_901:
	ds_read_b128 v[134:137], v149
	ds_read_b128 v[138:141], v149 offset:1024
	ds_read_b128 v[156:159], v149 offset:2048
	ds_read_b128 v[160:163], v149 offset:3072
	ds_read_b128 v[164:167], v150
	ds_read_b128 v[168:171], v150 offset:1024
	ds_read_b128 v[172:175], v150 offset:2048
	ds_read_b128 v[176:179], v150 offset:3072
	s_cmp_eq_u32 s56, 60
	s_cselect_b32 s4, s50, s52
	s_cselect_b32 s5, s23, s53
	s_cselect_b32 s30, s51, s54
	s_cselect_b32 s31, s21, s55
	s_add_u32 s6, s4, 0x8000
	s_addc_u32 s7, s5, 0
	ds_read_b128 v[180:183], v151
	ds_read_b128 v[184:187], v151 offset:1024
	ds_read_b128 v[188:191], v151 offset:2048
	ds_read_b128 v[192:195], v151 offset:3072
	ds_read_b128 v[196:199], v151 offset:4096
	ds_read_b128 v[200:203], v151 offset:5120
	ds_read_b128 v[210:213], v151 offset:6144
	ds_read_b128 v[214:217], v151 offset:7168
	s_waitcnt vmcnt(8)
	s_waitcnt lgkmcnt(0)
	s_barrier
	s_setprio 1
	s_waitcnt lgkmcnt(0)
	v_mfma_f32_16x16x32_bf16 v[126:129], v[134:137], v[180:183], v[126:129]
	v_mfma_f32_16x16x32_bf16 v[126:129], v[138:141], v[184:187], v[126:129]
	v_mfma_f32_16x16x32_bf16 v[118:121], v[138:141], v[192:195], v[118:121]
	v_mfma_f32_16x16x32_bf16 v[118:121], v[134:137], v[188:191], v[118:121]
	v_mfma_f32_16x16x32_bf16 v[106:109], v[134:137], v[196:199], v[106:109]
	v_mfma_f32_16x16x32_bf16 v[106:109], v[138:141], v[200:203], v[106:109]
	v_mfma_f32_16x16x32_bf16 v[82:85], v[138:141], v[214:217], v[82:85]
	v_mfma_f32_16x16x32_bf16 v[82:85], v[134:137], v[210:213], v[82:85]
	v_mfma_f32_16x16x32_bf16 v[78:81], v[156:159], v[210:213], v[78:81]
	v_mfma_f32_16x16x32_bf16 v[78:81], v[160:163], v[214:217], v[78:81]
	v_mfma_f32_16x16x32_bf16 v[98:101], v[160:163], v[200:203], v[98:101]
	v_mfma_f32_16x16x32_bf16 v[98:101], v[156:159], v[196:199], v[98:101]
	v_mfma_f32_16x16x32_bf16 v[114:117], v[156:159], v[188:191], v[114:117]
	v_mfma_f32_16x16x32_bf16 v[114:117], v[160:163], v[192:195], v[114:117]
	v_mfma_f32_16x16x32_bf16 v[122:125], v[160:163], v[184:187], v[122:125]
	v_mfma_f32_16x16x32_bf16 v[122:125], v[156:159], v[180:183], v[122:125]
	s_setprio 0
	s_setprio 1
	v_mfma_f32_16x16x32_bf16 v[102:105], v[172:175], v[180:183], v[102:105]
	v_mfma_f32_16x16x32_bf16 v[102:105], v[176:179], v[184:187], v[102:105]
	v_mfma_f32_16x16x32_bf16 v[90:93], v[176:179], v[192:195], v[90:93]
	v_mfma_f32_16x16x32_bf16 v[90:93], v[172:175], v[188:191], v[90:93]
	v_mfma_f32_16x16x32_bf16 v[74:77], v[172:175], v[196:199], v[74:77]
	v_mfma_f32_16x16x32_bf16 v[74:77], v[176:179], v[200:203], v[74:77]
	v_mfma_f32_16x16x32_bf16 v[66:69], v[176:179], v[214:217], v[66:69]
	v_mfma_f32_16x16x32_bf16 v[66:69], v[172:175], v[210:213], v[66:69]
	v_mfma_f32_16x16x32_bf16 v[70:73], v[164:167], v[210:213], v[70:73]
	v_mfma_f32_16x16x32_bf16 v[70:73], v[168:171], v[214:217], v[70:73]
	v_mfma_f32_16x16x32_bf16 v[86:89], v[168:171], v[200:203], v[86:89]
	v_mfma_f32_16x16x32_bf16 v[86:89], v[164:167], v[196:199], v[86:89]
	v_mfma_f32_16x16x32_bf16 v[94:97], v[164:167], v[188:191], v[94:97]
	v_mfma_f32_16x16x32_bf16 v[94:97], v[168:171], v[192:195], v[94:97]
	v_mfma_f32_16x16x32_bf16 v[110:113], v[168:171], v[184:187], v[110:113]
	v_mfma_f32_16x16x32_bf16 v[110:113], v[164:167], v[180:183], v[110:113]
	s_setprio 0
	s_barrier
	s_add_i32 s57, s46, s36
	s_mov_b64 s[58:59], s[30:31]
	s_mov_b32 m0, s57
	ds_read_b128 v[180:183], v151 offset:16384
	ds_read_b128 v[184:187], v151 offset:17408
	ds_read_b128 v[188:191], v151 offset:18432
	ds_read_b128 v[192:195], v151 offset:19456
	ds_read_b128 v[196:199], v151 offset:20480
	ds_read_b128 v[200:203], v151 offset:21504
	ds_read_b128 v[210:213], v151 offset:22528
	ds_read_b128 v[214:217], v151 offset:23552
	s_nop 0
	global_load_lds_dwordx4 v154, s[58:59]
	s_add_i32 m0, s57, 0x2000
	s_nop 0
	global_load_lds_dwordx4 v153, s[58:59]
	s_add_u32 s58, s30, 0x4000
	s_addc_u32 s59, s31, 0
	s_add_i32 s57, s47, s36
	s_mov_b32 m0, s57
	s_nop 0
	global_load_lds_dwordx4 v154, s[58:59]
	s_add_i32 m0, s57, 0x2000
	s_nop 0
	global_load_lds_dwordx4 v153, s[58:59]
	s_mov_b64 s[58:59], s[4:5]
	s_mov_b32 m0, s37
	s_nop 0
	global_load_lds_dwordx4 v154, s[58:59]
	s_mov_b32 m0, s38
	s_nop 0
	global_load_lds_dwordx4 v153, s[58:59]
	s_waitcnt vmcnt(8)
	s_waitcnt lgkmcnt(0)
	s_barrier
	s_setprio 1
	s_waitcnt lgkmcnt(0)
	v_mfma_f32_16x16x32_bf16 v[62:65], v[134:137], v[180:183], v[62:65]
	v_mfma_f32_16x16x32_bf16 v[62:65], v[138:141], v[184:187], v[62:65]
	v_mfma_f32_16x16x32_bf16 v[50:53], v[138:141], v[192:195], v[50:53]
	v_mfma_f32_16x16x32_bf16 v[50:53], v[134:137], v[188:191], v[50:53]
	v_mfma_f32_16x16x32_bf16 v[34:37], v[134:137], v[196:199], v[34:37]
	v_mfma_f32_16x16x32_bf16 v[34:37], v[138:141], v[200:203], v[34:37]
	v_mfma_f32_16x16x32_bf16 v[18:21], v[138:141], v[214:217], v[18:21]
	v_mfma_f32_16x16x32_bf16 v[18:21], v[134:137], v[210:213], v[18:21]
	v_mfma_f32_16x16x32_bf16 v[14:17], v[156:159], v[210:213], v[14:17]
	v_mfma_f32_16x16x32_bf16 v[14:17], v[160:163], v[214:217], v[14:17]
	v_mfma_f32_16x16x32_bf16 v[30:33], v[160:163], v[200:203], v[30:33]
	v_mfma_f32_16x16x32_bf16 v[30:33], v[156:159], v[196:199], v[30:33]
	v_mfma_f32_16x16x32_bf16 v[46:49], v[156:159], v[188:191], v[46:49]
	v_mfma_f32_16x16x32_bf16 v[46:49], v[160:163], v[192:195], v[46:49]
	v_mfma_f32_16x16x32_bf16 v[58:61], v[160:163], v[184:187], v[58:61]
	v_mfma_f32_16x16x32_bf16 v[58:61], v[156:159], v[180:183], v[58:61]
	s_setprio 0
	s_setprio 1
	v_mfma_f32_16x16x32_bf16 v[42:45], v[172:175], v[180:183], v[42:45]
	v_mfma_f32_16x16x32_bf16 v[42:45], v[176:179], v[184:187], v[42:45]
	v_mfma_f32_16x16x32_bf16 v[26:29], v[176:179], v[192:195], v[26:29]
	v_mfma_f32_16x16x32_bf16 v[26:29], v[172:175], v[188:191], v[26:29]
	v_mfma_f32_16x16x32_bf16 v[10:13], v[172:175], v[196:199], v[10:13]
	v_mfma_f32_16x16x32_bf16 v[10:13], v[176:179], v[200:203], v[10:13]
	v_mfma_f32_16x16x32_bf16 v[2:5], v[176:179], v[214:217], v[2:5]
	v_mfma_f32_16x16x32_bf16 v[2:5], v[172:175], v[210:213], v[2:5]
	v_mfma_f32_16x16x32_bf16 v[6:9], v[164:167], v[210:213], v[6:9]
	v_mfma_f32_16x16x32_bf16 v[6:9], v[168:171], v[214:217], v[6:9]
	v_mfma_f32_16x16x32_bf16 v[22:25], v[168:171], v[200:203], v[22:25]
	v_mfma_f32_16x16x32_bf16 v[22:25], v[164:167], v[196:199], v[22:25]
	v_mfma_f32_16x16x32_bf16 v[38:41], v[164:167], v[188:191], v[38:41]
	v_mfma_f32_16x16x32_bf16 v[38:41], v[168:171], v[192:195], v[38:41]
	v_mfma_f32_16x16x32_bf16 v[54:57], v[168:171], v[184:187], v[54:57]
	v_mfma_f32_16x16x32_bf16 v[54:57], v[164:167], v[180:183], v[54:57]
	s_setprio 0
	s_barrier
; #define PG8_STAGE(bufoff, gbase, voff) do { const char* _gb = (const char*)(gbase); asm volatile("" : "+s"(_gb)); _Pragma("unroll") for (int _i = 0; _i < 2; ++_i) \
;         __builtin_amdgcn_global_load_lds((const unsigned*)(_gb + (voff)[_i]), (PG8_LAS unsigned*)(lds + (bufoff) + ldsw + _i * 8192), 16, 0, 0); } while (0)
; #define PG8_LDA(dst, b, h) do { _Pragma("unroll") for (int m = 0; m < 4; ++m) _Pragma("unroll") for (int k = 0; k < 2; ++k) dst[m][k] = *(const PG8_LAS bf16x8*)(lds + PG8_SA(b, h) + aoff + m * 2048 + k * 1024); } while (0)
; #define PG8_LDB(dst, b, h) do { _Pragma("unroll") for (int n = 0; n < 2; ++n) _Pragma("unroll") for (int k = 0; k < 2; ++k) dst[n][k] = *(const PG8_LAS bf16x8*)(lds + PG8_SB(b, h) + boff + n * 2048 + k * 1024); } while (0)
; #define PG8_MMA(ai, bj, At, Bt) do { __builtin_amdgcn_s_setprio(1); _Pragma("unroll") for (int m = 0; m < 4; ++m) _Pragma("unroll") for (int n = 0; n < 2; ++n) _Pragma("unroll") for (int k = 0; k < 2; ++k) \
;         acc[ai][bj][m][n] = __builtin_amdgcn_mfma_f32_16x16x32_bf16(Bt[n][k], At[m][k], acc[ai][bj][m][n], 0, 0, 0); __builtin_amdgcn_s_setprio(0); } while (0)
; #define PG8_WAIT_V(n) asm volatile("s_waitcnt vmcnt(" #n ")" ::: "memory")
; #define PG8_WAIT_L(n) asm volatile("s_waitcnt lgkmcnt(" #n ")" ::: "memory")
; #define PG8_BAR __builtin_amdgcn_s_barrier()
; #define PG8_SCHED __builtin_amdgcn_sched_barrier(0)
; template <class Epi, class Sched, bool ALIGN_EPI = false, bool SP2 = false, bool HALFM = false>
; __device__ __forceinline__ void gemm_phase(PG8_LAS unsigned char* lds, const Gemm g, const Sched& S, const Epi& E) {
;     ...
;             PG8_LDB(B0, 1, 0); PG8_LDB(B1, 1, 1); PG8_SCHED; PG8_LDA(At, 1, 0); PG8_STAGE(PG8_SA(0, 1), a2 + hstepA, voffA);
;             PG8_WAIT_V8R; PG8_WAIT_L(0); PG8_BAR; PG8_MMA(0, 0, At, B0); PG8_MMA(0, 1, At, B1); PG8_BAR; PG8_SCHED;
;             if constexpr (!HALFM) { PG8_LDA(At, 1, 1); } PG8_STAGE(PG8_SB(1, 0), b3, voffB); PG8_STAGE(PG8_SB(1, 1), b3 + hstep, voffB); PG8_STAGE(PG8_SA(1, 0), a3, voffA);
;             PG8_WAIT_V(8); PG8_WAIT_L(0); PG8_BAR; if constexpr (!HALFM) { PG8_MMA(1, 0, At, B0); PG8_MMA(1, 1, At, B1); } PG8_BAR; PG8_SCHED;
;             PG8_STAGE(PG8_SA(1, 1), a3 + hstepA, voffA);
	s_add_i32 s57, 0, 0x18000
	v_add_u32_e32 v155, s57, v147
	s_add_i32 s60, 0, 0x1c000
	ds_read_b128 v[134:137], v155
	ds_read_b128 v[138:141], v155 offset:1024
	ds_read_b128 v[156:159], v155 offset:2048
	ds_read_b128 v[160:163], v155 offset:3072
	v_add_u32_e32 v155, s60, v147
	ds_read_b128 v[164:167], v155
	ds_read_b128 v[168:171], v155 offset:1024
	ds_read_b128 v[172:175], v155 offset:2048
	ds_read_b128 v[176:179], v155 offset:3072
	s_add_u32 s58, s4, 0x4000
	s_addc_u32 s59, s5, 0
	s_mov_b32 m0, s39
	ds_read_b128 v[180:183], v151 offset:32768
	ds_read_b128 v[184:187], v151 offset:33792
	ds_read_b128 v[188:191], v151 offset:34816
	ds_read_b128 v[192:195], v151 offset:35840
	ds_read_b128 v[196:199], v151 offset:36864
	ds_read_b128 v[200:203], v151 offset:37888
	ds_read_b128 v[210:213], v151 offset:38912
	ds_read_b128 v[214:217], v151 offset:39936
	s_nop 0
	global_load_lds_dwordx4 v154, s[58:59]
	s_mov_b32 m0, s40
	s_nop 0
	global_load_lds_dwordx4 v153, s[58:59]
	s_waitcnt vmcnt(8)
	s_waitcnt lgkmcnt(0)
	s_barrier
	s_setprio 1
	s_waitcnt lgkmcnt(0)
	v_mfma_f32_16x16x32_bf16 v[126:129], v[134:137], v[180:183], v[126:129]
	v_mfma_f32_16x16x32_bf16 v[126:129], v[138:141], v[184:187], v[126:129]
	v_mfma_f32_16x16x32_bf16 v[118:121], v[138:141], v[192:195], v[118:121]
	v_mfma_f32_16x16x32_bf16 v[118:121], v[134:137], v[188:191], v[118:121]
	v_mfma_f32_16x16x32_bf16 v[106:109], v[134:137], v[196:199], v[106:109]
	v_mfma_f32_16x16x32_bf16 v[106:109], v[138:141], v[200:203], v[106:109]
	v_mfma_f32_16x16x32_bf16 v[82:85], v[138:141], v[214:217], v[82:85]
	v_mfma_f32_16x16x32_bf16 v[82:85], v[134:137], v[210:213], v[82:85]
	v_mfma_f32_16x16x32_bf16 v[78:81], v[156:159], v[210:213], v[78:81]
	v_mfma_f32_16x16x32_bf16 v[78:81], v[160:163], v[214:217], v[78:81]
	v_mfma_f32_16x16x32_bf16 v[98:101], v[160:163], v[200:203], v[98:101]
	v_mfma_f32_16x16x32_bf16 v[98:101], v[156:159], v[196:199], v[98:101]
	v_mfma_f32_16x16x32_bf16 v[114:117], v[156:159], v[188:191], v[114:117]
	v_mfma_f32_16x16x32_bf16 v[114:117], v[160:163], v[192:195], v[114:117]
	v_mfma_f32_16x16x32_bf16 v[122:125], v[160:163], v[184:187], v[122:125]
	v_mfma_f32_16x16x32_bf16 v[122:125], v[156:159], v[180:183], v[122:125]
	s_setprio 0
	s_setprio 1
	v_mfma_f32_16x16x32_bf16 v[102:105], v[172:175], v[180:183], v[102:105]
	v_mfma_f32_16x16x32_bf16 v[102:105], v[176:179], v[184:187], v[102:105]
	v_mfma_f32_16x16x32_bf16 v[90:93], v[176:179], v[192:195], v[90:93]
	v_mfma_f32_16x16x32_bf16 v[90:93], v[172:175], v[188:191], v[90:93]
	v_mfma_f32_16x16x32_bf16 v[74:77], v[172:175], v[196:199], v[74:77]
	v_mfma_f32_16x16x32_bf16 v[74:77], v[176:179], v[200:203], v[74:77]
	v_mfma_f32_16x16x32_bf16 v[66:69], v[176:179], v[214:217], v[66:69]
	v_mfma_f32_16x16x32_bf16 v[66:69], v[172:175], v[210:213], v[66:69]
	v_mfma_f32_16x16x32_bf16 v[70:73], v[164:167], v[210:213], v[70:73]
	v_mfma_f32_16x16x32_bf16 v[70:73], v[168:171], v[214:217], v[70:73]
	v_mfma_f32_16x16x32_bf16 v[86:89], v[168:171], v[200:203], v[86:89]
	v_mfma_f32_16x16x32_bf16 v[86:89], v[164:167], v[196:199], v[86:89]
	v_mfma_f32_16x16x32_bf16 v[94:97], v[164:167], v[188:191], v[94:97]
	v_mfma_f32_16x16x32_bf16 v[94:97], v[168:171], v[192:195], v[94:97]
	v_mfma_f32_16x16x32_bf16 v[110:113], v[168:171], v[184:187], v[110:113]
	v_mfma_f32_16x16x32_bf16 v[110:113], v[164:167], v[180:183], v[110:113]
	s_setprio 0
	s_barrier
	s_add_u32 s58, s30, 0x8000
	s_addc_u32 s59, s31, 0
	s_add_i32 s57, s57, s36
	s_mov_b32 m0, s57
	ds_read_b128 v[180:183], v151 offset:49152
	ds_read_b128 v[184:187], v151 offset:50176
	ds_read_b128 v[188:191], v151 offset:51200
	ds_read_b128 v[192:195], v151 offset:52224
	ds_read_b128 v[196:199], v151 offset:53248
	ds_read_b128 v[200:203], v151 offset:54272
	ds_read_b128 v[210:213], v151 offset:55296
	ds_read_b128 v[214:217], v151 offset:56320
	s_nop 0
	global_load_lds_dwordx4 v154, s[58:59]
	s_add_i32 m0, s57, 0x2000
	s_add_u32 s30, s30, 0xc000
	s_addc_u32 s31, s31, 0
	s_add_i32 s57, s60, s36
	global_load_lds_dwordx4 v153, s[58:59]
	s_mov_b32 m0, s57
	s_nop 0
	global_load_lds_dwordx4 v154, s[30:31]
	s_add_i32 m0, s57, 0x2000
	s_nop 0
	global_load_lds_dwordx4 v153, s[30:31]
	s_mov_b32 m0, s42
	s_nop 0
	global_load_lds_dwordx4 v154, s[6:7]
	s_mov_b32 m0, s43
	s_nop 0
	global_load_lds_dwordx4 v153, s[6:7]
	s_waitcnt vmcnt(8)
	s_waitcnt lgkmcnt(0)
	s_barrier
	s_setprio 1
	s_waitcnt lgkmcnt(0)
	v_mfma_f32_16x16x32_bf16 v[62:65], v[134:137], v[180:183], v[62:65]
	v_mfma_f32_16x16x32_bf16 v[62:65], v[138:141], v[184:187], v[62:65]
	v_mfma_f32_16x16x32_bf16 v[50:53], v[138:141], v[192:195], v[50:53]
	v_mfma_f32_16x16x32_bf16 v[50:53], v[134:137], v[188:191], v[50:53]
	v_mfma_f32_16x16x32_bf16 v[34:37], v[134:137], v[196:199], v[34:37]
	v_mfma_f32_16x16x32_bf16 v[34:37], v[138:141], v[200:203], v[34:37]
	v_mfma_f32_16x16x32_bf16 v[18:21], v[138:141], v[214:217], v[18:21]
	v_mfma_f32_16x16x32_bf16 v[18:21], v[134:137], v[210:213], v[18:21]
	v_mfma_f32_16x16x32_bf16 v[14:17], v[156:159], v[210:213], v[14:17]
	v_mfma_f32_16x16x32_bf16 v[14:17], v[160:163], v[214:217], v[14:17]
	v_mfma_f32_16x16x32_bf16 v[30:33], v[160:163], v[200:203], v[30:33]
	v_mfma_f32_16x16x32_bf16 v[30:33], v[156:159], v[196:199], v[30:33]
	v_mfma_f32_16x16x32_bf16 v[46:49], v[156:159], v[188:191], v[46:49]
	v_mfma_f32_16x16x32_bf16 v[46:49], v[160:163], v[192:195], v[46:49]
	v_mfma_f32_16x16x32_bf16 v[58:61], v[160:163], v[184:187], v[58:61]
	v_mfma_f32_16x16x32_bf16 v[58:61], v[156:159], v[180:183], v[58:61]
	s_setprio 0
	s_setprio 1
	v_mfma_f32_16x16x32_bf16 v[42:45], v[172:175], v[180:183], v[42:45]
	v_mfma_f32_16x16x32_bf16 v[42:45], v[176:179], v[184:187], v[42:45]
	v_mfma_f32_16x16x32_bf16 v[26:29], v[176:179], v[192:195], v[26:29]
	v_mfma_f32_16x16x32_bf16 v[26:29], v[172:175], v[188:191], v[26:29]
	v_mfma_f32_16x16x32_bf16 v[10:13], v[172:175], v[196:199], v[10:13]
	v_mfma_f32_16x16x32_bf16 v[10:13], v[176:179], v[200:203], v[10:13]
	v_mfma_f32_16x16x32_bf16 v[2:5], v[176:179], v[214:217], v[2:5]
	v_mfma_f32_16x16x32_bf16 v[2:5], v[172:175], v[210:213], v[2:5]
	v_mfma_f32_16x16x32_bf16 v[6:9], v[164:167], v[210:213], v[6:9]
	v_mfma_f32_16x16x32_bf16 v[6:9], v[168:171], v[214:217], v[6:9]
	v_mfma_f32_16x16x32_bf16 v[22:25], v[168:171], v[200:203], v[22:25]
	v_mfma_f32_16x16x32_bf16 v[22:25], v[164:167], v[196:199], v[22:25]
	v_mfma_f32_16x16x32_bf16 v[38:41], v[164:167], v[188:191], v[38:41]
	v_mfma_f32_16x16x32_bf16 v[38:41], v[168:171], v[192:195], v[38:41]
	v_mfma_f32_16x16x32_bf16 v[54:57], v[168:171], v[184:187], v[54:57]
	v_mfma_f32_16x16x32_bf16 v[54:57], v[164:167], v[180:183], v[54:57]
	s_setprio 0
	s_barrier
	s_add_u32 s4, s4, 0xc000
	s_mov_b32 m0, s44
	s_addc_u32 s5, s5, 0
	s_add_i32 s56, s56, 2
	global_load_lds_dwordx4 v154, s[4:5]
	s_mov_b32 m0, s45
	s_add_u32 s52, s52, 0x10000
	global_load_lds_dwordx4 v153, s[4:5]
	s_addc_u32 s53, s53, 0
	s_add_u32 s54, s54, 0x10000
	s_addc_u32 s55, s55, 0
	s_cmp_gt_u32 s56, 61
	s_cbranch_scc0 .LBB0_901
	s_and_b64 vcc, exec, s[18:19]
	s_cbranch_vccz .LBB0_904
	s_barrier

; #define PG8_STAGE(bufoff, gbase, voff) do { const char* _gb = (const char*)(gbase); asm volatile("" : "+s"(_gb)); _Pragma("unroll") for (int _i = 0; _i < 2; ++_i) \
;         __builtin_amdgcn_global_load_lds((const unsigned*)(_gb + (voff)[_i]), (PG8_LAS unsigned*)(lds + (bufoff) + ldsw + _i * 8192), 16, 0, 0); } while (0)
; #define PG8_LDA(dst, b, h) do { _Pragma("unroll") for (int m = 0; m < 4; ++m) _Pragma("unroll") for (int k = 0; k < 2; ++k) dst[m][k] = *(const PG8_LAS bf16x8*)(lds + PG8_SA(b, h) + aoff + m * 2048 + k * 1024); } while (0)
; #define PG8_LDB(dst, b, h) do { _Pragma("unroll") for (int n = 0; n < 2; ++n) _Pragma("unroll") for (int k = 0; k < 2; ++k) dst[n][k] = *(const PG8_LAS bf16x8*)(lds + PG8_SB(b, h) + boff + n * 2048 + k * 1024); } while (0)
; #define PG8_WAIT_L(n) asm volatile("s_waitcnt lgkmcnt(" #n ")" ::: "memory")
; #define PG8_BAR __builtin_amdgcn_s_barrier()
; #define PG8_SCHED __builtin_amdgcn_sched_barrier(0)
; template <class Epi, class Sched, bool ALIGN_EPI = false, bool SP2 = false, bool HALFM = false>
; __device__ __forceinline__ void gemm_phase(PG8_LAS unsigned char* lds, const Gemm g, const Sched& S, const Epi& E) {
;     ...
;         for (int t = 0; t < nt; t += 2) {
;             const bool last = (t == nt - 2);
;             const char* a1 = cA + (size_t)(t + 1) * kstep;
;             const char* a2 = last ? nA : cA + (size_t)(t + 2) * kstep; const char* b2 = last ? nB : cB + (size_t)(t + 2) * kstep;
;             const char* a3 = a2 + kstep; const char* b3 = b2 + kstep;
;             if (last && has_next) S.a_ready(nxt);
;             if constexpr (Epi::HAS_PREFETCH) { if (last) E.prefetch(cur, wid, lane); }
;             asm volatile("" : "+v"(voffA[0]), "+v"(voffA[1])); voffB[0] = voffA[0]; voffB[1] = voffA[1];
;             if constexpr (SP2) {
;             PG8_LDB(B0, 0, 0); PG8_LDB(B1, 0, 1); PG8_SCHED; PG8_LDA(At, 0, 0);
;             PG8_WAIT_V8R; PG8_WAIT_L(0); PG8_BAR; PG8_MMA(0, 0, At, B0); PG8_MMA(0, 1, At, B1); PG8_BAR; PG8_SCHED;
;             if constexpr (!HALFM) { PG8_LDA(At, 0, 1); } PG8_STAGE(PG8_SB(0, 0), b2, voffB); PG8_STAGE(PG8_SB(0, 1), b2 + hstep, voffB); PG8_STAGE(PG8_SA(0, 0), a2, voffA);
;             PG8_WAIT_V8R; PG8_WAIT_L(0); PG8_BAR; if constexpr (!HALFM) { PG8_MMA(1, 0, At, B0); PG8_MMA(1, 1, At, B1); } PG8_BAR; PG8_SCHED;
.LBB0_918:
	ds_read_b128 v[132:135], v143
	ds_read_b128 v[136:139], v143 offset:1024
	ds_read_b128 v[148:151], v143 offset:2048
	ds_read_b128 v[152:155], v143 offset:3072
	ds_read_b128 v[156:159], v144
	ds_read_b128 v[160:163], v144 offset:1024
	ds_read_b128 v[164:167], v144 offset:2048
	ds_read_b128 v[168:171], v144 offset:3072
	s_cmp_eq_u32 s59, 60
	s_cselect_b32 s4, s53, s55
	s_cselect_b32 s5, s23, s56
	s_cselect_b32 s30, s54, s57
	s_cselect_b32 s31, s21, s58
	s_add_u32 s6, s4, 0x8000
	s_addc_u32 s7, s5, 0
	ds_read_b128 v[172:175], v145
	ds_read_b128 v[176:179], v145 offset:1024
	ds_read_b128 v[180:183], v145 offset:2048
	ds_read_b128 v[184:187], v145 offset:3072
	ds_read_b128 v[188:191], v145 offset:4096
	ds_read_b128 v[192:195], v145 offset:5120
	ds_read_b128 v[196:199], v145 offset:6144
	ds_read_b128 v[200:203], v145 offset:7168
	s_waitcnt vmcnt(8)
	s_waitcnt lgkmcnt(0)
	s_barrier
	s_setprio 1
	s_waitcnt lgkmcnt(0)
	v_mfma_f32_16x16x32_bf16 v[126:129], v[132:135], v[172:175], v[126:129]
	v_mfma_f32_16x16x32_bf16 v[126:129], v[136:139], v[176:179], v[126:129]
	v_mfma_f32_16x16x32_bf16 v[118:121], v[136:139], v[184:187], v[118:121]
	v_mfma_f32_16x16x32_bf16 v[118:121], v[132:135], v[180:183], v[118:121]
	v_mfma_f32_16x16x32_bf16 v[106:109], v[132:135], v[188:191], v[106:109]
	v_mfma_f32_16x16x32_bf16 v[106:109], v[136:139], v[192:195], v[106:109]
	v_mfma_f32_16x16x32_bf16 v[82:85], v[136:139], v[200:203], v[82:85]
	v_mfma_f32_16x16x32_bf16 v[82:85], v[132:135], v[196:199], v[82:85]
	v_mfma_f32_16x16x32_bf16 v[78:81], v[148:151], v[196:199], v[78:81]
	v_mfma_f32_16x16x32_bf16 v[78:81], v[152:155], v[200:203], v[78:81]
	v_mfma_f32_16x16x32_bf16 v[98:101], v[152:155], v[192:195], v[98:101]
	v_mfma_f32_16x16x32_bf16 v[98:101], v[148:151], v[188:191], v[98:101]
	v_mfma_f32_16x16x32_bf16 v[114:117], v[148:151], v[180:183], v[114:117]
	v_mfma_f32_16x16x32_bf16 v[114:117], v[152:155], v[184:187], v[114:117]
	v_mfma_f32_16x16x32_bf16 v[122:125], v[152:155], v[176:179], v[122:125]
	v_mfma_f32_16x16x32_bf16 v[122:125], v[148:151], v[172:175], v[122:125]
	s_setprio 0
	s_setprio 1
	v_mfma_f32_16x16x32_bf16 v[102:105], v[164:167], v[172:175], v[102:105]
	v_mfma_f32_16x16x32_bf16 v[102:105], v[168:171], v[176:179], v[102:105]
	v_mfma_f32_16x16x32_bf16 v[90:93], v[168:171], v[184:187], v[90:93]
	v_mfma_f32_16x16x32_bf16 v[90:93], v[164:167], v[180:183], v[90:93]
	v_mfma_f32_16x16x32_bf16 v[74:77], v[164:167], v[188:191], v[74:77]
	v_mfma_f32_16x16x32_bf16 v[74:77], v[168:171], v[192:195], v[74:77]
	v_mfma_f32_16x16x32_bf16 v[66:69], v[168:171], v[200:203], v[66:69]
	v_mfma_f32_16x16x32_bf16 v[66:69], v[164:167], v[196:199], v[66:69]
	v_mfma_f32_16x16x32_bf16 v[70:73], v[156:159], v[196:199], v[70:73]
	v_mfma_f32_16x16x32_bf16 v[70:73], v[160:163], v[200:203], v[70:73]
	v_mfma_f32_16x16x32_bf16 v[86:89], v[160:163], v[192:195], v[86:89]
	v_mfma_f32_16x16x32_bf16 v[86:89], v[156:159], v[188:191], v[86:89]
	v_mfma_f32_16x16x32_bf16 v[94:97], v[156:159], v[180:183], v[94:97]
	v_mfma_f32_16x16x32_bf16 v[94:97], v[160:163], v[184:187], v[94:97]
	v_mfma_f32_16x16x32_bf16 v[110:113], v[160:163], v[176:179], v[110:113]
	v_mfma_f32_16x16x32_bf16 v[110:113], v[156:159], v[172:175], v[110:113]
	s_setprio 0
	s_barrier
	s_add_i32 s62, s49, s39
	s_mov_b64 s[60:61], s[30:31]
	s_mov_b32 m0, s62
	ds_read_b128 v[172:175], v145 offset:16384
	ds_read_b128 v[176:179], v145 offset:17408
	ds_read_b128 v[180:183], v145 offset:18432
	ds_read_b128 v[184:187], v145 offset:19456
	ds_read_b128 v[188:191], v145 offset:20480
	ds_read_b128 v[192:195], v145 offset:21504
	ds_read_b128 v[196:199], v145 offset:22528
	ds_read_b128 v[200:203], v145 offset:23552
	s_nop 0
	global_load_lds_dwordx4 v130, s[60:61]
	s_add_i32 m0, s62, 0x2000
	s_nop 0
	global_load_lds_dwordx4 v142, s[60:61]
	s_add_u32 s60, s30, 0x4000
	s_addc_u32 s61, s31, 0
	s_add_i32 s62, s50, s39
	s_mov_b32 m0, s62
	s_nop 0
	global_load_lds_dwordx4 v130, s[60:61]
	s_add_i32 m0, s62, 0x2000
	s_nop 0
	global_load_lds_dwordx4 v142, s[60:61]
	s_mov_b64 s[60:61], s[4:5]
	s_mov_b32 m0, s40
	s_nop 0
	global_load_lds_dwordx4 v130, s[60:61]
	s_mov_b32 m0, s41
	s_nop 0
	global_load_lds_dwordx4 v142, s[60:61]
	s_waitcnt vmcnt(8)
	s_waitcnt lgkmcnt(0)
	s_barrier
	s_setprio 1
	s_waitcnt lgkmcnt(0)
	v_mfma_f32_16x16x32_bf16 v[62:65], v[132:135], v[172:175], v[62:65]
	v_mfma_f32_16x16x32_bf16 v[62:65], v[136:139], v[176:179], v[62:65]
	v_mfma_f32_16x16x32_bf16 v[50:53], v[136:139], v[184:187], v[50:53]
	v_mfma_f32_16x16x32_bf16 v[50:53], v[132:135], v[180:183], v[50:53]
	v_mfma_f32_16x16x32_bf16 v[34:37], v[132:135], v[188:191], v[34:37]
	v_mfma_f32_16x16x32_bf16 v[34:37], v[136:139], v[192:195], v[34:37]
	v_mfma_f32_16x16x32_bf16 v[18:21], v[136:139], v[200:203], v[18:21]
	v_mfma_f32_16x16x32_bf16 v[18:21], v[132:135], v[196:199], v[18:21]
	v_mfma_f32_16x16x32_bf16 v[14:17], v[148:151], v[196:199], v[14:17]
	v_mfma_f32_16x16x32_bf16 v[14:17], v[152:155], v[200:203], v[14:17]
	v_mfma_f32_16x16x32_bf16 v[30:33], v[152:155], v[192:195], v[30:33]
	v_mfma_f32_16x16x32_bf16 v[30:33], v[148:151], v[188:191], v[30:33]
	v_mfma_f32_16x16x32_bf16 v[46:49], v[148:151], v[180:183], v[46:49]
	v_mfma_f32_16x16x32_bf16 v[46:49], v[152:155], v[184:187], v[46:49]
	v_mfma_f32_16x16x32_bf16 v[58:61], v[152:155], v[176:179], v[58:61]
	v_mfma_f32_16x16x32_bf16 v[58:61], v[148:151], v[172:175], v[58:61]
	s_setprio 0
	s_setprio 1
	v_mfma_f32_16x16x32_bf16 v[42:45], v[164:167], v[172:175], v[42:45]
	v_mfma_f32_16x16x32_bf16 v[42:45], v[168:171], v[176:179], v[42:45]
	v_mfma_f32_16x16x32_bf16 v[26:29], v[168:171], v[184:187], v[26:29]
	v_mfma_f32_16x16x32_bf16 v[26:29], v[164:167], v[180:183], v[26:29]
	v_mfma_f32_16x16x32_bf16 v[10:13], v[164:167], v[188:191], v[10:13]
	v_mfma_f32_16x16x32_bf16 v[10:13], v[168:171], v[192:195], v[10:13]
	v_mfma_f32_16x16x32_bf16 v[2:5], v[168:171], v[200:203], v[2:5]
	v_mfma_f32_16x16x32_bf16 v[2:5], v[164:167], v[196:199], v[2:5]
	v_mfma_f32_16x16x32_bf16 v[6:9], v[156:159], v[196:199], v[6:9]
	v_mfma_f32_16x16x32_bf16 v[6:9], v[160:163], v[200:203], v[6:9]
	v_mfma_f32_16x16x32_bf16 v[22:25], v[160:163], v[192:195], v[22:25]
	v_mfma_f32_16x16x32_bf16 v[22:25], v[156:159], v[188:191], v[22:25]
	v_mfma_f32_16x16x32_bf16 v[38:41], v[156:159], v[180:183], v[38:41]
	v_mfma_f32_16x16x32_bf16 v[38:41], v[160:163], v[184:187], v[38:41]
	v_mfma_f32_16x16x32_bf16 v[54:57], v[160:163], v[176:179], v[54:57]
	v_mfma_f32_16x16x32_bf16 v[54:57], v[156:159], v[172:175], v[54:57]
	s_setprio 0
	s_barrier
; #define PG8_STAGE(bufoff, gbase, voff) do { const char* _gb = (const char*)(gbase); asm volatile("" : "+s"(_gb)); _Pragma("unroll") for (int _i = 0; _i < 2; ++_i) \
;         __builtin_amdgcn_global_load_lds((const unsigned*)(_gb + (voff)[_i]), (PG8_LAS unsigned*)(lds + (bufoff) + ldsw + _i * 8192), 16, 0, 0); } while (0)
; #define PG8_LDA(dst, b, h) do { _Pragma("unroll") for (int m = 0; m < 4; ++m) _Pragma("unroll") for (int k = 0; k < 2; ++k) dst[m][k] = *(const PG8_LAS bf16x8*)(lds + PG8_SA(b, h) + aoff + m * 2048 + k * 1024); } while (0)
; #define PG8_LDB(dst, b, h) do { _Pragma("unroll") for (int n = 0; n < 2; ++n) _Pragma("unroll") for (int k = 0; k < 2; ++k) dst[n][k] = *(const PG8_LAS bf16x8*)(lds + PG8_SB(b, h) + boff + n * 2048 + k * 1024); } while (0)
; #define PG8_MMA(ai, bj, At, Bt) do { __builtin_amdgcn_s_setprio(1); _Pragma("unroll") for (int m = 0; m < 4; ++m) _Pragma("unroll") for (int n = 0; n < 2; ++n) _Pragma("unroll") for (int k = 0; k < 2; ++k) \
;         acc[ai][bj][m][n] = __builtin_amdgcn_mfma_f32_16x16x32_bf16(Bt[n][k], At[m][k], acc[ai][bj][m][n], 0, 0, 0); __builtin_amdgcn_s_setprio(0); } while (0)
; #define PG8_WAIT_V(n) asm volatile("s_waitcnt vmcnt(" #n ")" ::: "memory")
; #define PG8_WAIT_L(n) asm volatile("s_waitcnt lgkmcnt(" #n ")" ::: "memory")
; #define PG8_BAR __builtin_amdgcn_s_barrier()
; #define PG8_SCHED __builtin_amdgcn_sched_barrier(0)
; template <class Epi, class Sched, bool ALIGN_EPI = false, bool SP2 = false, bool HALFM = false>
; __device__ __forceinline__ void gemm_phase(PG8_LAS unsigned char* lds, const Gemm g, const Sched& S, const Epi& E) {
;     ...
;             PG8_LDB(B0, 1, 0); PG8_LDB(B1, 1, 1); PG8_SCHED; PG8_LDA(At, 1, 0); PG8_STAGE(PG8_SA(0, 1), a2 + hstepA, voffA);
;             PG8_WAIT_V8R; PG8_WAIT_L(0); PG8_BAR; PG8_MMA(0, 0, At, B0); PG8_MMA(0, 1, At, B1); PG8_BAR; PG8_SCHED;
;             if constexpr (!HALFM) { PG8_LDA(At, 1, 1); } PG8_STAGE(PG8_SB(1, 0), b3, voffB); PG8_STAGE(PG8_SB(1, 1), b3 + hstep, voffB); PG8_STAGE(PG8_SA(1, 0), a3, voffA);
;             PG8_WAIT_V(8); PG8_WAIT_L(0); PG8_BAR; if constexpr (!HALFM) { PG8_MMA(1, 0, At, B0); PG8_MMA(1, 1, At, B1); } PG8_BAR; PG8_SCHED;
;             PG8_STAGE(PG8_SA(1, 1), a3 + hstepA, voffA);
	s_add_i32 s62, 0, 0x18000
	v_add_u32_e32 v147, s62, v140
	s_add_i32 s63, 0, 0x1c000
	ds_read_b128 v[132:135], v147
	ds_read_b128 v[136:139], v147 offset:1024
	ds_read_b128 v[148:151], v147 offset:2048
	ds_read_b128 v[152:155], v147 offset:3072
	v_add_u32_e32 v147, s63, v140
	ds_read_b128 v[156:159], v147
	ds_read_b128 v[160:163], v147 offset:1024
	ds_read_b128 v[164:167], v147 offset:2048
	ds_read_b128 v[168:171], v147 offset:3072
	s_add_u32 s60, s4, 0x4000
	s_addc_u32 s61, s5, 0
	s_mov_b32 m0, s42
	ds_read_b128 v[172:175], v145 offset:32768
	ds_read_b128 v[176:179], v145 offset:33792
	ds_read_b128 v[180:183], v145 offset:34816
	ds_read_b128 v[184:187], v145 offset:35840
	ds_read_b128 v[188:191], v145 offset:36864
	ds_read_b128 v[192:195], v145 offset:37888
	ds_read_b128 v[196:199], v145 offset:38912
	ds_read_b128 v[200:203], v145 offset:39936
	s_nop 0
	global_load_lds_dwordx4 v130, s[60:61]
	s_mov_b32 m0, s43
	s_nop 0
	global_load_lds_dwordx4 v142, s[60:61]
	s_waitcnt vmcnt(8)
	s_waitcnt lgkmcnt(0)
	s_barrier
	s_setprio 1
	s_waitcnt lgkmcnt(0)
	v_mfma_f32_16x16x32_bf16 v[126:129], v[132:135], v[172:175], v[126:129]
	v_mfma_f32_16x16x32_bf16 v[126:129], v[136:139], v[176:179], v[126:129]
	v_mfma_f32_16x16x32_bf16 v[118:121], v[136:139], v[184:187], v[118:121]
	v_mfma_f32_16x16x32_bf16 v[118:121], v[132:135], v[180:183], v[118:121]
	v_mfma_f32_16x16x32_bf16 v[106:109], v[132:135], v[188:191], v[106:109]
	v_mfma_f32_16x16x32_bf16 v[106:109], v[136:139], v[192:195], v[106:109]
	v_mfma_f32_16x16x32_bf16 v[82:85], v[136:139], v[200:203], v[82:85]
	v_mfma_f32_16x16x32_bf16 v[82:85], v[132:135], v[196:199], v[82:85]
	v_mfma_f32_16x16x32_bf16 v[78:81], v[148:151], v[196:199], v[78:81]
	v_mfma_f32_16x16x32_bf16 v[78:81], v[152:155], v[200:203], v[78:81]
	v_mfma_f32_16x16x32_bf16 v[98:101], v[152:155], v[192:195], v[98:101]
	v_mfma_f32_16x16x32_bf16 v[98:101], v[148:151], v[188:191], v[98:101]
	v_mfma_f32_16x16x32_bf16 v[114:117], v[148:151], v[180:183], v[114:117]
	v_mfma_f32_16x16x32_bf16 v[114:117], v[152:155], v[184:187], v[114:117]
	v_mfma_f32_16x16x32_bf16 v[122:125], v[152:155], v[176:179], v[122:125]
	v_mfma_f32_16x16x32_bf16 v[122:125], v[148:151], v[172:175], v[122:125]
	s_setprio 0
	s_setprio 1
	v_mfma_f32_16x16x32_bf16 v[102:105], v[164:167], v[172:175], v[102:105]
	v_mfma_f32_16x16x32_bf16 v[102:105], v[168:171], v[176:179], v[102:105]
	v_mfma_f32_16x16x32_bf16 v[90:93], v[168:171], v[184:187], v[90:93]
	v_mfma_f32_16x16x32_bf16 v[90:93], v[164:167], v[180:183], v[90:93]
	v_mfma_f32_16x16x32_bf16 v[74:77], v[164:167], v[188:191], v[74:77]
	v_mfma_f32_16x16x32_bf16 v[74:77], v[168:171], v[192:195], v[74:77]
	v_mfma_f32_16x16x32_bf16 v[66:69], v[168:171], v[200:203], v[66:69]
	v_mfma_f32_16x16x32_bf16 v[66:69], v[164:167], v[196:199], v[66:69]
	v_mfma_f32_16x16x32_bf16 v[70:73], v[156:159], v[196:199], v[70:73]
	v_mfma_f32_16x16x32_bf16 v[70:73], v[160:163], v[200:203], v[70:73]
	v_mfma_f32_16x16x32_bf16 v[86:89], v[160:163], v[192:195], v[86:89]
	v_mfma_f32_16x16x32_bf16 v[86:89], v[156:159], v[188:191], v[86:89]
	v_mfma_f32_16x16x32_bf16 v[94:97], v[156:159], v[180:183], v[94:97]
	v_mfma_f32_16x16x32_bf16 v[94:97], v[160:163], v[184:187], v[94:97]
	v_mfma_f32_16x16x32_bf16 v[110:113], v[160:163], v[176:179], v[110:113]
	v_mfma_f32_16x16x32_bf16 v[110:113], v[156:159], v[172:175], v[110:113]
	s_setprio 0
	s_barrier
	s_add_u32 s60, s30, 0x8000
	s_addc_u32 s61, s31, 0
	s_add_i32 s62, s62, s39
	s_mov_b32 m0, s62
	ds_read_b128 v[172:175], v145 offset:49152
	ds_read_b128 v[176:179], v145 offset:50176
	ds_read_b128 v[180:183], v145 offset:51200
	ds_read_b128 v[184:187], v145 offset:52224
	ds_read_b128 v[188:191], v145 offset:53248
	ds_read_b128 v[192:195], v145 offset:54272
	ds_read_b128 v[196:199], v145 offset:55296
	ds_read_b128 v[200:203], v145 offset:56320
	s_nop 0
	global_load_lds_dwordx4 v130, s[60:61]
	s_add_i32 m0, s62, 0x2000
	s_add_u32 s30, s30, 0xc000
	global_load_lds_dwordx4 v142, s[60:61]
	s_addc_u32 s31, s31, 0
	s_add_i32 s60, s63, s39
	s_mov_b32 m0, s60
	s_nop 0
	global_load_lds_dwordx4 v130, s[30:31]
	s_add_i32 m0, s60, 0x2000
	s_nop 0
	global_load_lds_dwordx4 v142, s[30:31]
	s_mov_b32 m0, s44
	s_nop 0
	global_load_lds_dwordx4 v130, s[6:7]
	s_mov_b32 m0, s45
	s_nop 0
	global_load_lds_dwordx4 v142, s[6:7]
	s_waitcnt vmcnt(8)
	s_waitcnt lgkmcnt(0)
	s_barrier
	s_setprio 1
	s_waitcnt lgkmcnt(0)
	v_mfma_f32_16x16x32_bf16 v[62:65], v[132:135], v[172:175], v[62:65]
	v_mfma_f32_16x16x32_bf16 v[62:65], v[136:139], v[176:179], v[62:65]
	v_mfma_f32_16x16x32_bf16 v[50:53], v[136:139], v[184:187], v[50:53]
	v_mfma_f32_16x16x32_bf16 v[50:53], v[132:135], v[180:183], v[50:53]
	v_mfma_f32_16x16x32_bf16 v[34:37], v[132:135], v[188:191], v[34:37]
	v_mfma_f32_16x16x32_bf16 v[34:37], v[136:139], v[192:195], v[34:37]
	v_mfma_f32_16x16x32_bf16 v[18:21], v[136:139], v[200:203], v[18:21]
	v_mfma_f32_16x16x32_bf16 v[18:21], v[132:135], v[196:199], v[18:21]
	v_mfma_f32_16x16x32_bf16 v[14:17], v[148:151], v[196:199], v[14:17]
	v_mfma_f32_16x16x32_bf16 v[14:17], v[152:155], v[200:203], v[14:17]
	v_mfma_f32_16x16x32_bf16 v[30:33], v[152:155], v[192:195], v[30:33]
	v_mfma_f32_16x16x32_bf16 v[30:33], v[148:151], v[188:191], v[30:33]
	v_mfma_f32_16x16x32_bf16 v[46:49], v[148:151], v[180:183], v[46:49]
	v_mfma_f32_16x16x32_bf16 v[46:49], v[152:155], v[184:187], v[46:49]
	v_mfma_f32_16x16x32_bf16 v[58:61], v[152:155], v[176:179], v[58:61]
	v_mfma_f32_16x16x32_bf16 v[58:61], v[148:151], v[172:175], v[58:61]
	s_setprio 0
	s_setprio 1
	v_mfma_f32_16x16x32_bf16 v[42:45], v[164:167], v[172:175], v[42:45]
	v_mfma_f32_16x16x32_bf16 v[42:45], v[168:171], v[176:179], v[42:45]
	v_mfma_f32_16x16x32_bf16 v[26:29], v[168:171], v[184:187], v[26:29]
	v_mfma_f32_16x16x32_bf16 v[26:29], v[164:167], v[180:183], v[26:29]
	v_mfma_f32_16x16x32_bf16 v[10:13], v[164:167], v[188:191], v[10:13]
	v_mfma_f32_16x16x32_bf16 v[10:13], v[168:171], v[192:195], v[10:13]
	v_mfma_f32_16x16x32_bf16 v[2:5], v[168:171], v[200:203], v[2:5]
	v_mfma_f32_16x16x32_bf16 v[2:5], v[164:167], v[196:199], v[2:5]
	v_mfma_f32_16x16x32_bf16 v[6:9], v[156:159], v[196:199], v[6:9]
	v_mfma_f32_16x16x32_bf16 v[6:9], v[160:163], v[200:203], v[6:9]
	v_mfma_f32_16x16x32_bf16 v[22:25], v[160:163], v[192:195], v[22:25]
	v_mfma_f32_16x16x32_bf16 v[22:25], v[156:159], v[188:191], v[22:25]
	v_mfma_f32_16x16x32_bf16 v[38:41], v[156:159], v[180:183], v[38:41]
	v_mfma_f32_16x16x32_bf16 v[38:41], v[160:163], v[184:187], v[38:41]
	v_mfma_f32_16x16x32_bf16 v[54:57], v[160:163], v[176:179], v[54:57]
	v_mfma_f32_16x16x32_bf16 v[54:57], v[156:159], v[172:175], v[54:57]
	s_setprio 0
	s_barrier
	s_add_u32 s4, s4, 0xc000
	s_mov_b32 m0, s46
	s_addc_u32 s5, s5, 0
	s_add_i32 s59, s59, 2
	global_load_lds_dwordx4 v130, s[4:5]
	s_mov_b32 m0, s47
	s_add_u32 s55, s55, 0x10000
	global_load_lds_dwordx4 v142, s[4:5]
	s_addc_u32 s56, s56, 0
	s_add_u32 s57, s57, 0x10000
	s_addc_u32 s58, s58, 0
	s_cmp_gt_u32 s59, 61
	s_cbranch_scc0 .LBB0_918
	s_and_b64 vcc, exec, s[16:17]
	s_cbranch_vccz .LBB0_921
	s_barrier

; #define LAS __attribute__((address_space(3)))
; #define LAS __attribute__((address_space(3)))
;     LAS unsigned* scr = (LAS unsigned*)(lds + wave * 16384);
;     WItem d0, d1; WRegs R0, R1;
;     constexpr int KB_ = DM / 32;
;     constexpr int NALL = EARLY ? KB_ * (INW / 128) : KB_ * (DM / 128) + KB_ * (CW / 128) + KB_ * (2 * CW / 128) + (CW / 32) * (DM / 128) + KB_ * (DFF2 / 128) + (DFF / 32) * (DM / 128);
;     const int hi_all = it_hi < NALL ? it_hi : NALL, total = hi_all - it_lo, nwgs = NGW / NWAVES, chunk = (((total + nwgs - 1) / nwgs) + NWAVES - 1) / NWAVES * NWAVES;
;     int it = it_lo + (gw / NWAVES) * chunk + (gw % NWAVES); const int wend0 = it_lo + (gw / NWAVES + 1) * chunk, wend = wend0 < hi_all ? wend0 : hi_all;
; __global__ void __launch_bounds__(NWAVES * 64, 2) mk_fwd(Args args) {
;     ...
;         { pg8::Gemm g{(const bf16*)(ws + WS_MB), (const bf16*)(ws + WS_WQKV) + (size_t)CW * DM, BATCH * NMEM, 2 * CW, DM, DM}; pg8::StaticOrder S; S.init(BATCH * NMEM, 2 * CW, G, (bx + G / 2) % G);
;           pg8::EpiScaleF32 E{(float*)(ws + WS_CKV), 2 * CW, (const float*)(ws + WS_SSQM)};
;           pg8::gemm_phase<pg8::EpiScaleF32, pg8::StaticOrder, true, true>(lds, g, S, E); }
;         if (CONV_OVERLAP && G >= 192 && bx >= G / 2 + 8) { __syncthreads(); convert_weights<false, true>(P, lds, (bx - (G / 2 + 8)) * NWAVES + wave, (G - (G / 2 + 8)) * NWAVES, wave, lane, LATE_SPLIT, 0x7fffffff); }
.LBB0_925:
	s_cmpk_lt_i32 s2, 0x88
	s_cbranch_scc1 .Lp6_hook_done
	s_cmp_lg_u32 s80, 0x100
	s_cbranch_scc1 .Lp6_hook_done
	s_cmp_gt_i32 s74, 4
	s_cbranch_scc1 .Lp6_hook_done
	s_cmp_lt_i32 s75, 7
	s_cbranch_scc1 .Lp6_hook_done
	v_writelane_b32 v255, s8, 8
	v_writelane_b32 v255, s9, 9
	v_writelane_b32 v255, s12, 10
	v_writelane_b32 v255, s16, 11
	v_writelane_b32 v255, s18, 12
	v_writelane_b32 v255, s19, 13
	v_writelane_b32 v255, s20, 14
	v_writelane_b32 v255, s21, 15
	v_writelane_b32 v255, s23, 16
	v_writelane_b32 v255, s24, 17
	v_writelane_b32 v255, s26, 18
	v_writelane_b32 v255, s34, 19
	v_readlane_b32 s70, v254, 0
	v_readlane_b32 s71, v254, 1
	v_and_b32_e32 v1, 63, v0
	v_readfirstlane_b32 s101, v0
	s_sub_u32 s100, s2, 0x88
	s_lshl_b32 s100, s100, 3
	s_sub_u32 s70, s70, 0xc0
	s_subb_u32 s71, s71, 0
	s_lshr_b32 s101, s101, 6
	s_add_u32 s101, s101, s100
	s_mov_b32 s100, 120
	s_mov_b32 s0, 0x2b00
	v_writelane_b32 v255, s0, 2
	s_mov_b32 s0, 0x6e00
	v_writelane_b32 v255, s0, 3
	s_mov_b32 s98, 1
	s_mov_b32 s99, 1
	s_mov_b64 s[4:5], -1
	s_branch .Lp4_conv_entry

; #define PG8_STAGE(bufoff, gbase, voff) do { const char* _gb = (const char*)(gbase); asm volatile("" : "+s"(_gb)); _Pragma("unroll") for (int _i = 0; _i < 2; ++_i) \
;         __builtin_amdgcn_global_load_lds((const unsigned*)(_gb + (voff)[_i]), (PG8_LAS unsigned*)(lds + (bufoff) + ldsw + _i * 8192), 16, 0, 0); } while (0)
; #define PG8_LDA(dst, b, h) do { _Pragma("unroll") for (int m = 0; m < 4; ++m) _Pragma("unroll") for (int k = 0; k < 2; ++k) dst[m][k] = *(const PG8_LAS bf16x8*)(lds + PG8_SA(b, h) + aoff + m * 2048 + k * 1024); } while (0)
; #define PG8_MMA(ai, bj, At, Bt) do { __builtin_amdgcn_s_setprio(1); _Pragma("unroll") for (int m = 0; m < 4; ++m) _Pragma("unroll") for (int n = 0; n < 2; ++n) _Pragma("unroll") for (int k = 0; k < 2; ++k) \
;         acc[ai][bj][m][n] = __builtin_amdgcn_mfma_f32_16x16x32_bf16(Bt[n][k], At[m][k], acc[ai][bj][m][n], 0, 0, 0); __builtin_amdgcn_s_setprio(0); } while (0)
; #define PG8_WAIT_L(n) asm volatile("s_waitcnt lgkmcnt(" #n ")" ::: "memory")
; #define PG8_BAR __builtin_amdgcn_s_barrier()
; #define PG8_SCHED __builtin_amdgcn_sched_barrier(0)
; template <class Epi, class Sched, bool ALIGN_EPI = false, bool SP2 = false, bool HALFM = false>
; __device__ __forceinline__ void gemm_phase(PG8_LAS unsigned char* lds, const Gemm g, const Sched& S, const Epi& E) {
;     ...
;             PG8_WAIT_V8R; PG8_WAIT_L(0); PG8_BAR; PG8_MMA(0, 0, At, B0); PG8_MMA(0, 1, At, B1); PG8_BAR; PG8_SCHED;
;             if constexpr (!HALFM) { PG8_LDA(At, 0, 1); } PG8_STAGE(PG8_SB(0, 0), b2, voffB); PG8_STAGE(PG8_SB(0, 1), b2 + hstep, voffB); PG8_STAGE(PG8_SA(0, 0), a2, voffA);
;             PG8_WAIT_V8R; PG8_WAIT_L(0); PG8_BAR; if constexpr (!HALFM) { PG8_MMA(1, 0, At, B0); PG8_MMA(1, 1, At, B1); } PG8_BAR; PG8_SCHED;
.Lry6:
	s_waitcnt lgkmcnt(0)
	s_barrier
	s_setprio 1
	s_waitcnt lgkmcnt(0)
	v_mfma_f32_16x16x32_bf16 v[126:129], v[130:133], v[162:165], v[126:129]
	v_mfma_f32_16x16x32_bf16 v[126:129], v[134:137], v[166:169], v[126:129]
	v_mfma_f32_16x16x32_bf16 v[110:113], v[134:137], v[178:181], v[110:113]
	v_mfma_f32_16x16x32_bf16 v[110:113], v[130:133], v[174:177], v[110:113]
	v_mfma_f32_16x16x32_bf16 v[94:97], v[130:133], v[182:185], v[94:97]
	v_mfma_f32_16x16x32_bf16 v[94:97], v[134:137], v[186:189], v[94:97]
	v_mfma_f32_16x16x32_bf16 v[78:81], v[134:137], v[194:197], v[78:81]
	v_mfma_f32_16x16x32_bf16 v[78:81], v[130:133], v[190:193], v[78:81]
	v_mfma_f32_16x16x32_bf16 v[74:77], v[138:141], v[190:193], v[74:77]
	v_mfma_f32_16x16x32_bf16 v[74:77], v[142:145], v[194:197], v[74:77]
	v_mfma_f32_16x16x32_bf16 v[90:93], v[142:145], v[186:189], v[90:93]
	v_mfma_f32_16x16x32_bf16 v[90:93], v[138:141], v[182:185], v[90:93]
	v_mfma_f32_16x16x32_bf16 v[106:109], v[138:141], v[174:177], v[106:109]
	v_mfma_f32_16x16x32_bf16 v[106:109], v[142:145], v[178:181], v[106:109]
	v_mfma_f32_16x16x32_bf16 v[122:125], v[142:145], v[166:169], v[122:125]
	v_mfma_f32_16x16x32_bf16 v[122:125], v[138:141], v[162:165], v[122:125]
	s_setprio 0
	s_setprio 1
	v_mfma_f32_16x16x32_bf16 v[114:117], v[154:157], v[162:165], v[114:117]
	v_mfma_f32_16x16x32_bf16 v[114:117], v[158:161], v[166:169], v[114:117]
	v_mfma_f32_16x16x32_bf16 v[98:101], v[158:161], v[178:181], v[98:101]
	v_mfma_f32_16x16x32_bf16 v[98:101], v[154:157], v[174:177], v[98:101]
	v_mfma_f32_16x16x32_bf16 v[82:85], v[154:157], v[182:185], v[82:85]
	v_mfma_f32_16x16x32_bf16 v[82:85], v[158:161], v[186:189], v[82:85]
	v_mfma_f32_16x16x32_bf16 v[66:69], v[158:161], v[194:197], v[66:69]
	v_mfma_f32_16x16x32_bf16 v[66:69], v[154:157], v[190:193], v[66:69]
	v_mfma_f32_16x16x32_bf16 v[70:73], v[146:149], v[190:193], v[70:73]
	v_mfma_f32_16x16x32_bf16 v[70:73], v[150:153], v[194:197], v[70:73]
	v_mfma_f32_16x16x32_bf16 v[86:89], v[150:153], v[186:189], v[86:89]
	v_mfma_f32_16x16x32_bf16 v[86:89], v[146:149], v[182:185], v[86:89]
	v_mfma_f32_16x16x32_bf16 v[102:105], v[146:149], v[174:177], v[102:105]
	v_mfma_f32_16x16x32_bf16 v[102:105], v[150:153], v[178:181], v[102:105]
	v_mfma_f32_16x16x32_bf16 v[118:121], v[150:153], v[166:169], v[118:121]
	v_mfma_f32_16x16x32_bf16 v[118:121], v[146:149], v[162:165], v[118:121]
	s_setprio 0
	s_barrier
	s_add_i32 s69, s54, s3
	s_mov_b64 s[66:67], s[34:35]
	s_mov_b32 m0, s69
	ds_read_b128 v[162:165], v211 offset:16384
	ds_read_b128 v[166:169], v211 offset:17408
	ds_read_b128 v[174:177], v211 offset:18432
	ds_read_b128 v[178:181], v211 offset:19456
	ds_read_b128 v[182:185], v211 offset:20480
	ds_read_b128 v[186:189], v211 offset:21504
	ds_read_b128 v[190:193], v211 offset:22528
	ds_read_b128 v[194:197], v211 offset:23552
	s_nop 0
	global_load_lds_dwordx4 v170, s[66:67]
	s_add_i32 m0, s69, 0x2000
	s_nop 0
	global_load_lds_dwordx4 v171, s[66:67]
	s_add_u32 s66, s34, 0x4000
	s_addc_u32 s67, s35, 0
	s_add_i32 s69, s55, s3
	s_mov_b32 m0, s69
	s_nop 0
	global_load_lds_dwordx4 v170, s[66:67]
	s_add_i32 m0, s69, 0x2000
	s_nop 0
	global_load_lds_dwordx4 v171, s[66:67]
	s_mov_b64 s[66:67], s[28:29]
	s_mov_b32 m0, s25
	s_nop 0
	global_load_lds_dwordx4 v170, s[66:67]
	s_mov_b32 m0, s27
	s_nop 0
	global_load_lds_dwordx4 v171, s[66:67]
	s_cmp_eq_u32 s68, 0
	s_cbranch_scc1 .Lrx7
	s_waitcnt vmcnt(40)
	s_branch .Lry7

; #define PG8_STAGE(bufoff, gbase, voff) do { const char* _gb = (const char*)(gbase); asm volatile("" : "+s"(_gb)); _Pragma("unroll") for (int _i = 0; _i < 2; ++_i) \
;         __builtin_amdgcn_global_load_lds((const unsigned*)(_gb + (voff)[_i]), (PG8_LAS unsigned*)(lds + (bufoff) + ldsw + _i * 8192), 16, 0, 0); } while (0)
; #define PG8_LDA(dst, b, h) do { _Pragma("unroll") for (int m = 0; m < 4; ++m) _Pragma("unroll") for (int k = 0; k < 2; ++k) dst[m][k] = *(const PG8_LAS bf16x8*)(lds + PG8_SA(b, h) + aoff + m * 2048 + k * 1024); } while (0)
; #define PG8_LDB(dst, b, h) do { _Pragma("unroll") for (int n = 0; n < 2; ++n) _Pragma("unroll") for (int k = 0; k < 2; ++k) dst[n][k] = *(const PG8_LAS bf16x8*)(lds + PG8_SB(b, h) + boff + n * 2048 + k * 1024); } while (0)
; #define PG8_MMA(ai, bj, At, Bt) do { __builtin_amdgcn_s_setprio(1); _Pragma("unroll") for (int m = 0; m < 4; ++m) _Pragma("unroll") for (int n = 0; n < 2; ++n) _Pragma("unroll") for (int k = 0; k < 2; ++k) \
;         acc[ai][bj][m][n] = __builtin_amdgcn_mfma_f32_16x16x32_bf16(Bt[n][k], At[m][k], acc[ai][bj][m][n], 0, 0, 0); __builtin_amdgcn_s_setprio(0); } while (0)
; #define PG8_WAIT_L(n) asm volatile("s_waitcnt lgkmcnt(" #n ")" ::: "memory")
; #define PG8_BAR __builtin_amdgcn_s_barrier()
; #define PG8_SCHED __builtin_amdgcn_sched_barrier(0)
; template <class Epi, class Sched, bool ALIGN_EPI = false, bool SP2 = false, bool HALFM = false>
; __device__ __forceinline__ void gemm_phase(PG8_LAS unsigned char* lds, const Gemm g, const Sched& S, const Epi& E) {
;     ...
;             PG8_WAIT_V8R; PG8_WAIT_L(0); PG8_BAR; if constexpr (!HALFM) { PG8_MMA(1, 0, At, B0); PG8_MMA(1, 1, At, B1); } PG8_BAR; PG8_SCHED;
;             PG8_LDB(B0, 1, 0); PG8_LDB(B1, 1, 1); PG8_SCHED; PG8_LDA(At, 1, 0); PG8_STAGE(PG8_SA(0, 1), a2 + hstepA, voffA);
;             PG8_WAIT_V8R; PG8_WAIT_L(0); PG8_BAR; PG8_MMA(0, 0, At, B0); PG8_MMA(0, 1, At, B1); PG8_BAR; PG8_SCHED;
.Lry7:
	s_waitcnt lgkmcnt(0)
	s_barrier
	s_setprio 1
	s_waitcnt lgkmcnt(0)
	v_mfma_f32_16x16x32_bf16 v[62:65], v[130:133], v[162:165], v[62:65]
	v_mfma_f32_16x16x32_bf16 v[62:65], v[134:137], v[166:169], v[62:65]
	v_mfma_f32_16x16x32_bf16 v[46:49], v[134:137], v[178:181], v[46:49]
	v_mfma_f32_16x16x32_bf16 v[46:49], v[130:133], v[174:177], v[46:49]
	v_mfma_f32_16x16x32_bf16 v[30:33], v[130:133], v[182:185], v[30:33]
	v_mfma_f32_16x16x32_bf16 v[30:33], v[134:137], v[186:189], v[30:33]
	v_mfma_f32_16x16x32_bf16 v[14:17], v[134:137], v[194:197], v[14:17]
	v_mfma_f32_16x16x32_bf16 v[14:17], v[130:133], v[190:193], v[14:17]
	v_mfma_f32_16x16x32_bf16 v[10:13], v[138:141], v[190:193], v[10:13]
	v_mfma_f32_16x16x32_bf16 v[10:13], v[142:145], v[194:197], v[10:13]
	v_mfma_f32_16x16x32_bf16 v[26:29], v[142:145], v[186:189], v[26:29]
	v_mfma_f32_16x16x32_bf16 v[26:29], v[138:141], v[182:185], v[26:29]
	v_mfma_f32_16x16x32_bf16 v[42:45], v[138:141], v[174:177], v[42:45]
	v_mfma_f32_16x16x32_bf16 v[42:45], v[142:145], v[178:181], v[42:45]
	v_mfma_f32_16x16x32_bf16 v[58:61], v[142:145], v[166:169], v[58:61]
	v_mfma_f32_16x16x32_bf16 v[58:61], v[138:141], v[162:165], v[58:61]
	s_setprio 0
	s_setprio 1
	v_mfma_f32_16x16x32_bf16 v[50:53], v[154:157], v[162:165], v[50:53]
	v_mfma_f32_16x16x32_bf16 v[50:53], v[158:161], v[166:169], v[50:53]
	v_mfma_f32_16x16x32_bf16 v[34:37], v[158:161], v[178:181], v[34:37]
	v_mfma_f32_16x16x32_bf16 v[34:37], v[154:157], v[174:177], v[34:37]
	v_mfma_f32_16x16x32_bf16 v[18:21], v[154:157], v[182:185], v[18:21]
	v_mfma_f32_16x16x32_bf16 v[18:21], v[158:161], v[186:189], v[18:21]
	v_mfma_f32_16x16x32_bf16 v[2:5], v[158:161], v[194:197], v[2:5]
	v_mfma_f32_16x16x32_bf16 v[2:5], v[154:157], v[190:193], v[2:5]
	v_mfma_f32_16x16x32_bf16 v[6:9], v[146:149], v[190:193], v[6:9]
	v_mfma_f32_16x16x32_bf16 v[6:9], v[150:153], v[194:197], v[6:9]
	v_mfma_f32_16x16x32_bf16 v[22:25], v[150:153], v[186:189], v[22:25]
	v_mfma_f32_16x16x32_bf16 v[22:25], v[146:149], v[182:185], v[22:25]
	v_mfma_f32_16x16x32_bf16 v[38:41], v[146:149], v[174:177], v[38:41]
	v_mfma_f32_16x16x32_bf16 v[38:41], v[150:153], v[178:181], v[38:41]
	v_mfma_f32_16x16x32_bf16 v[54:57], v[150:153], v[166:169], v[54:57]
	v_mfma_f32_16x16x32_bf16 v[54:57], v[146:149], v[162:165], v[54:57]
	s_setprio 0
	s_barrier
	s_add_i32 s69, 0, 0x18000
	s_add_i32 s70, 0, 0x1c000
	v_add_u32_e32 v142, s69, v206
	v_add_u32_e32 v158, s70, v206
	ds_read_b128 v[130:133], v142
	ds_read_b128 v[134:137], v142 offset:1024
	ds_read_b128 v[138:141], v142 offset:2048
	ds_read_b128 v[142:145], v142 offset:3072
	ds_read_b128 v[146:149], v158
	ds_read_b128 v[150:153], v158 offset:1024
	ds_read_b128 v[154:157], v158 offset:2048
	ds_read_b128 v[158:161], v158 offset:3072
	s_add_u32 s66, s28, 0x4000
	s_addc_u32 s67, s29, 0
	s_mov_b32 m0, s39
	ds_read_b128 v[162:165], v211 offset:32768
	ds_read_b128 v[166:169], v211 offset:33792
	ds_read_b128 v[174:177], v211 offset:34816
	ds_read_b128 v[178:181], v211 offset:35840
	ds_read_b128 v[182:185], v211 offset:36864
	ds_read_b128 v[186:189], v211 offset:37888
	ds_read_b128 v[190:193], v211 offset:38912
	ds_read_b128 v[194:197], v211 offset:39936
	s_nop 0
	global_load_lds_dwordx4 v170, s[66:67]
	s_mov_b32 m0, s40
	s_nop 0
	global_load_lds_dwordx4 v171, s[66:67]
	s_cmp_eq_u32 s68, 0
	s_cbranch_scc1 .Lrx8
	s_waitcnt vmcnt(40)
	s_branch .Lry8

; #define PG8_STAGE(bufoff, gbase, voff) do { const char* _gb = (const char*)(gbase); asm volatile("" : "+s"(_gb)); _Pragma("unroll") for (int _i = 0; _i < 2; ++_i) \
;         __builtin_amdgcn_global_load_lds((const unsigned*)(_gb + (voff)[_i]), (PG8_LAS unsigned*)(lds + (bufoff) + ldsw + _i * 8192), 16, 0, 0); } while (0)
; #define PG8_LDA(dst, b, h) do { _Pragma("unroll") for (int m = 0; m < 4; ++m) _Pragma("unroll") for (int k = 0; k < 2; ++k) dst[m][k] = *(const PG8_LAS bf16x8*)(lds + PG8_SA(b, h) + aoff + m * 2048 + k * 1024); } while (0)
; #define PG8_MMA(ai, bj, At, Bt) do { __builtin_amdgcn_s_setprio(1); _Pragma("unroll") for (int m = 0; m < 4; ++m) _Pragma("unroll") for (int n = 0; n < 2; ++n) _Pragma("unroll") for (int k = 0; k < 2; ++k) \
;         acc[ai][bj][m][n] = __builtin_amdgcn_mfma_f32_16x16x32_bf16(Bt[n][k], At[m][k], acc[ai][bj][m][n], 0, 0, 0); __builtin_amdgcn_s_setprio(0); } while (0)
; #define PG8_WAIT_V(n) asm volatile("s_waitcnt vmcnt(" #n ")" ::: "memory")
; #define PG8_WAIT_L(n) asm volatile("s_waitcnt lgkmcnt(" #n ")" ::: "memory")
; #define PG8_BAR __builtin_amdgcn_s_barrier()
; #define PG8_SCHED __builtin_amdgcn_sched_barrier(0)
; template <class Epi, class Sched, bool ALIGN_EPI = false, bool SP2 = false, bool HALFM = false>
; __device__ __forceinline__ void gemm_phase(PG8_LAS unsigned char* lds, const Gemm g, const Sched& S, const Epi& E) {
;     ...
;             PG8_WAIT_V8R; PG8_WAIT_L(0); PG8_BAR; PG8_MMA(0, 0, At, B0); PG8_MMA(0, 1, At, B1); PG8_BAR; PG8_SCHED;
;             if constexpr (!HALFM) { PG8_LDA(At, 1, 1); } PG8_STAGE(PG8_SB(1, 0), b3, voffB); PG8_STAGE(PG8_SB(1, 1), b3 + hstep, voffB); PG8_STAGE(PG8_SA(1, 0), a3, voffA);
;             PG8_WAIT_V(8); PG8_WAIT_L(0); PG8_BAR; if constexpr (!HALFM) { PG8_MMA(1, 0, At, B0); PG8_MMA(1, 1, At, B1); } PG8_BAR; PG8_SCHED;
;             PG8_STAGE(PG8_SA(1, 1), a3 + hstepA, voffA);
.Lry8:
	s_waitcnt lgkmcnt(0)
	s_barrier
	s_setprio 1
	s_waitcnt lgkmcnt(0)
	v_mfma_f32_16x16x32_bf16 v[126:129], v[130:133], v[162:165], v[126:129]
	v_mfma_f32_16x16x32_bf16 v[126:129], v[134:137], v[166:169], v[126:129]
	v_mfma_f32_16x16x32_bf16 v[110:113], v[134:137], v[178:181], v[110:113]
	v_mfma_f32_16x16x32_bf16 v[110:113], v[130:133], v[174:177], v[110:113]
	v_mfma_f32_16x16x32_bf16 v[94:97], v[130:133], v[182:185], v[94:97]
	v_mfma_f32_16x16x32_bf16 v[94:97], v[134:137], v[186:189], v[94:97]
	v_mfma_f32_16x16x32_bf16 v[78:81], v[134:137], v[194:197], v[78:81]
	v_mfma_f32_16x16x32_bf16 v[78:81], v[130:133], v[190:193], v[78:81]
	v_mfma_f32_16x16x32_bf16 v[74:77], v[138:141], v[190:193], v[74:77]
	v_mfma_f32_16x16x32_bf16 v[74:77], v[142:145], v[194:197], v[74:77]
	v_mfma_f32_16x16x32_bf16 v[90:93], v[142:145], v[186:189], v[90:93]
	v_mfma_f32_16x16x32_bf16 v[90:93], v[138:141], v[182:185], v[90:93]
	v_mfma_f32_16x16x32_bf16 v[106:109], v[138:141], v[174:177], v[106:109]
	v_mfma_f32_16x16x32_bf16 v[106:109], v[142:145], v[178:181], v[106:109]
	v_mfma_f32_16x16x32_bf16 v[122:125], v[142:145], v[166:169], v[122:125]
	v_mfma_f32_16x16x32_bf16 v[122:125], v[138:141], v[162:165], v[122:125]
	s_setprio 0
	s_setprio 1
	v_mfma_f32_16x16x32_bf16 v[114:117], v[154:157], v[162:165], v[114:117]
	v_mfma_f32_16x16x32_bf16 v[114:117], v[158:161], v[166:169], v[114:117]
	v_mfma_f32_16x16x32_bf16 v[98:101], v[158:161], v[178:181], v[98:101]
	v_mfma_f32_16x16x32_bf16 v[98:101], v[154:157], v[174:177], v[98:101]
	v_mfma_f32_16x16x32_bf16 v[82:85], v[154:157], v[182:185], v[82:85]
	v_mfma_f32_16x16x32_bf16 v[82:85], v[158:161], v[186:189], v[82:85]
	v_mfma_f32_16x16x32_bf16 v[66:69], v[158:161], v[194:197], v[66:69]
	v_mfma_f32_16x16x32_bf16 v[66:69], v[154:157], v[190:193], v[66:69]
	v_mfma_f32_16x16x32_bf16 v[70:73], v[146:149], v[190:193], v[70:73]
	v_mfma_f32_16x16x32_bf16 v[70:73], v[150:153], v[194:197], v[70:73]
	v_mfma_f32_16x16x32_bf16 v[86:89], v[150:153], v[186:189], v[86:89]
	v_mfma_f32_16x16x32_bf16 v[86:89], v[146:149], v[182:185], v[86:89]
	v_mfma_f32_16x16x32_bf16 v[102:105], v[146:149], v[174:177], v[102:105]
	v_mfma_f32_16x16x32_bf16 v[102:105], v[150:153], v[178:181], v[102:105]
	v_mfma_f32_16x16x32_bf16 v[118:121], v[150:153], v[166:169], v[118:121]
	v_mfma_f32_16x16x32_bf16 v[118:121], v[146:149], v[162:165], v[118:121]
	s_setprio 0
	s_barrier
	s_add_u32 s66, s34, 0x8000
	s_addc_u32 s67, s35, 0
	s_add_i32 s68, s69, s3
	s_mov_b32 m0, s68
	ds_read_b128 v[162:165], v211 offset:49152
	ds_read_b128 v[166:169], v211 offset:50176
	ds_read_b128 v[174:177], v211 offset:51200
	ds_read_b128 v[178:181], v211 offset:52224
	ds_read_b128 v[182:185], v211 offset:53248
	ds_read_b128 v[186:189], v211 offset:54272
	ds_read_b128 v[190:193], v211 offset:55296
	ds_read_b128 v[194:197], v211 offset:56320
	s_nop 0
	global_load_lds_dwordx4 v170, s[66:67]
	s_add_i32 m0, s68, 0x2000
	s_add_u32 s34, s34, 0xc000
	global_load_lds_dwordx4 v171, s[66:67]
	s_addc_u32 s35, s35, 0
	s_add_i32 s66, s70, s3
	s_mov_b32 m0, s66
	s_nop 0
	global_load_lds_dwordx4 v170, s[34:35]
	s_add_i32 m0, s66, 0x2000
	s_nop 0
	global_load_lds_dwordx4 v171, s[34:35]
	s_mov_b32 m0, s45
	s_nop 0
	global_load_lds_dwordx4 v170, s[30:31]
	s_mov_b32 m0, s46
	s_nop 0
	global_load_lds_dwordx4 v171, s[30:31]
	s_waitcnt vmcnt(8)
	s_waitcnt lgkmcnt(0)
	s_barrier
	s_setprio 1
	s_waitcnt lgkmcnt(0)
	v_mfma_f32_16x16x32_bf16 v[62:65], v[130:133], v[162:165], v[62:65]
	v_mfma_f32_16x16x32_bf16 v[62:65], v[134:137], v[166:169], v[62:65]
	v_mfma_f32_16x16x32_bf16 v[46:49], v[134:137], v[178:181], v[46:49]
	v_mfma_f32_16x16x32_bf16 v[46:49], v[130:133], v[174:177], v[46:49]
	v_mfma_f32_16x16x32_bf16 v[30:33], v[130:133], v[182:185], v[30:33]
	v_mfma_f32_16x16x32_bf16 v[30:33], v[134:137], v[186:189], v[30:33]
	v_mfma_f32_16x16x32_bf16 v[14:17], v[134:137], v[194:197], v[14:17]
	v_mfma_f32_16x16x32_bf16 v[14:17], v[130:133], v[190:193], v[14:17]
	v_mfma_f32_16x16x32_bf16 v[10:13], v[138:141], v[190:193], v[10:13]
	v_mfma_f32_16x16x32_bf16 v[10:13], v[142:145], v[194:197], v[10:13]
	v_mfma_f32_16x16x32_bf16 v[26:29], v[142:145], v[186:189], v[26:29]
	v_mfma_f32_16x16x32_bf16 v[26:29], v[138:141], v[182:185], v[26:29]
	v_mfma_f32_16x16x32_bf16 v[42:45], v[138:141], v[174:177], v[42:45]
	v_mfma_f32_16x16x32_bf16 v[42:45], v[142:145], v[178:181], v[42:45]
	v_mfma_f32_16x16x32_bf16 v[58:61], v[142:145], v[166:169], v[58:61]
	v_mfma_f32_16x16x32_bf16 v[58:61], v[138:141], v[162:165], v[58:61]
	s_setprio 0
	s_setprio 1
	v_mfma_f32_16x16x32_bf16 v[50:53], v[154:157], v[162:165], v[50:53]
	v_mfma_f32_16x16x32_bf16 v[50:53], v[158:161], v[166:169], v[50:53]
	v_mfma_f32_16x16x32_bf16 v[34:37], v[158:161], v[178:181], v[34:37]
	v_mfma_f32_16x16x32_bf16 v[34:37], v[154:157], v[174:177], v[34:37]
	v_mfma_f32_16x16x32_bf16 v[18:21], v[154:157], v[182:185], v[18:21]
	v_mfma_f32_16x16x32_bf16 v[18:21], v[158:161], v[186:189], v[18:21]
	v_mfma_f32_16x16x32_bf16 v[2:5], v[158:161], v[194:197], v[2:5]
	v_mfma_f32_16x16x32_bf16 v[2:5], v[154:157], v[190:193], v[2:5]
	v_mfma_f32_16x16x32_bf16 v[6:9], v[146:149], v[190:193], v[6:9]
	v_mfma_f32_16x16x32_bf16 v[6:9], v[150:153], v[194:197], v[6:9]
	v_mfma_f32_16x16x32_bf16 v[22:25], v[150:153], v[186:189], v[22:25]
	v_mfma_f32_16x16x32_bf16 v[22:25], v[146:149], v[182:185], v[22:25]
	v_mfma_f32_16x16x32_bf16 v[38:41], v[146:149], v[174:177], v[38:41]
	v_mfma_f32_16x16x32_bf16 v[38:41], v[150:153], v[178:181], v[38:41]
	v_mfma_f32_16x16x32_bf16 v[54:57], v[150:153], v[166:169], v[54:57]
	v_mfma_f32_16x16x32_bf16 v[54:57], v[146:149], v[162:165], v[54:57]
	s_setprio 0
	s_barrier
	s_add_u32 s28, s28, 0xc000
	s_mov_b32 m0, s47
	s_addc_u32 s29, s29, 0
	s_add_i32 s65, s65, 2
	global_load_lds_dwordx4 v170, s[28:29]
	s_mov_b32 m0, s48
	s_add_u32 s61, s61, 0x10000
	global_load_lds_dwordx4 v171, s[28:29]
	s_addc_u32 s62, s62, 0
	s_add_u32 s63, s63, 0x10000
	s_addc_u32 s64, s64, 0
	s_cmp_gt_u32 s65, 5
	s_cbranch_scc0 .LBB0_1079
	s_and_b64 vcc, exec, s[12:13]
	s_cbranch_vccz .LBB0_1082
	s_barrier

; #define PG8_STAGE(bufoff, gbase, voff) do { const char* _gb = (const char*)(gbase); asm volatile("" : "+s"(_gb)); _Pragma("unroll") for (int _i = 0; _i < 2; ++_i) \
;         __builtin_amdgcn_global_load_lds((const unsigned*)(_gb + (voff)[_i]), (PG8_LAS unsigned*)(lds + (bufoff) + ldsw + _i * 8192), 16, 0, 0); } while (0)
; #define PG8_LDA(dst, b, h) do { _Pragma("unroll") for (int m = 0; m < 4; ++m) _Pragma("unroll") for (int k = 0; k < 2; ++k) dst[m][k] = *(const PG8_LAS bf16x8*)(lds + PG8_SA(b, h) + aoff + m * 2048 + k * 1024); } while (0)
; #define PG8_MMA(ai, bj, At, Bt) do { __builtin_amdgcn_s_setprio(1); _Pragma("unroll") for (int m = 0; m < 4; ++m) _Pragma("unroll") for (int n = 0; n < 2; ++n) _Pragma("unroll") for (int k = 0; k < 2; ++k) \
;         acc[ai][bj][m][n] = __builtin_amdgcn_mfma_f32_16x16x32_bf16(Bt[n][k], At[m][k], acc[ai][bj][m][n], 0, 0, 0); __builtin_amdgcn_s_setprio(0); } while (0)
; #define PG8_WAIT_L(n) asm volatile("s_waitcnt lgkmcnt(" #n ")" ::: "memory")
; #define PG8_BAR __builtin_amdgcn_s_barrier()
; #define PG8_SCHED __builtin_amdgcn_sched_barrier(0)
; template <class Epi, class Sched, bool ALIGN_EPI = false, bool SP2 = false, bool HALFM = false>
; __device__ __forceinline__ void gemm_phase(PG8_LAS unsigned char* lds, const Gemm g, const Sched& S, const Epi& E) {
;     ...
;             PG8_WAIT_V8R; PG8_WAIT_L(0); PG8_BAR; PG8_MMA(0, 0, At, B0); PG8_MMA(0, 1, At, B1); PG8_BAR; PG8_SCHED;
;             if constexpr (!HALFM) { PG8_LDA(At, 0, 1); } PG8_STAGE(PG8_SB(0, 0), b2, voffB); PG8_STAGE(PG8_SB(0, 1), b2 + hstep, voffB); PG8_STAGE(PG8_SA(0, 0), a2, voffA);
;             PG8_WAIT_V8R; PG8_WAIT_L(0); PG8_BAR; if constexpr (!HALFM) { PG8_MMA(1, 0, At, B0); PG8_MMA(1, 1, At, B1); } PG8_BAR; PG8_SCHED;
.Lry9:
	s_waitcnt lgkmcnt(0)
	s_barrier
	s_setprio 1
	s_waitcnt lgkmcnt(0)
	v_mfma_f32_16x16x32_bf16 v[126:129], v[134:137], v[180:183], v[126:129]
	v_mfma_f32_16x16x32_bf16 v[126:129], v[138:141], v[184:187], v[126:129]
	v_mfma_f32_16x16x32_bf16 v[122:125], v[138:141], v[192:195], v[122:125]
	v_mfma_f32_16x16x32_bf16 v[122:125], v[134:137], v[188:191], v[122:125]
	v_mfma_f32_16x16x32_bf16 v[118:121], v[134:137], v[196:199], v[118:121]
	v_mfma_f32_16x16x32_bf16 v[118:121], v[138:141], v[200:203], v[118:121]
	v_mfma_f32_16x16x32_bf16 v[114:117], v[138:141], v[218:221], v[114:117]
	v_mfma_f32_16x16x32_bf16 v[114:117], v[134:137], v[204:207], v[114:117]
	v_mfma_f32_16x16x32_bf16 v[50:53], v[142:145], v[204:207], v[50:53]
	v_mfma_f32_16x16x32_bf16 v[50:53], v[160:163], v[218:221], v[50:53]
	v_mfma_f32_16x16x32_bf16 v[54:57], v[160:163], v[200:203], v[54:57]
	v_mfma_f32_16x16x32_bf16 v[54:57], v[142:145], v[196:199], v[54:57]
	v_mfma_f32_16x16x32_bf16 v[58:61], v[142:145], v[188:191], v[58:61]
	v_mfma_f32_16x16x32_bf16 v[58:61], v[160:163], v[192:195], v[58:61]
	v_mfma_f32_16x16x32_bf16 v[66:69], v[160:163], v[184:187], v[66:69]
	v_mfma_f32_16x16x32_bf16 v[66:69], v[142:145], v[180:183], v[66:69]
	s_setprio 0
	s_setprio 1
	v_mfma_f32_16x16x32_bf16 v[46:49], v[172:175], v[180:183], v[46:49]
	v_mfma_f32_16x16x32_bf16 v[46:49], v[176:179], v[184:187], v[46:49]
	v_mfma_f32_16x16x32_bf16 v[42:45], v[176:179], v[192:195], v[42:45]
	v_mfma_f32_16x16x32_bf16 v[42:45], v[172:175], v[188:191], v[42:45]
	v_mfma_f32_16x16x32_bf16 v[38:41], v[172:175], v[196:199], v[38:41]
	v_mfma_f32_16x16x32_bf16 v[38:41], v[176:179], v[200:203], v[38:41]
	v_mfma_f32_16x16x32_bf16 v[34:37], v[176:179], v[218:221], v[34:37]
	v_mfma_f32_16x16x32_bf16 v[34:37], v[172:175], v[204:207], v[34:37]
	v_mfma_f32_16x16x32_bf16 v[98:101], v[164:167], v[204:207], v[98:101]
	v_mfma_f32_16x16x32_bf16 v[98:101], v[168:171], v[218:221], v[98:101]
	v_mfma_f32_16x16x32_bf16 v[102:105], v[168:171], v[200:203], v[102:105]
	v_mfma_f32_16x16x32_bf16 v[102:105], v[164:167], v[196:199], v[102:105]
	v_mfma_f32_16x16x32_bf16 v[106:109], v[164:167], v[188:191], v[106:109]
	v_mfma_f32_16x16x32_bf16 v[106:109], v[168:171], v[192:195], v[106:109]
	v_mfma_f32_16x16x32_bf16 v[110:113], v[168:171], v[184:187], v[110:113]
	v_mfma_f32_16x16x32_bf16 v[110:113], v[164:167], v[180:183], v[110:113]
	s_setprio 0
	s_barrier
	s_add_i32 vcc_lo, s81, s60
	s_mov_b64 s[96:97], s[46:47]
	s_mov_b32 m0, vcc_lo
	ds_read_b128 v[180:183], v214 offset:16384
	ds_read_b128 v[184:187], v214 offset:17408
	ds_read_b128 v[188:191], v214 offset:18432
	ds_read_b128 v[192:195], v214 offset:19456
	ds_read_b128 v[196:199], v214 offset:20480
	ds_read_b128 v[200:203], v214 offset:21504
	ds_read_b128 v[204:207], v214 offset:22528
	ds_read_b128 v[218:221], v214 offset:23552
	s_nop 0
	global_load_lds_dwordx4 v217, s[96:97]
	s_add_i32 m0, vcc_lo, 0x2000
	s_nop 0
	global_load_lds_dwordx4 v216, s[96:97]
	s_add_u32 s96, s46, 0x4000
	s_addc_u32 s97, s47, 0
	s_add_i32 vcc_lo, s86, s60
	s_mov_b32 m0, vcc_lo
	s_nop 0
	global_load_lds_dwordx4 v217, s[96:97]
	s_add_i32 m0, vcc_lo, 0x2000
	s_nop 0
	global_load_lds_dwordx4 v216, s[96:97]
	s_mov_b64 s[96:97], s[4:5]
	s_mov_b32 m0, s61
	s_nop 0
	global_load_lds_dwordx4 v217, s[96:97]
	s_mov_b32 m0, s62
	s_nop 0
	global_load_lds_dwordx4 v216, s[96:97]
	s_cmp_eq_u32 s95, 0
	s_cbranch_scc1 .Lrx10
	s_waitcnt vmcnt(20)
	s_branch .Lry10

; #define PG8_STAGE(bufoff, gbase, voff) do { const char* _gb = (const char*)(gbase); asm volatile("" : "+s"(_gb)); _Pragma("unroll") for (int _i = 0; _i < 2; ++_i) \
;         __builtin_amdgcn_global_load_lds((const unsigned*)(_gb + (voff)[_i]), (PG8_LAS unsigned*)(lds + (bufoff) + ldsw + _i * 8192), 16, 0, 0); } while (0)
; #define PG8_LDA(dst, b, h) do { _Pragma("unroll") for (int m = 0; m < 4; ++m) _Pragma("unroll") for (int k = 0; k < 2; ++k) dst[m][k] = *(const PG8_LAS bf16x8*)(lds + PG8_SA(b, h) + aoff + m * 2048 + k * 1024); } while (0)
; #define PG8_LDB(dst, b, h) do { _Pragma("unroll") for (int n = 0; n < 2; ++n) _Pragma("unroll") for (int k = 0; k < 2; ++k) dst[n][k] = *(const PG8_LAS bf16x8*)(lds + PG8_SB(b, h) + boff + n * 2048 + k * 1024); } while (0)
; #define PG8_MMA(ai, bj, At, Bt) do { __builtin_amdgcn_s_setprio(1); _Pragma("unroll") for (int m = 0; m < 4; ++m) _Pragma("unroll") for (int n = 0; n < 2; ++n) _Pragma("unroll") for (int k = 0; k < 2; ++k) \
;         acc[ai][bj][m][n] = __builtin_amdgcn_mfma_f32_16x16x32_bf16(Bt[n][k], At[m][k], acc[ai][bj][m][n], 0, 0, 0); __builtin_amdgcn_s_setprio(0); } while (0)
; #define PG8_WAIT_L(n) asm volatile("s_waitcnt lgkmcnt(" #n ")" ::: "memory")
; #define PG8_BAR __builtin_amdgcn_s_barrier()
; #define PG8_SCHED __builtin_amdgcn_sched_barrier(0)
; template <class Epi, class Sched, bool ALIGN_EPI = false, bool SP2 = false, bool HALFM = false>
; __device__ __forceinline__ void gemm_phase(PG8_LAS unsigned char* lds, const Gemm g, const Sched& S, const Epi& E) {
;     ...
;             PG8_WAIT_V8R; PG8_WAIT_L(0); PG8_BAR; if constexpr (!HALFM) { PG8_MMA(1, 0, At, B0); PG8_MMA(1, 1, At, B1); } PG8_BAR; PG8_SCHED;
;             PG8_LDB(B0, 1, 0); PG8_LDB(B1, 1, 1); PG8_SCHED; PG8_LDA(At, 1, 0); PG8_STAGE(PG8_SA(0, 1), a2 + hstepA, voffA);
;             PG8_WAIT_V8R; PG8_WAIT_L(0); PG8_BAR; PG8_MMA(0, 0, At, B0); PG8_MMA(0, 1, At, B1); PG8_BAR; PG8_SCHED;
.Lry10:
	s_waitcnt lgkmcnt(0)
	s_barrier
	s_setprio 1
	s_waitcnt lgkmcnt(0)
	v_mfma_f32_16x16x32_bf16 v[94:97], v[134:137], v[180:183], v[94:97]
	v_mfma_f32_16x16x32_bf16 v[94:97], v[138:141], v[184:187], v[94:97]
	v_mfma_f32_16x16x32_bf16 v[90:93], v[138:141], v[192:195], v[90:93]
	v_mfma_f32_16x16x32_bf16 v[90:93], v[134:137], v[188:191], v[90:93]
	v_mfma_f32_16x16x32_bf16 v[86:89], v[134:137], v[196:199], v[86:89]
	v_mfma_f32_16x16x32_bf16 v[86:89], v[138:141], v[200:203], v[86:89]
	v_mfma_f32_16x16x32_bf16 v[82:85], v[138:141], v[218:221], v[82:85]
	v_mfma_f32_16x16x32_bf16 v[82:85], v[134:137], v[204:207], v[82:85]
	v_mfma_f32_16x16x32_bf16 v[18:21], v[142:145], v[204:207], v[18:21]
	v_mfma_f32_16x16x32_bf16 v[18:21], v[160:163], v[218:221], v[18:21]
	v_mfma_f32_16x16x32_bf16 v[22:25], v[160:163], v[200:203], v[22:25]
	v_mfma_f32_16x16x32_bf16 v[22:25], v[142:145], v[196:199], v[22:25]
	v_mfma_f32_16x16x32_bf16 v[26:29], v[142:145], v[188:191], v[26:29]
	v_mfma_f32_16x16x32_bf16 v[26:29], v[160:163], v[192:195], v[26:29]
	v_mfma_f32_16x16x32_bf16 v[30:33], v[160:163], v[184:187], v[30:33]
	v_mfma_f32_16x16x32_bf16 v[30:33], v[142:145], v[180:183], v[30:33]
	s_setprio 0
	s_setprio 1
	v_mfma_f32_16x16x32_bf16 v[14:17], v[172:175], v[180:183], v[14:17]
	v_mfma_f32_16x16x32_bf16 v[14:17], v[176:179], v[184:187], v[14:17]
	v_mfma_f32_16x16x32_bf16 v[10:13], v[176:179], v[192:195], v[10:13]
	v_mfma_f32_16x16x32_bf16 v[10:13], v[172:175], v[188:191], v[10:13]
	v_mfma_f32_16x16x32_bf16 v[6:9], v[172:175], v[196:199], v[6:9]
	v_mfma_f32_16x16x32_bf16 v[6:9], v[176:179], v[200:203], v[6:9]
	v_mfma_f32_16x16x32_bf16 v[2:5], v[176:179], v[218:221], v[2:5]
	v_mfma_f32_16x16x32_bf16 v[2:5], v[172:175], v[204:207], v[2:5]
	v_mfma_f32_16x16x32_bf16 v[62:65], v[164:167], v[204:207], v[62:65]
	v_mfma_f32_16x16x32_bf16 v[62:65], v[168:171], v[218:221], v[62:65]
	v_mfma_f32_16x16x32_bf16 v[70:73], v[168:171], v[200:203], v[70:73]
	v_mfma_f32_16x16x32_bf16 v[70:73], v[164:167], v[196:199], v[70:73]
	v_mfma_f32_16x16x32_bf16 v[74:77], v[164:167], v[188:191], v[74:77]
	v_mfma_f32_16x16x32_bf16 v[74:77], v[168:171], v[192:195], v[74:77]
	v_mfma_f32_16x16x32_bf16 v[78:81], v[168:171], v[184:187], v[78:81]
	v_mfma_f32_16x16x32_bf16 v[78:81], v[164:167], v[180:183], v[78:81]
	s_setprio 0
	s_barrier
	s_add_i32 vcc_lo, 0, 0x18000
	v_add_u32_e32 v150, vcc_lo, v147
	s_add_i32 vcc_hi, 0, 0x1c000
	ds_read_b128 v[134:137], v150
	ds_read_b128 v[138:141], v150 offset:1024
	ds_read_b128 v[142:145], v150 offset:2048
	ds_read_b128 v[160:163], v150 offset:3072
	v_add_u32_e32 v150, vcc_hi, v147
	ds_read_b128 v[164:167], v150
	ds_read_b128 v[168:171], v150 offset:1024
	ds_read_b128 v[172:175], v150 offset:2048
	ds_read_b128 v[176:179], v150 offset:3072
	s_add_u32 s96, s4, 0x4000
	s_addc_u32 s97, s5, 0
	s_mov_b32 m0, s63
	ds_read_b128 v[180:183], v214 offset:32768
	ds_read_b128 v[184:187], v214 offset:33792
	ds_read_b128 v[188:191], v214 offset:34816
	ds_read_b128 v[192:195], v214 offset:35840
	ds_read_b128 v[196:199], v214 offset:36864
	ds_read_b128 v[200:203], v214 offset:37888
	ds_read_b128 v[204:207], v214 offset:38912
	ds_read_b128 v[218:221], v214 offset:39936
	s_nop 0
	global_load_lds_dwordx4 v217, s[96:97]
	s_mov_b32 m0, s64
	s_nop 0
	global_load_lds_dwordx4 v216, s[96:97]
	s_cmp_eq_u32 s95, 0
	s_cbranch_scc1 .Lrx11
	s_waitcnt vmcnt(20)
	s_branch .Lry11

; #define PG8_STAGE(bufoff, gbase, voff) do { const char* _gb = (const char*)(gbase); asm volatile("" : "+s"(_gb)); _Pragma("unroll") for (int _i = 0; _i < 2; ++_i) \
;         __builtin_amdgcn_global_load_lds((const unsigned*)(_gb + (voff)[_i]), (PG8_LAS unsigned*)(lds + (bufoff) + ldsw + _i * 8192), 16, 0, 0); } while (0)
; #define PG8_LDA(dst, b, h) do { _Pragma("unroll") for (int m = 0; m < 4; ++m) _Pragma("unroll") for (int k = 0; k < 2; ++k) dst[m][k] = *(const PG8_LAS bf16x8*)(lds + PG8_SA(b, h) + aoff + m * 2048 + k * 1024); } while (0)
; #define PG8_MMA(ai, bj, At, Bt) do { __builtin_amdgcn_s_setprio(1); _Pragma("unroll") for (int m = 0; m < 4; ++m) _Pragma("unroll") for (int n = 0; n < 2; ++n) _Pragma("unroll") for (int k = 0; k < 2; ++k) \
;         acc[ai][bj][m][n] = __builtin_amdgcn_mfma_f32_16x16x32_bf16(Bt[n][k], At[m][k], acc[ai][bj][m][n], 0, 0, 0); __builtin_amdgcn_s_setprio(0); } while (0)
; #define PG8_WAIT_V(n) asm volatile("s_waitcnt vmcnt(" #n ")" ::: "memory")
; #define PG8_WAIT_L(n) asm volatile("s_waitcnt lgkmcnt(" #n ")" ::: "memory")
; #define PG8_BAR __builtin_amdgcn_s_barrier()
; #define PG8_SCHED __builtin_amdgcn_sched_barrier(0)
; template <class Epi, class Sched, bool ALIGN_EPI = false, bool SP2 = false, bool HALFM = false>
; __device__ __forceinline__ void gemm_phase(PG8_LAS unsigned char* lds, const Gemm g, const Sched& S, const Epi& E) {
;     ...
;             PG8_WAIT_V8R; PG8_WAIT_L(0); PG8_BAR; PG8_MMA(0, 0, At, B0); PG8_MMA(0, 1, At, B1); PG8_BAR; PG8_SCHED;
;             if constexpr (!HALFM) { PG8_LDA(At, 1, 1); } PG8_STAGE(PG8_SB(1, 0), b3, voffB); PG8_STAGE(PG8_SB(1, 1), b3 + hstep, voffB); PG8_STAGE(PG8_SA(1, 0), a3, voffA);
;             PG8_WAIT_V(8); PG8_WAIT_L(0); PG8_BAR; if constexpr (!HALFM) { PG8_MMA(1, 0, At, B0); PG8_MMA(1, 1, At, B1); } PG8_BAR; PG8_SCHED;
;             PG8_STAGE(PG8_SA(1, 1), a3 + hstepA, voffA);
.Lry11:
	s_waitcnt lgkmcnt(0)
	s_barrier
	s_setprio 1
	s_waitcnt lgkmcnt(0)
	v_mfma_f32_16x16x32_bf16 v[126:129], v[134:137], v[180:183], v[126:129]
	v_mfma_f32_16x16x32_bf16 v[126:129], v[138:141], v[184:187], v[126:129]
	v_mfma_f32_16x16x32_bf16 v[122:125], v[138:141], v[192:195], v[122:125]
	v_mfma_f32_16x16x32_bf16 v[122:125], v[134:137], v[188:191], v[122:125]
	v_mfma_f32_16x16x32_bf16 v[118:121], v[134:137], v[196:199], v[118:121]
	v_mfma_f32_16x16x32_bf16 v[118:121], v[138:141], v[200:203], v[118:121]
	v_mfma_f32_16x16x32_bf16 v[114:117], v[138:141], v[218:221], v[114:117]
	v_mfma_f32_16x16x32_bf16 v[114:117], v[134:137], v[204:207], v[114:117]
	v_mfma_f32_16x16x32_bf16 v[50:53], v[142:145], v[204:207], v[50:53]
	v_mfma_f32_16x16x32_bf16 v[50:53], v[160:163], v[218:221], v[50:53]
	v_mfma_f32_16x16x32_bf16 v[54:57], v[160:163], v[200:203], v[54:57]
	v_mfma_f32_16x16x32_bf16 v[54:57], v[142:145], v[196:199], v[54:57]
	v_mfma_f32_16x16x32_bf16 v[58:61], v[142:145], v[188:191], v[58:61]
	v_mfma_f32_16x16x32_bf16 v[58:61], v[160:163], v[192:195], v[58:61]
	v_mfma_f32_16x16x32_bf16 v[66:69], v[160:163], v[184:187], v[66:69]
	v_mfma_f32_16x16x32_bf16 v[66:69], v[142:145], v[180:183], v[66:69]
	s_setprio 0
	s_setprio 1
	v_mfma_f32_16x16x32_bf16 v[46:49], v[172:175], v[180:183], v[46:49]
	v_mfma_f32_16x16x32_bf16 v[46:49], v[176:179], v[184:187], v[46:49]
	v_mfma_f32_16x16x32_bf16 v[42:45], v[176:179], v[192:195], v[42:45]
	v_mfma_f32_16x16x32_bf16 v[42:45], v[172:175], v[188:191], v[42:45]
	v_mfma_f32_16x16x32_bf16 v[38:41], v[172:175], v[196:199], v[38:41]
	v_mfma_f32_16x16x32_bf16 v[38:41], v[176:179], v[200:203], v[38:41]
	v_mfma_f32_16x16x32_bf16 v[34:37], v[176:179], v[218:221], v[34:37]
	v_mfma_f32_16x16x32_bf16 v[34:37], v[172:175], v[204:207], v[34:37]
	v_mfma_f32_16x16x32_bf16 v[98:101], v[164:167], v[204:207], v[98:101]
	v_mfma_f32_16x16x32_bf16 v[98:101], v[168:171], v[218:221], v[98:101]
	v_mfma_f32_16x16x32_bf16 v[102:105], v[168:171], v[200:203], v[102:105]
	v_mfma_f32_16x16x32_bf16 v[102:105], v[164:167], v[196:199], v[102:105]
	v_mfma_f32_16x16x32_bf16 v[106:109], v[164:167], v[188:191], v[106:109]
	v_mfma_f32_16x16x32_bf16 v[106:109], v[168:171], v[192:195], v[106:109]
	v_mfma_f32_16x16x32_bf16 v[110:113], v[168:171], v[184:187], v[110:113]
	v_mfma_f32_16x16x32_bf16 v[110:113], v[164:167], v[180:183], v[110:113]
	s_setprio 0
	s_barrier
	s_add_i32 s95, vcc_lo, s60
	s_mov_b32 m0, s95
	ds_read_b128 v[180:183], v214 offset:49152
	ds_read_b128 v[184:187], v214 offset:50176
	ds_read_b128 v[188:191], v214 offset:51200
	ds_read_b128 v[192:195], v214 offset:52224
	ds_read_b128 v[196:199], v214 offset:53248
	ds_read_b128 v[200:203], v214 offset:54272
	ds_read_b128 v[204:207], v214 offset:55296
	ds_read_b128 v[218:221], v214 offset:56320
	s_nop 0
	global_load_lds_dwordx4 v217, s[50:51]
	s_add_i32 m0, s95, 0x2000
	s_add_u32 s46, s46, 0xc000
	global_load_lds_dwordx4 v216, s[50:51]
	s_addc_u32 s47, s47, 0
	s_add_i32 s50, vcc_hi, s60
	s_mov_b32 m0, s50
	s_nop 0
	global_load_lds_dwordx4 v217, s[46:47]
	s_add_i32 m0, s50, 0x2000
	s_nop 0
	global_load_lds_dwordx4 v216, s[46:47]
	s_mov_b32 m0, s67
	s_nop 0
	global_load_lds_dwordx4 v217, s[48:49]
	s_mov_b32 m0, s68
	s_nop 0
	global_load_lds_dwordx4 v216, s[48:49]
	s_waitcnt vmcnt(8)
	s_waitcnt lgkmcnt(0)
	s_barrier
	s_setprio 1
	s_waitcnt lgkmcnt(0)
	v_mfma_f32_16x16x32_bf16 v[94:97], v[134:137], v[180:183], v[94:97]
	v_mfma_f32_16x16x32_bf16 v[94:97], v[138:141], v[184:187], v[94:97]
	v_mfma_f32_16x16x32_bf16 v[90:93], v[138:141], v[192:195], v[90:93]
	v_mfma_f32_16x16x32_bf16 v[90:93], v[134:137], v[188:191], v[90:93]
	v_mfma_f32_16x16x32_bf16 v[86:89], v[134:137], v[196:199], v[86:89]
	v_mfma_f32_16x16x32_bf16 v[86:89], v[138:141], v[200:203], v[86:89]
	v_mfma_f32_16x16x32_bf16 v[82:85], v[138:141], v[218:221], v[82:85]
	v_mfma_f32_16x16x32_bf16 v[82:85], v[134:137], v[204:207], v[82:85]
	v_mfma_f32_16x16x32_bf16 v[18:21], v[142:145], v[204:207], v[18:21]
	v_mfma_f32_16x16x32_bf16 v[18:21], v[160:163], v[218:221], v[18:21]
	v_mfma_f32_16x16x32_bf16 v[22:25], v[160:163], v[200:203], v[22:25]
	v_mfma_f32_16x16x32_bf16 v[22:25], v[142:145], v[196:199], v[22:25]
	v_mfma_f32_16x16x32_bf16 v[26:29], v[142:145], v[188:191], v[26:29]
	v_mfma_f32_16x16x32_bf16 v[26:29], v[160:163], v[192:195], v[26:29]
	v_mfma_f32_16x16x32_bf16 v[30:33], v[160:163], v[184:187], v[30:33]
	v_mfma_f32_16x16x32_bf16 v[30:33], v[142:145], v[180:183], v[30:33]
	s_setprio 0
	s_setprio 1
	v_mfma_f32_16x16x32_bf16 v[14:17], v[172:175], v[180:183], v[14:17]
	v_mfma_f32_16x16x32_bf16 v[14:17], v[176:179], v[184:187], v[14:17]
	v_mfma_f32_16x16x32_bf16 v[10:13], v[176:179], v[192:195], v[10:13]
	v_mfma_f32_16x16x32_bf16 v[10:13], v[172:175], v[188:191], v[10:13]
	v_mfma_f32_16x16x32_bf16 v[6:9], v[172:175], v[196:199], v[6:9]
	v_mfma_f32_16x16x32_bf16 v[6:9], v[176:179], v[200:203], v[6:9]
	v_mfma_f32_16x16x32_bf16 v[2:5], v[176:179], v[218:221], v[2:5]
	v_mfma_f32_16x16x32_bf16 v[2:5], v[172:175], v[204:207], v[2:5]
	v_mfma_f32_16x16x32_bf16 v[62:65], v[164:167], v[204:207], v[62:65]
	v_mfma_f32_16x16x32_bf16 v[62:65], v[168:171], v[218:221], v[62:65]
	v_mfma_f32_16x16x32_bf16 v[70:73], v[168:171], v[200:203], v[70:73]
	v_mfma_f32_16x16x32_bf16 v[70:73], v[164:167], v[196:199], v[70:73]
	v_mfma_f32_16x16x32_bf16 v[74:77], v[164:167], v[188:191], v[74:77]
	v_mfma_f32_16x16x32_bf16 v[74:77], v[168:171], v[192:195], v[74:77]
	v_mfma_f32_16x16x32_bf16 v[78:81], v[168:171], v[184:187], v[78:81]
	v_mfma_f32_16x16x32_bf16 v[78:81], v[164:167], v[180:183], v[78:81]
	s_setprio 0
	s_barrier
	s_add_u32 s4, s4, 0xc000
	s_mov_b32 m0, s69
	s_addc_u32 s5, s5, 0
	s_add_i32 s94, s94, 2
	global_load_lds_dwordx4 v217, s[4:5]
	s_mov_b32 m0, s70
	s_add_u32 s13, s13, 0x10000
	global_load_lds_dwordx4 v216, s[4:5]
	s_addc_u32 s15, s15, 0
	s_add_u32 s91, s91, 0x10000
	s_addc_u32 s93, s93, 0
	s_cmp_gt_u32 s94, 61
	s_cbranch_scc1 .LBB0_1175

; #define PG8_STAGE(bufoff, gbase, voff) do { const char* _gb = (const char*)(gbase); asm volatile("" : "+s"(_gb)); _Pragma("unroll") for (int _i = 0; _i < 2; ++_i) \
;         __builtin_amdgcn_global_load_lds((const unsigned*)(_gb + (voff)[_i]), (PG8_LAS unsigned*)(lds + (bufoff) + ldsw + _i * 8192), 16, 0, 0); } while (0)
; #define PG8_LDA(dst, b, h) do { _Pragma("unroll") for (int m = 0; m < 4; ++m) _Pragma("unroll") for (int k = 0; k < 2; ++k) dst[m][k] = *(const PG8_LAS bf16x8*)(lds + PG8_SA(b, h) + aoff + m * 2048 + k * 1024); } while (0)
; #define PG8_LDB(dst, b, h) do { _Pragma("unroll") for (int n = 0; n < 2; ++n) _Pragma("unroll") for (int k = 0; k < 2; ++k) dst[n][k] = *(const PG8_LAS bf16x8*)(lds + PG8_SB(b, h) + boff + n * 2048 + k * 1024); } while (0)
; #define PG8_WAIT_L(n) asm volatile("s_waitcnt lgkmcnt(" #n ")" ::: "memory")
; #define PG8_BAR __builtin_amdgcn_s_barrier()
; #define PG8_SCHED __builtin_amdgcn_sched_barrier(0)
; template <class Epi, class Sched, bool ALIGN_EPI = false, bool SP2 = false, bool HALFM = false>
; __device__ __forceinline__ void gemm_phase(PG8_LAS unsigned char* lds, const Gemm g, const Sched& S, const Epi& E) {
;     ...
;         for (int t = 0; t < nt; t += 2) {
;             const bool last = (t == nt - 2);
;             const char* a1 = cA + (size_t)(t + 1) * kstep;
;             const char* a2 = last ? nA : cA + (size_t)(t + 2) * kstep; const char* b2 = last ? nB : cB + (size_t)(t + 2) * kstep;
;             const char* a3 = a2 + kstep; const char* b3 = b2 + kstep;
;             if (last && has_next) S.a_ready(nxt);
;             if constexpr (Epi::HAS_PREFETCH) { if (last) E.prefetch(cur, wid, lane); }
;             asm volatile("" : "+v"(voffA[0]), "+v"(voffA[1])); voffB[0] = voffA[0]; voffB[1] = voffA[1];
;             if constexpr (SP2) {
;             PG8_LDB(B0, 0, 0); PG8_LDB(B1, 0, 1); PG8_SCHED; PG8_LDA(At, 0, 0);
;             PG8_WAIT_V8R; PG8_WAIT_L(0); PG8_BAR; PG8_MMA(0, 0, At, B0); PG8_MMA(0, 1, At, B1); PG8_BAR; PG8_SCHED;
;             if constexpr (!HALFM) { PG8_LDA(At, 0, 1); } PG8_STAGE(PG8_SB(0, 0), b2, voffB); PG8_STAGE(PG8_SB(0, 1), b2 + hstep, voffB); PG8_STAGE(PG8_SA(0, 0), a2, voffA);
;             PG8_WAIT_V8R; PG8_WAIT_L(0); PG8_BAR; if constexpr (!HALFM) { PG8_MMA(1, 0, At, B0); PG8_MMA(1, 1, At, B1); } PG8_BAR; PG8_SCHED;
.LBB0_1242:
	v_add_u32_e32 v90, s65, v134
	v_add_u32_e32 v106, s66, v134
	ds_read_b128 v[70:73], v90
	ds_read_b128 v[74:77], v90 offset:1024
	ds_read_b128 v[78:81], v90 offset:2048
	ds_read_b128 v[90:93], v90 offset:3072
	ds_read_b128 v[94:97], v106
	ds_read_b128 v[98:101], v106 offset:1024
	ds_read_b128 v[102:105], v106 offset:2048
	ds_read_b128 v[106:109], v106 offset:3072
	s_and_b64 s[14:15], s[14:15], exec
	s_cselect_b32 s14, s70, s5
	s_cselect_b32 s15, s37, s13
	s_cselect_b32 s45, s23, s77
	s_cselect_b32 s44, s71, s76
	s_add_u32 s46, s14, 0x8000
	s_addc_u32 s47, s15, 0
	s_add_u32 s48, s44, 0x8000
	s_addc_u32 s49, s45, 0
	ds_read_b128 v[110:113], v136
	ds_read_b128 v[114:117], v136 offset:1024
	ds_read_b128 v[118:121], v136 offset:2048
	ds_read_b128 v[122:125], v136 offset:3072
	ds_read_b128 v[126:129], v136 offset:4096
	ds_read_b128 v[130:133], v136 offset:5120
	ds_read_b128 v[140:143], v136 offset:6144
	ds_read_b128 v[150:153], v136 offset:7168
	s_waitcnt vmcnt(8)
	s_waitcnt lgkmcnt(0)
	s_barrier
	s_setprio 1
	s_waitcnt lgkmcnt(0)
	v_mfma_f32_16x16x32_bf16 v[62:65], v[70:73], v[110:113], v[62:65]
	v_mfma_f32_16x16x32_bf16 v[62:65], v[74:77], v[114:117], v[62:65]
	v_mfma_f32_16x16x32_bf16 v[58:61], v[74:77], v[122:125], v[58:61]
	v_mfma_f32_16x16x32_bf16 v[58:61], v[70:73], v[118:121], v[58:61]
	v_mfma_f32_16x16x32_bf16 v[54:57], v[70:73], v[126:129], v[54:57]
	v_mfma_f32_16x16x32_bf16 v[54:57], v[74:77], v[130:133], v[54:57]
	v_mfma_f32_16x16x32_bf16 v[50:53], v[74:77], v[150:153], v[50:53]
	v_mfma_f32_16x16x32_bf16 v[50:53], v[70:73], v[140:143], v[50:53]
	v_mfma_f32_16x16x32_bf16 v[18:21], v[78:81], v[140:143], v[18:21]
	v_mfma_f32_16x16x32_bf16 v[18:21], v[90:93], v[150:153], v[18:21]
	v_mfma_f32_16x16x32_bf16 v[22:25], v[90:93], v[130:133], v[22:25]
	v_mfma_f32_16x16x32_bf16 v[22:25], v[78:81], v[126:129], v[22:25]
	v_mfma_f32_16x16x32_bf16 v[26:29], v[78:81], v[118:121], v[26:29]
	v_mfma_f32_16x16x32_bf16 v[26:29], v[90:93], v[122:125], v[26:29]
	v_mfma_f32_16x16x32_bf16 v[30:33], v[90:93], v[114:117], v[30:33]
	v_mfma_f32_16x16x32_bf16 v[30:33], v[78:81], v[110:113], v[30:33]
	s_setprio 0
	s_setprio 1
	v_mfma_f32_16x16x32_bf16 v[14:17], v[102:105], v[110:113], v[14:17]
	v_mfma_f32_16x16x32_bf16 v[14:17], v[106:109], v[114:117], v[14:17]
	v_mfma_f32_16x16x32_bf16 v[10:13], v[106:109], v[122:125], v[10:13]
	v_mfma_f32_16x16x32_bf16 v[10:13], v[102:105], v[118:121], v[10:13]
	v_mfma_f32_16x16x32_bf16 v[6:9], v[102:105], v[126:129], v[6:9]
	v_mfma_f32_16x16x32_bf16 v[6:9], v[106:109], v[130:133], v[6:9]
	v_mfma_f32_16x16x32_bf16 v[2:5], v[106:109], v[150:153], v[2:5]
	v_mfma_f32_16x16x32_bf16 v[2:5], v[102:105], v[140:143], v[2:5]
	v_mfma_f32_16x16x32_bf16 v[34:37], v[94:97], v[140:143], v[34:37]
	v_mfma_f32_16x16x32_bf16 v[34:37], v[98:101], v[150:153], v[34:37]
	v_mfma_f32_16x16x32_bf16 v[38:41], v[98:101], v[130:133], v[38:41]
	v_mfma_f32_16x16x32_bf16 v[38:41], v[94:97], v[126:129], v[38:41]
	v_mfma_f32_16x16x32_bf16 v[42:45], v[94:97], v[118:121], v[42:45]
	v_mfma_f32_16x16x32_bf16 v[42:45], v[98:101], v[122:125], v[42:45]
	v_mfma_f32_16x16x32_bf16 v[46:49], v[98:101], v[114:117], v[46:49]
	v_mfma_f32_16x16x32_bf16 v[46:49], v[94:97], v[110:113], v[46:49]
	s_setprio 0
	s_barrier
	s_add_i32 s88, s65, s3
	s_mov_b64 s[86:87], s[44:45]
	s_mov_b32 m0, s88
	s_nop 0
	global_load_lds_dwordx4 v138, s[86:87]
	s_add_i32 m0, s88, 0x2000
	s_nop 0
	global_load_lds_dwordx4 v149, s[86:87]
	s_add_u32 s86, s44, 0x4000
	s_addc_u32 s87, s45, 0
	s_add_i32 s88, s66, s3
	s_mov_b32 m0, s88
	s_nop 0
	global_load_lds_dwordx4 v138, s[86:87]
	s_add_i32 m0, s88, 0x2000
	s_nop 0
	global_load_lds_dwordx4 v149, s[86:87]
	s_mov_b64 s[86:87], s[14:15]
	s_mov_b32 m0, s33
	s_nop 0
	global_load_lds_dwordx4 v138, s[86:87]
	s_mov_b32 m0, s50
	s_nop 0
	global_load_lds_dwordx4 v149, s[86:87]
	s_waitcnt vmcnt(8)
	s_waitcnt lgkmcnt(0)
	s_barrier
	s_barrier
; #define PG8_STAGE(bufoff, gbase, voff) do { const char* _gb = (const char*)(gbase); asm volatile("" : "+s"(_gb)); _Pragma("unroll") for (int _i = 0; _i < 2; ++_i) \
;         __builtin_amdgcn_global_load_lds((const unsigned*)(_gb + (voff)[_i]), (PG8_LAS unsigned*)(lds + (bufoff) + ldsw + _i * 8192), 16, 0, 0); } while (0)
; #define PG8_LDA(dst, b, h) do { _Pragma("unroll") for (int m = 0; m < 4; ++m) _Pragma("unroll") for (int k = 0; k < 2; ++k) dst[m][k] = *(const PG8_LAS bf16x8*)(lds + PG8_SA(b, h) + aoff + m * 2048 + k * 1024); } while (0)
; #define PG8_LDB(dst, b, h) do { _Pragma("unroll") for (int n = 0; n < 2; ++n) _Pragma("unroll") for (int k = 0; k < 2; ++k) dst[n][k] = *(const PG8_LAS bf16x8*)(lds + PG8_SB(b, h) + boff + n * 2048 + k * 1024); } while (0)
; #define PG8_MMA(ai, bj, At, Bt) do { __builtin_amdgcn_s_setprio(1); _Pragma("unroll") for (int m = 0; m < 4; ++m) _Pragma("unroll") for (int n = 0; n < 2; ++n) _Pragma("unroll") for (int k = 0; k < 2; ++k) \
;         acc[ai][bj][m][n] = __builtin_amdgcn_mfma_f32_16x16x32_bf16(Bt[n][k], At[m][k], acc[ai][bj][m][n], 0, 0, 0); __builtin_amdgcn_s_setprio(0); } while (0)
; #define PG8_WAIT_V(n) asm volatile("s_waitcnt vmcnt(" #n ")" ::: "memory")
; #define PG8_WAIT_L(n) asm volatile("s_waitcnt lgkmcnt(" #n ")" ::: "memory")
; #define PG8_BAR __builtin_amdgcn_s_barrier()
; #define PG8_SCHED __builtin_amdgcn_sched_barrier(0)
; template <class Epi, class Sched, bool ALIGN_EPI = false, bool SP2 = false, bool HALFM = false>
; __device__ __forceinline__ void gemm_phase(PG8_LAS unsigned char* lds, const Gemm g, const Sched& S, const Epi& E) {
;     ...
;             PG8_LDB(B0, 1, 0); PG8_LDB(B1, 1, 1); PG8_SCHED; PG8_LDA(At, 1, 0); PG8_STAGE(PG8_SA(0, 1), a2 + hstepA, voffA);
;             PG8_WAIT_V8R; PG8_WAIT_L(0); PG8_BAR; PG8_MMA(0, 0, At, B0); PG8_MMA(0, 1, At, B1); PG8_BAR; PG8_SCHED;
;             if constexpr (!HALFM) { PG8_LDA(At, 1, 1); } PG8_STAGE(PG8_SB(1, 0), b3, voffB); PG8_STAGE(PG8_SB(1, 1), b3 + hstep, voffB); PG8_STAGE(PG8_SA(1, 0), a3, voffA);
;             PG8_WAIT_V(8); PG8_WAIT_L(0); PG8_BAR; if constexpr (!HALFM) { PG8_MMA(1, 0, At, B0); PG8_MMA(1, 1, At, B1); } PG8_BAR; PG8_SCHED;
;             PG8_STAGE(PG8_SA(1, 1), a3 + hstepA, voffA);
	s_add_i32 s88, 0, 0x18000
	s_add_i32 s89, 0, 0x1c000
	v_add_u32_e32 v90, s88, v134
	v_add_u32_e32 v106, s89, v134
	ds_read_b128 v[70:73], v90
	ds_read_b128 v[74:77], v90 offset:1024
	ds_read_b128 v[78:81], v90 offset:2048
	ds_read_b128 v[90:93], v90 offset:3072
	ds_read_b128 v[94:97], v106
	ds_read_b128 v[98:101], v106 offset:1024
	ds_read_b128 v[102:105], v106 offset:2048
	ds_read_b128 v[106:109], v106 offset:3072
	s_add_u32 s86, s14, 0x4000
	s_addc_u32 s87, s15, 0
	s_mov_b32 m0, s51
	ds_read_b128 v[110:113], v136 offset:32768
	ds_read_b128 v[114:117], v136 offset:33792
	ds_read_b128 v[118:121], v136 offset:34816
	ds_read_b128 v[122:125], v136 offset:35840
	ds_read_b128 v[126:129], v136 offset:36864
	ds_read_b128 v[130:133], v136 offset:37888
	ds_read_b128 v[140:143], v136 offset:38912
	ds_read_b128 v[150:153], v136 offset:39936
	s_nop 0
	global_load_lds_dwordx4 v138, s[86:87]
	s_mov_b32 m0, s56
	s_nop 0
	global_load_lds_dwordx4 v149, s[86:87]
	s_waitcnt vmcnt(8)
	s_waitcnt lgkmcnt(0)
	s_barrier
	s_setprio 1
	s_waitcnt lgkmcnt(0)
	v_mfma_f32_16x16x32_bf16 v[62:65], v[70:73], v[110:113], v[62:65]
	v_mfma_f32_16x16x32_bf16 v[62:65], v[74:77], v[114:117], v[62:65]
	v_mfma_f32_16x16x32_bf16 v[58:61], v[74:77], v[122:125], v[58:61]
	v_mfma_f32_16x16x32_bf16 v[58:61], v[70:73], v[118:121], v[58:61]
	v_mfma_f32_16x16x32_bf16 v[54:57], v[70:73], v[126:129], v[54:57]
	v_mfma_f32_16x16x32_bf16 v[54:57], v[74:77], v[130:133], v[54:57]
	v_mfma_f32_16x16x32_bf16 v[50:53], v[74:77], v[150:153], v[50:53]
	v_mfma_f32_16x16x32_bf16 v[50:53], v[70:73], v[140:143], v[50:53]
	v_mfma_f32_16x16x32_bf16 v[18:21], v[78:81], v[140:143], v[18:21]
	v_mfma_f32_16x16x32_bf16 v[18:21], v[90:93], v[150:153], v[18:21]
	v_mfma_f32_16x16x32_bf16 v[22:25], v[90:93], v[130:133], v[22:25]
	v_mfma_f32_16x16x32_bf16 v[22:25], v[78:81], v[126:129], v[22:25]
	v_mfma_f32_16x16x32_bf16 v[26:29], v[78:81], v[118:121], v[26:29]
	v_mfma_f32_16x16x32_bf16 v[26:29], v[90:93], v[122:125], v[26:29]
	v_mfma_f32_16x16x32_bf16 v[30:33], v[90:93], v[114:117], v[30:33]
	v_mfma_f32_16x16x32_bf16 v[30:33], v[78:81], v[110:113], v[30:33]
	s_setprio 0
	s_setprio 1
	v_mfma_f32_16x16x32_bf16 v[14:17], v[102:105], v[110:113], v[14:17]
	v_mfma_f32_16x16x32_bf16 v[14:17], v[106:109], v[114:117], v[14:17]
	v_mfma_f32_16x16x32_bf16 v[10:13], v[106:109], v[122:125], v[10:13]
	v_mfma_f32_16x16x32_bf16 v[10:13], v[102:105], v[118:121], v[10:13]
	v_mfma_f32_16x16x32_bf16 v[6:9], v[102:105], v[126:129], v[6:9]
	v_mfma_f32_16x16x32_bf16 v[6:9], v[106:109], v[130:133], v[6:9]
	v_mfma_f32_16x16x32_bf16 v[2:5], v[106:109], v[150:153], v[2:5]
	v_mfma_f32_16x16x32_bf16 v[2:5], v[102:105], v[140:143], v[2:5]
	v_mfma_f32_16x16x32_bf16 v[34:37], v[94:97], v[140:143], v[34:37]
	v_mfma_f32_16x16x32_bf16 v[34:37], v[98:101], v[150:153], v[34:37]
	v_mfma_f32_16x16x32_bf16 v[38:41], v[98:101], v[130:133], v[38:41]
	v_mfma_f32_16x16x32_bf16 v[38:41], v[94:97], v[126:129], v[38:41]
	v_mfma_f32_16x16x32_bf16 v[42:45], v[94:97], v[118:121], v[42:45]
	v_mfma_f32_16x16x32_bf16 v[42:45], v[98:101], v[122:125], v[42:45]
	v_mfma_f32_16x16x32_bf16 v[46:49], v[98:101], v[114:117], v[46:49]
	v_mfma_f32_16x16x32_bf16 v[46:49], v[94:97], v[110:113], v[46:49]
	s_setprio 0
	s_barrier
	s_add_i32 s86, s88, s3
	s_mov_b32 m0, s86
	s_nop 0
	global_load_lds_dwordx4 v138, s[48:49]
	s_add_i32 m0, s86, 0x2000
	s_add_u32 s44, s44, 0xc000
	global_load_lds_dwordx4 v149, s[48:49]
	s_addc_u32 s45, s45, 0
	s_add_i32 s48, s89, s3
	s_mov_b32 m0, s48
	s_nop 0
	global_load_lds_dwordx4 v138, s[44:45]
	s_add_i32 m0, s48, 0x2000
	s_nop 0
	global_load_lds_dwordx4 v149, s[44:45]
	s_mov_b32 m0, s59
	s_nop 0
	global_load_lds_dwordx4 v138, s[46:47]
	s_mov_b32 m0, s60
	s_nop 0
	global_load_lds_dwordx4 v149, s[46:47]
	s_waitcnt vmcnt(8)
	s_waitcnt lgkmcnt(0)
	s_barrier
	s_barrier
	s_add_u32 s14, s14, 0xc000
	s_mov_b32 m0, s61
	s_addc_u32 s15, s15, 0
	s_add_i32 s81, s81, 2
	global_load_lds_dwordx4 v138, s[14:15]
	s_mov_b32 m0, s62
	s_add_u32 s5, s5, 0x10000
	global_load_lds_dwordx4 v149, s[14:15]
	s_addc_u32 s13, s13, 0
	s_add_u32 s76, s76, 0x10000
	s_addc_u32 s77, s77, 0
	s_cmp_gt_u32 s81, 61
	s_cbranch_scc1 .LBB0_1246

; #define PG8_STAGE(bufoff, gbase, voff) do { const char* _gb = (const char*)(gbase); asm volatile("" : "+s"(_gb)); _Pragma("unroll") for (int _i = 0; _i < 2; ++_i) \
;         __builtin_amdgcn_global_load_lds((const unsigned*)(_gb + (voff)[_i]), (PG8_LAS unsigned*)(lds + (bufoff) + ldsw + _i * 8192), 16, 0, 0); } while (0)
; #define PG8_LDA(dst, b, h) do { _Pragma("unroll") for (int m = 0; m < 4; ++m) _Pragma("unroll") for (int k = 0; k < 2; ++k) dst[m][k] = *(const PG8_LAS bf16x8*)(lds + PG8_SA(b, h) + aoff + m * 2048 + k * 1024); } while (0)
; #define PG8_MMA(ai, bj, At, Bt) do { __builtin_amdgcn_s_setprio(1); _Pragma("unroll") for (int m = 0; m < 4; ++m) _Pragma("unroll") for (int n = 0; n < 2; ++n) _Pragma("unroll") for (int k = 0; k < 2; ++k) \
;         acc[ai][bj][m][n] = __builtin_amdgcn_mfma_f32_16x16x32_bf16(Bt[n][k], At[m][k], acc[ai][bj][m][n], 0, 0, 0); __builtin_amdgcn_s_setprio(0); } while (0)
; #define PG8_WAIT_L(n) asm volatile("s_waitcnt lgkmcnt(" #n ")" ::: "memory")
; #define PG8_BAR __builtin_amdgcn_s_barrier()
; #define PG8_SCHED __builtin_amdgcn_sched_barrier(0)
; template <class Epi, class Sched, bool ALIGN_EPI = false, bool SP2 = false, bool HALFM = false>
; __device__ __forceinline__ void gemm_phase(PG8_LAS unsigned char* lds, const Gemm g, const Sched& S, const Epi& E) {
;     ...
;             PG8_WAIT_V8R; PG8_WAIT_L(0); PG8_BAR; PG8_MMA(0, 0, At, B0); PG8_MMA(0, 1, At, B1); PG8_BAR; PG8_SCHED;
;             if constexpr (!HALFM) { PG8_LDA(At, 0, 1); } PG8_STAGE(PG8_SB(0, 0), b2, voffB); PG8_STAGE(PG8_SB(0, 1), b2 + hstep, voffB); PG8_STAGE(PG8_SA(0, 0), a2, voffA);
;             PG8_WAIT_V8R; PG8_WAIT_L(0); PG8_BAR; if constexpr (!HALFM) { PG8_MMA(1, 0, At, B0); PG8_MMA(1, 1, At, B1); } PG8_BAR; PG8_SCHED;
.Lry12:
	s_waitcnt lgkmcnt(0)
	s_barrier
	s_setprio 1
	s_waitcnt lgkmcnt(0)
	v_mfma_f32_16x16x32_bf16 v[124:127], v[134:137], v[166:169], v[124:127]
	v_mfma_f32_16x16x32_bf16 v[124:127], v[138:141], v[170:173], v[124:127]
	v_mfma_f32_16x16x32_bf16 v[112:115], v[138:141], v[178:181], v[112:115]
	v_mfma_f32_16x16x32_bf16 v[112:115], v[134:137], v[174:177], v[112:115]
	v_mfma_f32_16x16x32_bf16 v[92:95], v[134:137], v[182:185], v[92:95]
	v_mfma_f32_16x16x32_bf16 v[92:95], v[138:141], v[198:201], v[92:95]
	v_mfma_f32_16x16x32_bf16 v[80:83], v[138:141], v[206:209], v[80:83]
	v_mfma_f32_16x16x32_bf16 v[80:83], v[134:137], v[202:205], v[80:83]
	v_mfma_f32_16x16x32_bf16 v[72:75], v[142:145], v[202:205], v[72:75]
	v_mfma_f32_16x16x32_bf16 v[72:75], v[146:149], v[206:209], v[72:75]
	v_mfma_f32_16x16x32_bf16 v[88:91], v[146:149], v[198:201], v[88:91]
	v_mfma_f32_16x16x32_bf16 v[88:91], v[142:145], v[182:185], v[88:91]
	v_mfma_f32_16x16x32_bf16 v[104:107], v[142:145], v[174:177], v[104:107]
	v_mfma_f32_16x16x32_bf16 v[104:107], v[146:149], v[178:181], v[104:107]
	v_mfma_f32_16x16x32_bf16 v[120:123], v[146:149], v[170:173], v[120:123]
	v_mfma_f32_16x16x32_bf16 v[120:123], v[142:145], v[166:169], v[120:123]
	s_setprio 0
	s_setprio 1
	v_mfma_f32_16x16x32_bf16 v[108:111], v[158:161], v[166:169], v[108:111]
	v_mfma_f32_16x16x32_bf16 v[108:111], v[162:165], v[170:173], v[108:111]
	v_mfma_f32_16x16x32_bf16 v[96:99], v[162:165], v[178:181], v[96:99]
	v_mfma_f32_16x16x32_bf16 v[96:99], v[158:161], v[174:177], v[96:99]
	v_mfma_f32_16x16x32_bf16 v[76:79], v[158:161], v[182:185], v[76:79]
	v_mfma_f32_16x16x32_bf16 v[76:79], v[162:165], v[198:201], v[76:79]
	v_mfma_f32_16x16x32_bf16 v[64:67], v[162:165], v[206:209], v[64:67]
	v_mfma_f32_16x16x32_bf16 v[64:67], v[158:161], v[202:205], v[64:67]
	v_mfma_f32_16x16x32_bf16 v[68:71], v[150:153], v[202:205], v[68:71]
	v_mfma_f32_16x16x32_bf16 v[68:71], v[154:157], v[206:209], v[68:71]
	v_mfma_f32_16x16x32_bf16 v[84:87], v[154:157], v[198:201], v[84:87]
	v_mfma_f32_16x16x32_bf16 v[84:87], v[150:153], v[182:185], v[84:87]
	v_mfma_f32_16x16x32_bf16 v[100:103], v[150:153], v[174:177], v[100:103]
	v_mfma_f32_16x16x32_bf16 v[100:103], v[154:157], v[178:181], v[100:103]
	v_mfma_f32_16x16x32_bf16 v[116:119], v[154:157], v[170:173], v[116:119]
	v_mfma_f32_16x16x32_bf16 v[116:119], v[150:153], v[166:169], v[116:119]
	s_setprio 0
	s_barrier
	s_add_i32 s58, s43, s20
	s_mov_b64 s[56:57], s[18:19]
	s_mov_b32 m0, s58
	ds_read_b128 v[166:169], v196 offset:16384
	ds_read_b128 v[170:173], v196 offset:17408
	ds_read_b128 v[174:177], v196 offset:18432
	ds_read_b128 v[178:181], v196 offset:19456
	ds_read_b128 v[182:185], v196 offset:20480
	ds_read_b128 v[198:201], v196 offset:21504
	ds_read_b128 v[202:205], v196 offset:22528
	ds_read_b128 v[206:209], v196 offset:23552
	s_nop 0
	global_load_lds_dwordx4 v197, s[56:57]
	s_add_i32 m0, s58, 0x2000
	s_nop 0
	global_load_lds_dwordx4 v186, s[56:57]
	s_add_u32 s56, s18, 0x4000
	s_addc_u32 s57, s19, 0
	s_add_i32 s58, s44, s20
	s_mov_b32 m0, s58
	s_nop 0
	global_load_lds_dwordx4 v197, s[56:57]
	s_add_i32 m0, s58, 0x2000
	s_nop 0
	global_load_lds_dwordx4 v186, s[56:57]
	s_mov_b64 s[56:57], s[14:15]
	s_mov_b32 m0, s25
	s_nop 0
	global_load_lds_dwordx4 v197, s[56:57]
	s_mov_b32 m0, s26
	s_nop 0
	global_load_lds_dwordx4 v186, s[56:57]
	s_cmp_eq_u32 s55, 0
	s_cbranch_scc1 .Lrx13
	s_waitcnt vmcnt(56)
	s_branch .Lry13

; #define PG8_STAGE(bufoff, gbase, voff) do { const char* _gb = (const char*)(gbase); asm volatile("" : "+s"(_gb)); _Pragma("unroll") for (int _i = 0; _i < 2; ++_i) \
;         __builtin_amdgcn_global_load_lds((const unsigned*)(_gb + (voff)[_i]), (PG8_LAS unsigned*)(lds + (bufoff) + ldsw + _i * 8192), 16, 0, 0); } while (0)
; #define PG8_LDA(dst, b, h) do { _Pragma("unroll") for (int m = 0; m < 4; ++m) _Pragma("unroll") for (int k = 0; k < 2; ++k) dst[m][k] = *(const PG8_LAS bf16x8*)(lds + PG8_SA(b, h) + aoff + m * 2048 + k * 1024); } while (0)
; #define PG8_LDB(dst, b, h) do { _Pragma("unroll") for (int n = 0; n < 2; ++n) _Pragma("unroll") for (int k = 0; k < 2; ++k) dst[n][k] = *(const PG8_LAS bf16x8*)(lds + PG8_SB(b, h) + boff + n * 2048 + k * 1024); } while (0)
; #define PG8_MMA(ai, bj, At, Bt) do { __builtin_amdgcn_s_setprio(1); _Pragma("unroll") for (int m = 0; m < 4; ++m) _Pragma("unroll") for (int n = 0; n < 2; ++n) _Pragma("unroll") for (int k = 0; k < 2; ++k) \
;         acc[ai][bj][m][n] = __builtin_amdgcn_mfma_f32_16x16x32_bf16(Bt[n][k], At[m][k], acc[ai][bj][m][n], 0, 0, 0); __builtin_amdgcn_s_setprio(0); } while (0)
; #define PG8_WAIT_L(n) asm volatile("s_waitcnt lgkmcnt(" #n ")" ::: "memory")
; #define PG8_BAR __builtin_amdgcn_s_barrier()
; #define PG8_SCHED __builtin_amdgcn_sched_barrier(0)
; template <class Epi, class Sched, bool ALIGN_EPI = false, bool SP2 = false, bool HALFM = false>
; __device__ __forceinline__ void gemm_phase(PG8_LAS unsigned char* lds, const Gemm g, const Sched& S, const Epi& E) {
;     ...
;             PG8_WAIT_V8R; PG8_WAIT_L(0); PG8_BAR; if constexpr (!HALFM) { PG8_MMA(1, 0, At, B0); PG8_MMA(1, 1, At, B1); } PG8_BAR; PG8_SCHED;
;             PG8_LDB(B0, 1, 0); PG8_LDB(B1, 1, 1); PG8_SCHED; PG8_LDA(At, 1, 0); PG8_STAGE(PG8_SA(0, 1), a2 + hstepA, voffA);
;             PG8_WAIT_V8R; PG8_WAIT_L(0); PG8_BAR; PG8_MMA(0, 0, At, B0); PG8_MMA(0, 1, At, B1); PG8_BAR; PG8_SCHED;
.Lry13:
	s_waitcnt lgkmcnt(0)
	s_barrier
	s_setprio 1
	s_waitcnt lgkmcnt(0)
	v_mfma_f32_16x16x32_bf16 v[60:63], v[134:137], v[166:169], v[60:63]
	v_mfma_f32_16x16x32_bf16 v[60:63], v[138:141], v[170:173], v[60:63]
	v_mfma_f32_16x16x32_bf16 v[48:51], v[138:141], v[178:181], v[48:51]
	v_mfma_f32_16x16x32_bf16 v[48:51], v[134:137], v[174:177], v[48:51]
	v_mfma_f32_16x16x32_bf16 v[32:35], v[134:137], v[182:185], v[32:35]
	v_mfma_f32_16x16x32_bf16 v[32:35], v[138:141], v[198:201], v[32:35]
	v_mfma_f32_16x16x32_bf16 v[16:19], v[138:141], v[206:209], v[16:19]
	v_mfma_f32_16x16x32_bf16 v[16:19], v[134:137], v[202:205], v[16:19]
	v_mfma_f32_16x16x32_bf16 v[8:11], v[142:145], v[202:205], v[8:11]
	v_mfma_f32_16x16x32_bf16 v[8:11], v[146:149], v[206:209], v[8:11]
	v_mfma_f32_16x16x32_bf16 v[24:27], v[146:149], v[198:201], v[24:27]
	v_mfma_f32_16x16x32_bf16 v[24:27], v[142:145], v[182:185], v[24:27]
	v_mfma_f32_16x16x32_bf16 v[40:43], v[142:145], v[174:177], v[40:43]
	v_mfma_f32_16x16x32_bf16 v[40:43], v[146:149], v[178:181], v[40:43]
	v_mfma_f32_16x16x32_bf16 v[56:59], v[146:149], v[170:173], v[56:59]
	v_mfma_f32_16x16x32_bf16 v[56:59], v[142:145], v[166:169], v[56:59]
	s_setprio 0
	s_setprio 1
	v_mfma_f32_16x16x32_bf16 v[44:47], v[158:161], v[166:169], v[44:47]
	v_mfma_f32_16x16x32_bf16 v[44:47], v[162:165], v[170:173], v[44:47]
	v_mfma_f32_16x16x32_bf16 v[28:31], v[162:165], v[178:181], v[28:31]
	v_mfma_f32_16x16x32_bf16 v[28:31], v[158:161], v[174:177], v[28:31]
	v_mfma_f32_16x16x32_bf16 v[12:15], v[158:161], v[182:185], v[12:15]
	v_mfma_f32_16x16x32_bf16 v[12:15], v[162:165], v[198:201], v[12:15]
	v_mfma_f32_16x16x32_bf16 v[0:3], v[162:165], v[206:209], v[0:3]
	v_mfma_f32_16x16x32_bf16 v[0:3], v[158:161], v[202:205], v[0:3]
	v_mfma_f32_16x16x32_bf16 v[4:7], v[150:153], v[202:205], v[4:7]
	v_mfma_f32_16x16x32_bf16 v[4:7], v[154:157], v[206:209], v[4:7]
	v_mfma_f32_16x16x32_bf16 v[20:23], v[154:157], v[198:201], v[20:23]
	v_mfma_f32_16x16x32_bf16 v[20:23], v[150:153], v[182:185], v[20:23]
	v_mfma_f32_16x16x32_bf16 v[36:39], v[150:153], v[174:177], v[36:39]
	v_mfma_f32_16x16x32_bf16 v[36:39], v[154:157], v[178:181], v[36:39]
	v_mfma_f32_16x16x32_bf16 v[52:55], v[154:157], v[170:173], v[52:55]
	v_mfma_f32_16x16x32_bf16 v[52:55], v[150:153], v[166:169], v[52:55]
	s_setprio 0
	s_barrier
	s_add_i32 s58, 0, 0x18000
	v_add_u32_e32 v128, s58, v189
	s_add_i32 s59, 0, 0x1c000
	ds_read_b128 v[134:137], v128
	ds_read_b128 v[138:141], v128 offset:1024
	ds_read_b128 v[142:145], v128 offset:2048
	ds_read_b128 v[146:149], v128 offset:3072
	v_add_u32_e32 v128, s59, v189
	ds_read_b128 v[150:153], v128
	ds_read_b128 v[154:157], v128 offset:1024
	ds_read_b128 v[158:161], v128 offset:2048
	ds_read_b128 v[162:165], v128 offset:3072
	s_add_u32 s56, s14, 0x4000
	s_addc_u32 s57, s15, 0
	s_mov_b32 m0, s27
	ds_read_b128 v[166:169], v196 offset:32768
	ds_read_b128 v[170:173], v196 offset:33792
	ds_read_b128 v[174:177], v196 offset:34816
	ds_read_b128 v[178:181], v196 offset:35840
	ds_read_b128 v[182:185], v196 offset:36864
	ds_read_b128 v[198:201], v196 offset:37888
	ds_read_b128 v[202:205], v196 offset:38912
	ds_read_b128 v[206:209], v196 offset:39936
	s_nop 0
	global_load_lds_dwordx4 v197, s[56:57]
	s_mov_b32 m0, s28
	s_nop 0
	global_load_lds_dwordx4 v186, s[56:57]
	s_cmp_eq_u32 s55, 0
	s_cbranch_scc1 .Lrx14
	s_waitcnt vmcnt(56)
	s_branch .Lry14

; #define PG8_STAGE(bufoff, gbase, voff) do { const char* _gb = (const char*)(gbase); asm volatile("" : "+s"(_gb)); _Pragma("unroll") for (int _i = 0; _i < 2; ++_i) \
;         __builtin_amdgcn_global_load_lds((const unsigned*)(_gb + (voff)[_i]), (PG8_LAS unsigned*)(lds + (bufoff) + ldsw + _i * 8192), 16, 0, 0); } while (0)
; #define PG8_LDA(dst, b, h) do { _Pragma("unroll") for (int m = 0; m < 4; ++m) _Pragma("unroll") for (int k = 0; k < 2; ++k) dst[m][k] = *(const PG8_LAS bf16x8*)(lds + PG8_SA(b, h) + aoff + m * 2048 + k * 1024); } while (0)
; #define PG8_MMA(ai, bj, At, Bt) do { __builtin_amdgcn_s_setprio(1); _Pragma("unroll") for (int m = 0; m < 4; ++m) _Pragma("unroll") for (int n = 0; n < 2; ++n) _Pragma("unroll") for (int k = 0; k < 2; ++k) \
;         acc[ai][bj][m][n] = __builtin_amdgcn_mfma_f32_16x16x32_bf16(Bt[n][k], At[m][k], acc[ai][bj][m][n], 0, 0, 0); __builtin_amdgcn_s_setprio(0); } while (0)
; #define PG8_WAIT_V(n) asm volatile("s_waitcnt vmcnt(" #n ")" ::: "memory")
; #define PG8_WAIT_L(n) asm volatile("s_waitcnt lgkmcnt(" #n ")" ::: "memory")
; #define PG8_BAR __builtin_amdgcn_s_barrier()
; #define PG8_SCHED __builtin_amdgcn_sched_barrier(0)
; template <class Epi, class Sched, bool ALIGN_EPI = false, bool SP2 = false, bool HALFM = false>
; __device__ __forceinline__ void gemm_phase(PG8_LAS unsigned char* lds, const Gemm g, const Sched& S, const Epi& E) {
;     ...
;             PG8_WAIT_V8R; PG8_WAIT_L(0); PG8_BAR; PG8_MMA(0, 0, At, B0); PG8_MMA(0, 1, At, B1); PG8_BAR; PG8_SCHED;
;             if constexpr (!HALFM) { PG8_LDA(At, 1, 1); } PG8_STAGE(PG8_SB(1, 0), b3, voffB); PG8_STAGE(PG8_SB(1, 1), b3 + hstep, voffB); PG8_STAGE(PG8_SA(1, 0), a3, voffA);
;             PG8_WAIT_V(8); PG8_WAIT_L(0); PG8_BAR; if constexpr (!HALFM) { PG8_MMA(1, 0, At, B0); PG8_MMA(1, 1, At, B1); } PG8_BAR; PG8_SCHED;
;             PG8_STAGE(PG8_SA(1, 1), a3 + hstepA, voffA);
.Lry14:
	s_waitcnt lgkmcnt(0)
	s_barrier
	s_setprio 1
	s_waitcnt lgkmcnt(0)
	v_mfma_f32_16x16x32_bf16 v[124:127], v[134:137], v[166:169], v[124:127]
	v_mfma_f32_16x16x32_bf16 v[124:127], v[138:141], v[170:173], v[124:127]
	v_mfma_f32_16x16x32_bf16 v[112:115], v[138:141], v[178:181], v[112:115]
	v_mfma_f32_16x16x32_bf16 v[112:115], v[134:137], v[174:177], v[112:115]
	v_mfma_f32_16x16x32_bf16 v[92:95], v[134:137], v[182:185], v[92:95]
	v_mfma_f32_16x16x32_bf16 v[92:95], v[138:141], v[198:201], v[92:95]
	v_mfma_f32_16x16x32_bf16 v[80:83], v[138:141], v[206:209], v[80:83]
	v_mfma_f32_16x16x32_bf16 v[80:83], v[134:137], v[202:205], v[80:83]
	v_mfma_f32_16x16x32_bf16 v[72:75], v[142:145], v[202:205], v[72:75]
	v_mfma_f32_16x16x32_bf16 v[72:75], v[146:149], v[206:209], v[72:75]
	v_mfma_f32_16x16x32_bf16 v[88:91], v[146:149], v[198:201], v[88:91]
	v_mfma_f32_16x16x32_bf16 v[88:91], v[142:145], v[182:185], v[88:91]
	v_mfma_f32_16x16x32_bf16 v[104:107], v[142:145], v[174:177], v[104:107]
	v_mfma_f32_16x16x32_bf16 v[104:107], v[146:149], v[178:181], v[104:107]
	v_mfma_f32_16x16x32_bf16 v[120:123], v[146:149], v[170:173], v[120:123]
	v_mfma_f32_16x16x32_bf16 v[120:123], v[142:145], v[166:169], v[120:123]
	s_setprio 0
	s_setprio 1
	v_mfma_f32_16x16x32_bf16 v[108:111], v[158:161], v[166:169], v[108:111]
	v_mfma_f32_16x16x32_bf16 v[108:111], v[162:165], v[170:173], v[108:111]
	v_mfma_f32_16x16x32_bf16 v[96:99], v[162:165], v[178:181], v[96:99]
	v_mfma_f32_16x16x32_bf16 v[96:99], v[158:161], v[174:177], v[96:99]
	v_mfma_f32_16x16x32_bf16 v[76:79], v[158:161], v[182:185], v[76:79]
	v_mfma_f32_16x16x32_bf16 v[76:79], v[162:165], v[198:201], v[76:79]
	v_mfma_f32_16x16x32_bf16 v[64:67], v[162:165], v[206:209], v[64:67]
	v_mfma_f32_16x16x32_bf16 v[64:67], v[158:161], v[202:205], v[64:67]
	v_mfma_f32_16x16x32_bf16 v[68:71], v[150:153], v[202:205], v[68:71]
	v_mfma_f32_16x16x32_bf16 v[68:71], v[154:157], v[206:209], v[68:71]
	v_mfma_f32_16x16x32_bf16 v[84:87], v[154:157], v[198:201], v[84:87]
	v_mfma_f32_16x16x32_bf16 v[84:87], v[150:153], v[182:185], v[84:87]
	v_mfma_f32_16x16x32_bf16 v[100:103], v[150:153], v[174:177], v[100:103]
	v_mfma_f32_16x16x32_bf16 v[100:103], v[154:157], v[178:181], v[100:103]
	v_mfma_f32_16x16x32_bf16 v[116:119], v[154:157], v[170:173], v[116:119]
	v_mfma_f32_16x16x32_bf16 v[116:119], v[150:153], v[166:169], v[116:119]
	s_setprio 0
	s_barrier
	s_add_u32 s56, s18, 0x8000
	s_addc_u32 s57, s19, 0
	s_add_i32 s55, s58, s20
	s_mov_b32 m0, s55
	ds_read_b128 v[166:169], v196 offset:49152
	ds_read_b128 v[170:173], v196 offset:50176
	ds_read_b128 v[174:177], v196 offset:51200
	ds_read_b128 v[178:181], v196 offset:52224
	ds_read_b128 v[182:185], v196 offset:53248
	ds_read_b128 v[198:201], v196 offset:54272
	ds_read_b128 v[202:205], v196 offset:55296
	ds_read_b128 v[206:209], v196 offset:56320
	s_nop 0
	global_load_lds_dwordx4 v197, s[56:57]
	s_add_i32 m0, s55, 0x2000
	s_add_u32 s18, s18, 0xc000
	s_addc_u32 s19, s19, 0
	s_add_i32 s55, s59, s20
	global_load_lds_dwordx4 v186, s[56:57]
	s_mov_b32 m0, s55
	s_nop 0
	global_load_lds_dwordx4 v197, s[18:19]
	s_add_i32 m0, s55, 0x2000
	s_nop 0
	global_load_lds_dwordx4 v186, s[18:19]
	s_mov_b32 m0, s34
	s_nop 0
	global_load_lds_dwordx4 v197, s[16:17]
	s_mov_b32 m0, s35
	s_nop 0
	global_load_lds_dwordx4 v186, s[16:17]
	s_waitcnt vmcnt(8)
	s_waitcnt lgkmcnt(0)
	s_barrier
	s_setprio 1
	s_waitcnt lgkmcnt(0)
	v_mfma_f32_16x16x32_bf16 v[60:63], v[134:137], v[166:169], v[60:63]
	v_mfma_f32_16x16x32_bf16 v[60:63], v[138:141], v[170:173], v[60:63]
	v_mfma_f32_16x16x32_bf16 v[48:51], v[138:141], v[178:181], v[48:51]
	v_mfma_f32_16x16x32_bf16 v[48:51], v[134:137], v[174:177], v[48:51]
	v_mfma_f32_16x16x32_bf16 v[32:35], v[134:137], v[182:185], v[32:35]
	v_mfma_f32_16x16x32_bf16 v[32:35], v[138:141], v[198:201], v[32:35]
	v_mfma_f32_16x16x32_bf16 v[16:19], v[138:141], v[206:209], v[16:19]
	v_mfma_f32_16x16x32_bf16 v[16:19], v[134:137], v[202:205], v[16:19]
	v_mfma_f32_16x16x32_bf16 v[8:11], v[142:145], v[202:205], v[8:11]
	v_mfma_f32_16x16x32_bf16 v[8:11], v[146:149], v[206:209], v[8:11]
	v_mfma_f32_16x16x32_bf16 v[24:27], v[146:149], v[198:201], v[24:27]
	v_mfma_f32_16x16x32_bf16 v[24:27], v[142:145], v[182:185], v[24:27]
	v_mfma_f32_16x16x32_bf16 v[40:43], v[142:145], v[174:177], v[40:43]
	v_mfma_f32_16x16x32_bf16 v[40:43], v[146:149], v[178:181], v[40:43]
	v_mfma_f32_16x16x32_bf16 v[56:59], v[146:149], v[170:173], v[56:59]
	v_mfma_f32_16x16x32_bf16 v[56:59], v[142:145], v[166:169], v[56:59]
	s_setprio 0
	s_setprio 1
	v_mfma_f32_16x16x32_bf16 v[44:47], v[158:161], v[166:169], v[44:47]
	v_mfma_f32_16x16x32_bf16 v[44:47], v[162:165], v[170:173], v[44:47]
	v_mfma_f32_16x16x32_bf16 v[28:31], v[162:165], v[178:181], v[28:31]
	v_mfma_f32_16x16x32_bf16 v[28:31], v[158:161], v[174:177], v[28:31]
	v_mfma_f32_16x16x32_bf16 v[12:15], v[158:161], v[182:185], v[12:15]
	v_mfma_f32_16x16x32_bf16 v[12:15], v[162:165], v[198:201], v[12:15]
	v_mfma_f32_16x16x32_bf16 v[0:3], v[162:165], v[206:209], v[0:3]
	v_mfma_f32_16x16x32_bf16 v[0:3], v[158:161], v[202:205], v[0:3]
	v_mfma_f32_16x16x32_bf16 v[4:7], v[150:153], v[202:205], v[4:7]
	v_mfma_f32_16x16x32_bf16 v[4:7], v[154:157], v[206:209], v[4:7]
	v_mfma_f32_16x16x32_bf16 v[20:23], v[154:157], v[198:201], v[20:23]
	v_mfma_f32_16x16x32_bf16 v[20:23], v[150:153], v[182:185], v[20:23]
	v_mfma_f32_16x16x32_bf16 v[36:39], v[150:153], v[174:177], v[36:39]
	v_mfma_f32_16x16x32_bf16 v[36:39], v[154:157], v[178:181], v[36:39]
	v_mfma_f32_16x16x32_bf16 v[52:55], v[154:157], v[170:173], v[52:55]
	v_mfma_f32_16x16x32_bf16 v[52:55], v[150:153], v[166:169], v[52:55]
	s_setprio 0
	s_barrier
	s_add_u32 s14, s14, 0xc000
	s_mov_b32 m0, s36
	s_addc_u32 s15, s15, 0
	s_add_i32 s54, s54, 2
	global_load_lds_dwordx4 v197, s[14:15]
	s_mov_b32 m0, s37
	s_add_u32 s50, s50, 0x10000
	global_load_lds_dwordx4 v186, s[14:15]
	s_addc_u32 s51, s51, 0
	s_add_u32 s52, s52, 0x10000
	s_addc_u32 s53, s53, 0
	s_cmpk_gt_u32 s54, 0xa9
	s_cbranch_scc0 .LBB0_1422
	s_and_b64 vcc, exec, s[6:7]
	s_cbranch_vccz .LBB0_1425
	s_barrier
